# stores-only GEMM epilogues: next unit's first A stage hoisted above the stores, first three super-phases peeled with vmcnt(24); EpiResid GEMMs keep the 2-wait peel
# speedup vs baseline: 1.0046x; 1.0031x over previous
.LBB0_270:
	s_or_b64 exec, exec, s[48:49]
	s_ashr_i32 s27, s26, 31
	s_lshl_b64 s[48:49], s[26:27], 19
	s_add_u32 s48, s80, s48
	s_addc_u32 s49, s81, s49
	s_and_b64 s[50:51], s[46:47], exec
	s_cselect_b32 s27, s49, s55
	s_cselect_b32 s53, s48, s54
	s_ashr_i32 s31, s30, 31
	s_lshl_b64 s[50:51], s[30:31], 19
	s_add_u32 s50, s1, s50
	s_addc_u32 s51, s0, s51
	s_and_b64 s[58:59], s[46:47], exec
	s_cselect_b32 s31, s51, s57
	s_cselect_b32 s67, s50, s56
	s_add_u32 s54, s54, 0x40080
	s_addc_u32 s55, s55, 0
	s_add_u32 s68, s56, 0x100
	v_mov_b32_e32 v0, 0
	s_addc_u32 s69, s57, 0
	s_mov_b32 s70, -2
	v_mov_b32_e32 v1, v0
	v_mov_b32_e32 v2, v0
	v_mov_b32_e32 v3, v0
	v_mov_b32_e32 v4, v0
	v_mov_b32_e32 v5, v0
	v_mov_b32_e32 v6, v0
	v_mov_b32_e32 v7, v0
	v_mov_b32_e32 v16, v0
	v_mov_b32_e32 v17, v0
	v_mov_b32_e32 v18, v0
	v_mov_b32_e32 v19, v0
	v_mov_b32_e32 v20, v0
	v_mov_b32_e32 v21, v0
	v_mov_b32_e32 v22, v0
	v_mov_b32_e32 v23, v0
	v_mov_b32_e32 v32, v0
	v_mov_b32_e32 v33, v0
	v_mov_b32_e32 v34, v0
	v_mov_b32_e32 v35, v0
	v_mov_b32_e32 v36, v0
	v_mov_b32_e32 v37, v0
	v_mov_b32_e32 v38, v0
	v_mov_b32_e32 v39, v0
	v_mov_b32_e32 v48, v0
	v_mov_b32_e32 v49, v0
	v_mov_b32_e32 v50, v0
	v_mov_b32_e32 v51, v0
	v_mov_b32_e32 v52, v0
	v_mov_b32_e32 v53, v0
	v_mov_b32_e32 v54, v0
	v_mov_b32_e32 v55, v0
	v_mov_b32_e32 v8, v0
	v_mov_b32_e32 v9, v0
	v_mov_b32_e32 v10, v0
	v_mov_b32_e32 v11, v0
	v_mov_b32_e32 v12, v0
	v_mov_b32_e32 v13, v0
	v_mov_b32_e32 v14, v0
	v_mov_b32_e32 v15, v0
	v_mov_b32_e32 v24, v0
	v_mov_b32_e32 v25, v0
	v_mov_b32_e32 v26, v0
	v_mov_b32_e32 v27, v0
	v_mov_b32_e32 v28, v0
	v_mov_b32_e32 v29, v0
	v_mov_b32_e32 v30, v0
	v_mov_b32_e32 v31, v0
	v_mov_b32_e32 v40, v0
	v_mov_b32_e32 v41, v0
	v_mov_b32_e32 v42, v0
	v_mov_b32_e32 v43, v0
	v_mov_b32_e32 v44, v0
	v_mov_b32_e32 v45, v0
	v_mov_b32_e32 v46, v0
	v_mov_b32_e32 v47, v0
	v_mov_b32_e32 v56, v0
	v_mov_b32_e32 v57, v0
	v_mov_b32_e32 v58, v0
	v_mov_b32_e32 v59, v0
	v_mov_b32_e32 v60, v0
	v_mov_b32_e32 v61, v0
	v_mov_b32_e32 v62, v0
	v_mov_b32_e32 v63, v0
	v_mov_b32_e32 v64, v0
	v_mov_b32_e32 v65, v0
	v_mov_b32_e32 v66, v0
	v_mov_b32_e32 v67, v0
	v_mov_b32_e32 v68, v0
	v_mov_b32_e32 v69, v0
	v_mov_b32_e32 v70, v0
	v_mov_b32_e32 v71, v0
	v_mov_b32_e32 v80, v0
	v_mov_b32_e32 v81, v0
	v_mov_b32_e32 v82, v0
	v_mov_b32_e32 v83, v0
	v_mov_b32_e32 v84, v0
	v_mov_b32_e32 v85, v0
	v_mov_b32_e32 v86, v0
	v_mov_b32_e32 v87, v0
	v_mov_b32_e32 v96, v0
	v_mov_b32_e32 v97, v0
	v_mov_b32_e32 v98, v0
	v_mov_b32_e32 v99, v0
	v_mov_b32_e32 v100, v0
	v_mov_b32_e32 v101, v0
	v_mov_b32_e32 v102, v0
	v_mov_b32_e32 v103, v0
	v_mov_b32_e32 v112, v0
	v_mov_b32_e32 v113, v0
	v_mov_b32_e32 v114, v0
	v_mov_b32_e32 v115, v0
	v_mov_b32_e32 v116, v0
	v_mov_b32_e32 v117, v0
	v_mov_b32_e32 v118, v0
	v_mov_b32_e32 v119, v0
	v_mov_b32_e32 v72, v0
	v_mov_b32_e32 v73, v0
	v_mov_b32_e32 v74, v0
	v_mov_b32_e32 v75, v0
	v_mov_b32_e32 v76, v0
	v_mov_b32_e32 v77, v0
	v_mov_b32_e32 v78, v0
	v_mov_b32_e32 v79, v0
	v_mov_b32_e32 v88, v0
	v_mov_b32_e32 v89, v0
	v_mov_b32_e32 v90, v0
	v_mov_b32_e32 v91, v0
	v_mov_b32_e32 v92, v0
	v_mov_b32_e32 v93, v0
	v_mov_b32_e32 v94, v0
	v_mov_b32_e32 v95, v0
	v_mov_b32_e32 v104, v0
	v_mov_b32_e32 v105, v0
	v_mov_b32_e32 v106, v0
	v_mov_b32_e32 v107, v0
	v_mov_b32_e32 v108, v0
	v_mov_b32_e32 v109, v0
	v_mov_b32_e32 v110, v0
	v_mov_b32_e32 v111, v0
	v_mov_b32_e32 v120, v0
	v_mov_b32_e32 v121, v0
	v_mov_b32_e32 v122, v0
	v_mov_b32_e32 v123, v0
	v_mov_b32_e32 v124, v0
	v_mov_b32_e32 v125, v0
	v_mov_b32_e32 v126, v0
	v_mov_b32_e32 v127, v0
	s_cmp_eq_u32 s9, 0
	s_cbranch_scc1 .LBB0_271
	s_add_u32 s56, s54, 0xfffc0080
	s_addc_u32 s57, s55, -1
	s_add_i32 s71, 0, 0x10000
	s_cmp_eq_u32 s70, 12
	s_cselect_b32 s59, s27, s57
	s_cselect_b32 s58, s53, s56
	v_add_u32_e32 v144, s71, v158
	s_cselect_b32 s57, s31, s69
	s_cselect_b32 s56, s67, s68
	s_add_i32 s76, 0, 0x14000
	ds_read_b128 v[164:167], v144
	ds_read_b128 v[168:171], v144 offset:1024
	ds_read_b128 v[172:175], v144 offset:2048
	ds_read_b128 v[176:179], v144 offset:3072
	v_add_u32_e32 v144, s76, v158
	ds_read_b128 v[180:183], v144
	ds_read_b128 v[184:187], v144 offset:1024
	ds_read_b128 v[188:191], v144 offset:2048
	ds_read_b128 v[192:195], v144 offset:3072
	ds_read_b128 v[200:203], v162
	ds_read_b128 v[216:219], v162 offset:1024
	ds_read_b128 v[220:223], v162 offset:2048
	ds_read_b128 v[224:227], v162 offset:3072
	ds_read_b128 v[228:231], v162 offset:4096
	ds_read_b128 v[232:235], v162 offset:5120
	ds_read_b128 v[236:239], v162 offset:6144
	ds_read_b128 v[240:243], v162 offset:7168
	s_waitcnt vmcnt(24)
	s_waitcnt lgkmcnt(0)
	s_barrier
	s_setprio 1
	s_waitcnt lgkmcnt(0)
	v_mfma_f32_16x16x32_bf16 v[124:127], v[164:167], v[200:203], v[124:127]
	v_mfma_f32_16x16x32_bf16 v[120:123], v[172:175], v[200:203], v[120:123]
	v_mfma_f32_16x16x32_bf16 v[108:111], v[164:167], v[220:223], v[108:111]
	v_mfma_f32_16x16x32_bf16 v[104:107], v[172:175], v[220:223], v[104:107]
	v_mfma_f32_16x16x32_bf16 v[92:95], v[164:167], v[228:231], v[92:95]
	v_mfma_f32_16x16x32_bf16 v[88:91], v[172:175], v[228:231], v[88:91]
	v_mfma_f32_16x16x32_bf16 v[76:79], v[164:167], v[236:239], v[76:79]
	v_mfma_f32_16x16x32_bf16 v[72:75], v[172:175], v[236:239], v[72:75]
	v_mfma_f32_16x16x32_bf16 v[124:127], v[168:171], v[216:219], v[124:127]
	v_mfma_f32_16x16x32_bf16 v[120:123], v[176:179], v[216:219], v[120:123]
	v_mfma_f32_16x16x32_bf16 v[108:111], v[168:171], v[224:227], v[108:111]
	v_mfma_f32_16x16x32_bf16 v[104:107], v[176:179], v[224:227], v[104:107]
	v_mfma_f32_16x16x32_bf16 v[92:95], v[168:171], v[232:235], v[92:95]
	v_mfma_f32_16x16x32_bf16 v[88:91], v[176:179], v[232:235], v[88:91]
	v_mfma_f32_16x16x32_bf16 v[76:79], v[168:171], v[240:243], v[76:79]
	v_mfma_f32_16x16x32_bf16 v[72:75], v[176:179], v[240:243], v[72:75]
	s_setprio 0
	s_setprio 1
	v_mfma_f32_16x16x32_bf16 v[116:119], v[180:183], v[200:203], v[116:119]
	v_mfma_f32_16x16x32_bf16 v[112:115], v[188:191], v[200:203], v[112:115]
	v_mfma_f32_16x16x32_bf16 v[100:103], v[180:183], v[220:223], v[100:103]
	v_mfma_f32_16x16x32_bf16 v[96:99], v[188:191], v[220:223], v[96:99]
	v_mfma_f32_16x16x32_bf16 v[84:87], v[180:183], v[228:231], v[84:87]
	v_mfma_f32_16x16x32_bf16 v[80:83], v[188:191], v[228:231], v[80:83]
	v_mfma_f32_16x16x32_bf16 v[68:71], v[180:183], v[236:239], v[68:71]
	v_mfma_f32_16x16x32_bf16 v[64:67], v[188:191], v[236:239], v[64:67]
	v_mfma_f32_16x16x32_bf16 v[116:119], v[184:187], v[216:219], v[116:119]
	v_mfma_f32_16x16x32_bf16 v[112:115], v[192:195], v[216:219], v[112:115]
	v_mfma_f32_16x16x32_bf16 v[100:103], v[184:187], v[224:227], v[100:103]
	v_mfma_f32_16x16x32_bf16 v[96:99], v[192:195], v[224:227], v[96:99]
	v_mfma_f32_16x16x32_bf16 v[84:87], v[184:187], v[232:235], v[84:87]
	v_mfma_f32_16x16x32_bf16 v[80:83], v[192:195], v[232:235], v[80:83]
	v_mfma_f32_16x16x32_bf16 v[68:71], v[184:187], v[240:243], v[68:71]
	v_mfma_f32_16x16x32_bf16 v[64:67], v[192:195], v[240:243], v[64:67]
	s_setprio 0
	s_barrier
	s_add_i32 s71, s71, s33
	v_lshl_add_u64 v[144:145], s[56:57], 0, v[128:129]
	s_mov_b32 m0, s71
	ds_read_b128 v[200:203], v162 offset:16384
	ds_read_b128 v[216:219], v162 offset:17408
	ds_read_b128 v[220:223], v162 offset:18432
	ds_read_b128 v[224:227], v162 offset:19456
	ds_read_b128 v[228:231], v162 offset:20480
	ds_read_b128 v[232:235], v162 offset:21504
	ds_read_b128 v[236:239], v162 offset:22528
	ds_read_b128 v[240:243], v162 offset:23552
	global_load_lds_dwordx4 v[144:145], off
	s_add_i32 m0, s71, 0x2000
	s_add_u32 s72, s56, 0x40000
	v_lshl_add_u64 v[196:197], s[56:57], 0, v[134:135]
	s_addc_u32 s73, s57, 0
	s_add_i32 s71, s76, s33
	global_load_lds_dwordx4 v[196:197], off
	v_lshl_add_u64 v[204:205], s[72:73], 0, v[128:129]
	s_mov_b32 m0, s71
	v_lshl_add_u64 v[206:207], s[58:59], 0, v[132:133]
	global_load_lds_dwordx4 v[204:205], off
	v_lshl_add_u64 v[204:205], s[72:73], 0, v[134:135]
	s_add_i32 m0, s71, 0x2000
	s_nop 0
	global_load_lds_dwordx4 v[204:205], off
	v_lshl_add_u64 v[204:205], s[58:59], 0, v[130:131]
	s_mov_b32 m0, s60
	s_nop 0
	global_load_lds_dwordx4 v[204:205], off
	s_mov_b32 m0, s61
	s_nop 0
	global_load_lds_dwordx4 v[206:207], off
	s_waitcnt vmcnt(24)
	s_waitcnt lgkmcnt(0)
	s_barrier
	s_setprio 1
	s_waitcnt lgkmcnt(0)
	v_mfma_f32_16x16x32_bf16 v[60:63], v[164:167], v[200:203], v[60:63]
	v_mfma_f32_16x16x32_bf16 v[56:59], v[172:175], v[200:203], v[56:59]
	v_mfma_f32_16x16x32_bf16 v[44:47], v[164:167], v[220:223], v[44:47]
	v_mfma_f32_16x16x32_bf16 v[40:43], v[172:175], v[220:223], v[40:43]
	v_mfma_f32_16x16x32_bf16 v[28:31], v[164:167], v[228:231], v[28:31]
	v_mfma_f32_16x16x32_bf16 v[24:27], v[172:175], v[228:231], v[24:27]
	v_mfma_f32_16x16x32_bf16 v[12:15], v[164:167], v[236:239], v[12:15]
	v_mfma_f32_16x16x32_bf16 v[8:11], v[172:175], v[236:239], v[8:11]
	v_mfma_f32_16x16x32_bf16 v[60:63], v[168:171], v[216:219], v[60:63]
	v_mfma_f32_16x16x32_bf16 v[56:59], v[176:179], v[216:219], v[56:59]
	v_mfma_f32_16x16x32_bf16 v[44:47], v[168:171], v[224:227], v[44:47]
	v_mfma_f32_16x16x32_bf16 v[40:43], v[176:179], v[224:227], v[40:43]
	v_mfma_f32_16x16x32_bf16 v[28:31], v[168:171], v[232:235], v[28:31]
	v_mfma_f32_16x16x32_bf16 v[24:27], v[176:179], v[232:235], v[24:27]
	v_mfma_f32_16x16x32_bf16 v[12:15], v[168:171], v[240:243], v[12:15]
	v_mfma_f32_16x16x32_bf16 v[8:11], v[176:179], v[240:243], v[8:11]
	s_setprio 0
	s_setprio 1
	v_mfma_f32_16x16x32_bf16 v[52:55], v[180:183], v[200:203], v[52:55]
	v_mfma_f32_16x16x32_bf16 v[48:51], v[188:191], v[200:203], v[48:51]
	v_mfma_f32_16x16x32_bf16 v[36:39], v[180:183], v[220:223], v[36:39]
	v_mfma_f32_16x16x32_bf16 v[32:35], v[188:191], v[220:223], v[32:35]
	v_mfma_f32_16x16x32_bf16 v[20:23], v[180:183], v[228:231], v[20:23]
	v_mfma_f32_16x16x32_bf16 v[16:19], v[188:191], v[228:231], v[16:19]
	v_mfma_f32_16x16x32_bf16 v[4:7], v[180:183], v[236:239], v[4:7]
	v_mfma_f32_16x16x32_bf16 v[0:3], v[188:191], v[236:239], v[0:3]
	v_mfma_f32_16x16x32_bf16 v[52:55], v[184:187], v[216:219], v[52:55]
	v_mfma_f32_16x16x32_bf16 v[48:51], v[192:195], v[216:219], v[48:51]
	v_mfma_f32_16x16x32_bf16 v[36:39], v[184:187], v[224:227], v[36:39]
	v_mfma_f32_16x16x32_bf16 v[32:35], v[192:195], v[224:227], v[32:35]
	v_mfma_f32_16x16x32_bf16 v[20:23], v[184:187], v[232:235], v[20:23]
	v_mfma_f32_16x16x32_bf16 v[16:19], v[192:195], v[232:235], v[16:19]
	v_mfma_f32_16x16x32_bf16 v[4:7], v[184:187], v[240:243], v[4:7]
	v_mfma_f32_16x16x32_bf16 v[0:3], v[192:195], v[240:243], v[0:3]
	s_setprio 0
	s_barrier
	s_add_i32 s71, 0, 0x18000
	v_add_u32_e32 v163, s71, v158
	s_add_i32 s72, 0, 0x1c000
	ds_read_b128 v[164:167], v163
	ds_read_b128 v[168:171], v163 offset:1024
	ds_read_b128 v[172:175], v163 offset:2048
	ds_read_b128 v[176:179], v163 offset:3072
	v_add_u32_e32 v163, s72, v158
	ds_read_b128 v[180:183], v163
	ds_read_b128 v[184:187], v163 offset:1024
	ds_read_b128 v[188:191], v163 offset:2048
	ds_read_b128 v[192:195], v163 offset:3072
	s_add_u32 s58, s58, 0x40000
	s_addc_u32 s59, s59, 0
	s_mov_b32 m0, s62
	v_lshl_add_u64 v[244:245], s[58:59], 0, v[130:131]
	ds_read_b128 v[200:203], v162 offset:32768
	ds_read_b128 v[216:219], v162 offset:33792
	ds_read_b128 v[220:223], v162 offset:34816
	ds_read_b128 v[224:227], v162 offset:35840
	ds_read_b128 v[228:231], v162 offset:36864
	ds_read_b128 v[232:235], v162 offset:37888
	ds_read_b128 v[236:239], v162 offset:38912
	ds_read_b128 v[240:243], v162 offset:39936
	global_load_lds_dwordx4 v[244:245], off
	v_lshl_add_u64 v[244:245], s[58:59], 0, v[132:133]
	s_mov_b32 m0, s63
	s_nop 0
	global_load_lds_dwordx4 v[244:245], off
	s_waitcnt vmcnt(24)
	s_waitcnt lgkmcnt(0)
	s_barrier
	s_setprio 1
	s_waitcnt lgkmcnt(0)
	v_mfma_f32_16x16x32_bf16 v[124:127], v[164:167], v[200:203], v[124:127]
	v_mfma_f32_16x16x32_bf16 v[120:123], v[172:175], v[200:203], v[120:123]
	v_mfma_f32_16x16x32_bf16 v[108:111], v[164:167], v[220:223], v[108:111]
	v_mfma_f32_16x16x32_bf16 v[104:107], v[172:175], v[220:223], v[104:107]
	v_mfma_f32_16x16x32_bf16 v[92:95], v[164:167], v[228:231], v[92:95]
	v_mfma_f32_16x16x32_bf16 v[88:91], v[172:175], v[228:231], v[88:91]
	v_mfma_f32_16x16x32_bf16 v[76:79], v[164:167], v[236:239], v[76:79]
	v_mfma_f32_16x16x32_bf16 v[72:75], v[172:175], v[236:239], v[72:75]
	v_mfma_f32_16x16x32_bf16 v[124:127], v[168:171], v[216:219], v[124:127]
	v_mfma_f32_16x16x32_bf16 v[120:123], v[176:179], v[216:219], v[120:123]
	v_mfma_f32_16x16x32_bf16 v[108:111], v[168:171], v[224:227], v[108:111]
	v_mfma_f32_16x16x32_bf16 v[104:107], v[176:179], v[224:227], v[104:107]
	v_mfma_f32_16x16x32_bf16 v[92:95], v[168:171], v[232:235], v[92:95]
	v_mfma_f32_16x16x32_bf16 v[88:91], v[176:179], v[232:235], v[88:91]
	v_mfma_f32_16x16x32_bf16 v[76:79], v[168:171], v[240:243], v[76:79]
	v_mfma_f32_16x16x32_bf16 v[72:75], v[176:179], v[240:243], v[72:75]
	s_setprio 0
	s_setprio 1
	v_mfma_f32_16x16x32_bf16 v[116:119], v[180:183], v[200:203], v[116:119]
	v_mfma_f32_16x16x32_bf16 v[112:115], v[188:191], v[200:203], v[112:115]
	v_mfma_f32_16x16x32_bf16 v[100:103], v[180:183], v[220:223], v[100:103]
	v_mfma_f32_16x16x32_bf16 v[96:99], v[188:191], v[220:223], v[96:99]
	v_mfma_f32_16x16x32_bf16 v[84:87], v[180:183], v[228:231], v[84:87]
	v_mfma_f32_16x16x32_bf16 v[80:83], v[188:191], v[228:231], v[80:83]
	v_mfma_f32_16x16x32_bf16 v[68:71], v[180:183], v[236:239], v[68:71]
	v_mfma_f32_16x16x32_bf16 v[64:67], v[188:191], v[236:239], v[64:67]
	v_mfma_f32_16x16x32_bf16 v[116:119], v[184:187], v[216:219], v[116:119]
	v_mfma_f32_16x16x32_bf16 v[112:115], v[192:195], v[216:219], v[112:115]
	v_mfma_f32_16x16x32_bf16 v[100:103], v[184:187], v[224:227], v[100:103]
	v_mfma_f32_16x16x32_bf16 v[96:99], v[192:195], v[224:227], v[96:99]
	v_mfma_f32_16x16x32_bf16 v[84:87], v[184:187], v[232:235], v[84:87]
	v_mfma_f32_16x16x32_bf16 v[80:83], v[192:195], v[232:235], v[80:83]
	v_mfma_f32_16x16x32_bf16 v[68:71], v[184:187], v[240:243], v[68:71]
	v_mfma_f32_16x16x32_bf16 v[64:67], v[192:195], v[240:243], v[64:67]
	s_setprio 0
	s_barrier
	s_branch .Lp1e_q3
.LBB0_271:
	s_add_u32 s56, s54, 0xfffc0080
	s_addc_u32 s57, s55, -1
	s_add_i32 s71, 0, 0x10000
	s_cmp_eq_u32 s70, 12
	s_cselect_b32 s59, s27, s57
	s_cselect_b32 s58, s53, s56
	v_add_u32_e32 v144, s71, v158
	s_cselect_b32 s57, s31, s69
	s_cselect_b32 s56, s67, s68
	s_add_i32 s76, 0, 0x14000
	ds_read_b128 v[164:167], v144
	ds_read_b128 v[168:171], v144 offset:1024
	ds_read_b128 v[172:175], v144 offset:2048
	ds_read_b128 v[176:179], v144 offset:3072
	v_add_u32_e32 v144, s76, v158
	ds_read_b128 v[180:183], v144
	ds_read_b128 v[184:187], v144 offset:1024
	ds_read_b128 v[188:191], v144 offset:2048
	ds_read_b128 v[192:195], v144 offset:3072
	v_lshl_add_u64 v[144:145], s[54:55], 0, v[140:141]
	s_add_i32 m0, s60, 0xc000
	ds_read_b128 v[200:203], v162
	ds_read_b128 v[216:219], v162 offset:1024
	ds_read_b128 v[220:223], v162 offset:2048
	ds_read_b128 v[224:227], v162 offset:3072
	ds_read_b128 v[228:231], v162 offset:4096
	ds_read_b128 v[232:235], v162 offset:5120
	ds_read_b128 v[236:239], v162 offset:6144
	ds_read_b128 v[240:243], v162 offset:7168
	global_load_lds_dwordx4 v[144:145], off
	v_lshl_add_u64 v[144:145], s[54:55], 0, v[142:143]
	s_add_i32 m0, s60, 0xe000
	s_nop 0
	global_load_lds_dwordx4 v[144:145], off
	s_waitcnt vmcnt(8)
	s_waitcnt lgkmcnt(0)
	s_barrier
	s_setprio 1
	s_waitcnt lgkmcnt(0)
	v_mfma_f32_16x16x32_bf16 v[124:127], v[164:167], v[200:203], v[124:127]
	v_mfma_f32_16x16x32_bf16 v[120:123], v[172:175], v[200:203], v[120:123]
	v_mfma_f32_16x16x32_bf16 v[108:111], v[164:167], v[220:223], v[108:111]
	v_mfma_f32_16x16x32_bf16 v[104:107], v[172:175], v[220:223], v[104:107]
	v_mfma_f32_16x16x32_bf16 v[92:95], v[164:167], v[228:231], v[92:95]
	v_mfma_f32_16x16x32_bf16 v[88:91], v[172:175], v[228:231], v[88:91]
	v_mfma_f32_16x16x32_bf16 v[76:79], v[164:167], v[236:239], v[76:79]
	v_mfma_f32_16x16x32_bf16 v[72:75], v[172:175], v[236:239], v[72:75]
	v_mfma_f32_16x16x32_bf16 v[124:127], v[168:171], v[216:219], v[124:127]
	v_mfma_f32_16x16x32_bf16 v[120:123], v[176:179], v[216:219], v[120:123]
	v_mfma_f32_16x16x32_bf16 v[108:111], v[168:171], v[224:227], v[108:111]
	v_mfma_f32_16x16x32_bf16 v[104:107], v[176:179], v[224:227], v[104:107]
	v_mfma_f32_16x16x32_bf16 v[92:95], v[168:171], v[232:235], v[92:95]
	v_mfma_f32_16x16x32_bf16 v[88:91], v[176:179], v[232:235], v[88:91]
	v_mfma_f32_16x16x32_bf16 v[76:79], v[168:171], v[240:243], v[76:79]
	v_mfma_f32_16x16x32_bf16 v[72:75], v[176:179], v[240:243], v[72:75]
	s_setprio 0
	s_setprio 1
	v_mfma_f32_16x16x32_bf16 v[116:119], v[180:183], v[200:203], v[116:119]
	v_mfma_f32_16x16x32_bf16 v[112:115], v[188:191], v[200:203], v[112:115]
	v_mfma_f32_16x16x32_bf16 v[100:103], v[180:183], v[220:223], v[100:103]
	v_mfma_f32_16x16x32_bf16 v[96:99], v[188:191], v[220:223], v[96:99]
	v_mfma_f32_16x16x32_bf16 v[84:87], v[180:183], v[228:231], v[84:87]
	v_mfma_f32_16x16x32_bf16 v[80:83], v[188:191], v[228:231], v[80:83]
	v_mfma_f32_16x16x32_bf16 v[68:71], v[180:183], v[236:239], v[68:71]
	v_mfma_f32_16x16x32_bf16 v[64:67], v[188:191], v[236:239], v[64:67]
	v_mfma_f32_16x16x32_bf16 v[116:119], v[184:187], v[216:219], v[116:119]
	v_mfma_f32_16x16x32_bf16 v[112:115], v[192:195], v[216:219], v[112:115]
	v_mfma_f32_16x16x32_bf16 v[100:103], v[184:187], v[224:227], v[100:103]
	v_mfma_f32_16x16x32_bf16 v[96:99], v[192:195], v[224:227], v[96:99]
	v_mfma_f32_16x16x32_bf16 v[84:87], v[184:187], v[232:235], v[84:87]
	v_mfma_f32_16x16x32_bf16 v[80:83], v[192:195], v[232:235], v[80:83]
	v_mfma_f32_16x16x32_bf16 v[68:71], v[184:187], v[240:243], v[68:71]
	v_mfma_f32_16x16x32_bf16 v[64:67], v[192:195], v[240:243], v[64:67]
	s_setprio 0
	s_barrier
	s_add_i32 s71, s71, s33
	v_lshl_add_u64 v[144:145], s[56:57], 0, v[128:129]
	s_mov_b32 m0, s71
	ds_read_b128 v[200:203], v162 offset:16384
	ds_read_b128 v[216:219], v162 offset:17408
	ds_read_b128 v[220:223], v162 offset:18432
	ds_read_b128 v[224:227], v162 offset:19456
	ds_read_b128 v[228:231], v162 offset:20480
	ds_read_b128 v[232:235], v162 offset:21504
	ds_read_b128 v[236:239], v162 offset:22528
	ds_read_b128 v[240:243], v162 offset:23552
	global_load_lds_dwordx4 v[144:145], off
	s_add_i32 m0, s71, 0x2000
	s_add_u32 s72, s56, 0x40000
	v_lshl_add_u64 v[196:197], s[56:57], 0, v[134:135]
	s_addc_u32 s73, s57, 0
	s_add_i32 s71, s76, s33
	global_load_lds_dwordx4 v[196:197], off
	v_lshl_add_u64 v[204:205], s[72:73], 0, v[128:129]
	s_mov_b32 m0, s71
	v_lshl_add_u64 v[206:207], s[58:59], 0, v[132:133]
	global_load_lds_dwordx4 v[204:205], off
	v_lshl_add_u64 v[204:205], s[72:73], 0, v[134:135]
	s_add_i32 m0, s71, 0x2000
	s_nop 0
	global_load_lds_dwordx4 v[204:205], off
	v_lshl_add_u64 v[204:205], s[58:59], 0, v[130:131]
	s_mov_b32 m0, s60
	s_nop 0
	global_load_lds_dwordx4 v[204:205], off
	s_mov_b32 m0, s61
	s_nop 0
	global_load_lds_dwordx4 v[206:207], off
	s_waitcnt vmcnt(8)
	s_waitcnt lgkmcnt(0)
	s_barrier
	s_setprio 1
	s_waitcnt lgkmcnt(0)
	v_mfma_f32_16x16x32_bf16 v[60:63], v[164:167], v[200:203], v[60:63]
	v_mfma_f32_16x16x32_bf16 v[56:59], v[172:175], v[200:203], v[56:59]
	v_mfma_f32_16x16x32_bf16 v[44:47], v[164:167], v[220:223], v[44:47]
	v_mfma_f32_16x16x32_bf16 v[40:43], v[172:175], v[220:223], v[40:43]
	v_mfma_f32_16x16x32_bf16 v[28:31], v[164:167], v[228:231], v[28:31]
	v_mfma_f32_16x16x32_bf16 v[24:27], v[172:175], v[228:231], v[24:27]
	v_mfma_f32_16x16x32_bf16 v[12:15], v[164:167], v[236:239], v[12:15]
	v_mfma_f32_16x16x32_bf16 v[8:11], v[172:175], v[236:239], v[8:11]
	v_mfma_f32_16x16x32_bf16 v[60:63], v[168:171], v[216:219], v[60:63]
	v_mfma_f32_16x16x32_bf16 v[56:59], v[176:179], v[216:219], v[56:59]
	v_mfma_f32_16x16x32_bf16 v[44:47], v[168:171], v[224:227], v[44:47]
	v_mfma_f32_16x16x32_bf16 v[40:43], v[176:179], v[224:227], v[40:43]
	v_mfma_f32_16x16x32_bf16 v[28:31], v[168:171], v[232:235], v[28:31]
	v_mfma_f32_16x16x32_bf16 v[24:27], v[176:179], v[232:235], v[24:27]
	v_mfma_f32_16x16x32_bf16 v[12:15], v[168:171], v[240:243], v[12:15]
	v_mfma_f32_16x16x32_bf16 v[8:11], v[176:179], v[240:243], v[8:11]
	s_setprio 0
	s_setprio 1
	v_mfma_f32_16x16x32_bf16 v[52:55], v[180:183], v[200:203], v[52:55]
	v_mfma_f32_16x16x32_bf16 v[48:51], v[188:191], v[200:203], v[48:51]
	v_mfma_f32_16x16x32_bf16 v[36:39], v[180:183], v[220:223], v[36:39]
	v_mfma_f32_16x16x32_bf16 v[32:35], v[188:191], v[220:223], v[32:35]
	v_mfma_f32_16x16x32_bf16 v[20:23], v[180:183], v[228:231], v[20:23]
	v_mfma_f32_16x16x32_bf16 v[16:19], v[188:191], v[228:231], v[16:19]
	v_mfma_f32_16x16x32_bf16 v[4:7], v[180:183], v[236:239], v[4:7]
	v_mfma_f32_16x16x32_bf16 v[0:3], v[188:191], v[236:239], v[0:3]
	v_mfma_f32_16x16x32_bf16 v[52:55], v[184:187], v[216:219], v[52:55]
	v_mfma_f32_16x16x32_bf16 v[48:51], v[192:195], v[216:219], v[48:51]
	v_mfma_f32_16x16x32_bf16 v[36:39], v[184:187], v[224:227], v[36:39]
	v_mfma_f32_16x16x32_bf16 v[32:35], v[192:195], v[224:227], v[32:35]
	v_mfma_f32_16x16x32_bf16 v[20:23], v[184:187], v[232:235], v[20:23]
	v_mfma_f32_16x16x32_bf16 v[16:19], v[192:195], v[232:235], v[16:19]
	v_mfma_f32_16x16x32_bf16 v[4:7], v[184:187], v[240:243], v[4:7]
	v_mfma_f32_16x16x32_bf16 v[0:3], v[192:195], v[240:243], v[0:3]
	s_setprio 0
	s_barrier
	s_add_i32 s71, 0, 0x18000
	v_add_u32_e32 v163, s71, v158
	s_add_i32 s72, 0, 0x1c000
	ds_read_b128 v[164:167], v163
	ds_read_b128 v[168:171], v163 offset:1024
	ds_read_b128 v[172:175], v163 offset:2048
	ds_read_b128 v[176:179], v163 offset:3072
	v_add_u32_e32 v163, s72, v158
	ds_read_b128 v[180:183], v163
	ds_read_b128 v[184:187], v163 offset:1024
	ds_read_b128 v[188:191], v163 offset:2048
	ds_read_b128 v[192:195], v163 offset:3072
	s_add_u32 s58, s58, 0x40000
	s_addc_u32 s59, s59, 0
	s_mov_b32 m0, s62
	v_lshl_add_u64 v[244:245], s[58:59], 0, v[130:131]
	ds_read_b128 v[200:203], v162 offset:32768
	ds_read_b128 v[216:219], v162 offset:33792
	ds_read_b128 v[220:223], v162 offset:34816
	ds_read_b128 v[224:227], v162 offset:35840
	ds_read_b128 v[228:231], v162 offset:36864
	ds_read_b128 v[232:235], v162 offset:37888
	ds_read_b128 v[236:239], v162 offset:38912
	ds_read_b128 v[240:243], v162 offset:39936
	global_load_lds_dwordx4 v[244:245], off
	v_lshl_add_u64 v[244:245], s[58:59], 0, v[132:133]
	s_mov_b32 m0, s63
	s_nop 0
	global_load_lds_dwordx4 v[244:245], off
	s_waitcnt vmcnt(8)
	s_waitcnt lgkmcnt(0)
	s_barrier
	s_setprio 1
	s_waitcnt lgkmcnt(0)
	v_mfma_f32_16x16x32_bf16 v[124:127], v[164:167], v[200:203], v[124:127]
	v_mfma_f32_16x16x32_bf16 v[120:123], v[172:175], v[200:203], v[120:123]
	v_mfma_f32_16x16x32_bf16 v[108:111], v[164:167], v[220:223], v[108:111]
	v_mfma_f32_16x16x32_bf16 v[104:107], v[172:175], v[220:223], v[104:107]
	v_mfma_f32_16x16x32_bf16 v[92:95], v[164:167], v[228:231], v[92:95]
	v_mfma_f32_16x16x32_bf16 v[88:91], v[172:175], v[228:231], v[88:91]
	v_mfma_f32_16x16x32_bf16 v[76:79], v[164:167], v[236:239], v[76:79]
	v_mfma_f32_16x16x32_bf16 v[72:75], v[172:175], v[236:239], v[72:75]
	v_mfma_f32_16x16x32_bf16 v[124:127], v[168:171], v[216:219], v[124:127]
	v_mfma_f32_16x16x32_bf16 v[120:123], v[176:179], v[216:219], v[120:123]
	v_mfma_f32_16x16x32_bf16 v[108:111], v[168:171], v[224:227], v[108:111]
	v_mfma_f32_16x16x32_bf16 v[104:107], v[176:179], v[224:227], v[104:107]
	v_mfma_f32_16x16x32_bf16 v[92:95], v[168:171], v[232:235], v[92:95]
	v_mfma_f32_16x16x32_bf16 v[88:91], v[176:179], v[232:235], v[88:91]
	v_mfma_f32_16x16x32_bf16 v[76:79], v[168:171], v[240:243], v[76:79]
	v_mfma_f32_16x16x32_bf16 v[72:75], v[176:179], v[240:243], v[72:75]
	s_setprio 0
	s_setprio 1
	v_mfma_f32_16x16x32_bf16 v[116:119], v[180:183], v[200:203], v[116:119]
	v_mfma_f32_16x16x32_bf16 v[112:115], v[188:191], v[200:203], v[112:115]
	v_mfma_f32_16x16x32_bf16 v[100:103], v[180:183], v[220:223], v[100:103]
	v_mfma_f32_16x16x32_bf16 v[96:99], v[188:191], v[220:223], v[96:99]
	v_mfma_f32_16x16x32_bf16 v[84:87], v[180:183], v[228:231], v[84:87]
	v_mfma_f32_16x16x32_bf16 v[80:83], v[188:191], v[228:231], v[80:83]
	v_mfma_f32_16x16x32_bf16 v[68:71], v[180:183], v[236:239], v[68:71]
	v_mfma_f32_16x16x32_bf16 v[64:67], v[188:191], v[236:239], v[64:67]
	v_mfma_f32_16x16x32_bf16 v[116:119], v[184:187], v[216:219], v[116:119]
	v_mfma_f32_16x16x32_bf16 v[112:115], v[192:195], v[216:219], v[112:115]
	v_mfma_f32_16x16x32_bf16 v[100:103], v[184:187], v[224:227], v[100:103]
	v_mfma_f32_16x16x32_bf16 v[96:99], v[192:195], v[224:227], v[96:99]
	v_mfma_f32_16x16x32_bf16 v[84:87], v[184:187], v[232:235], v[84:87]
	v_mfma_f32_16x16x32_bf16 v[80:83], v[192:195], v[232:235], v[80:83]
	v_mfma_f32_16x16x32_bf16 v[68:71], v[184:187], v[240:243], v[68:71]
	v_mfma_f32_16x16x32_bf16 v[64:67], v[192:195], v[240:243], v[64:67]
	s_setprio 0
	s_barrier
.Lp1e_q3:
	s_add_i32 s58, s71, s33
	v_lshl_add_u64 v[144:145], v[144:145], 0, s[88:89]
	s_mov_b32 m0, s58
	ds_read_b128 v[200:203], v162 offset:49152
	ds_read_b128 v[216:219], v162 offset:50176
	ds_read_b128 v[220:223], v162 offset:51200
	ds_read_b128 v[224:227], v162 offset:52224
	ds_read_b128 v[228:231], v162 offset:53248
	ds_read_b128 v[232:235], v162 offset:54272
	ds_read_b128 v[236:239], v162 offset:55296
	ds_read_b128 v[240:243], v162 offset:56320
	global_load_lds_dwordx4 v[144:145], off
	s_add_i32 m0, s58, 0x2000
	s_add_u32 s56, s56, 0x40080
	v_lshl_add_u64 v[144:145], v[196:197], 0, s[88:89]
	s_addc_u32 s57, s57, 0
	s_add_i32 s58, s72, s33
	global_load_lds_dwordx4 v[144:145], off
	v_lshl_add_u64 v[144:145], s[56:57], 0, v[128:129]
	s_mov_b32 m0, s58
	s_nop 0
	global_load_lds_dwordx4 v[144:145], off
	v_lshl_add_u64 v[144:145], s[56:57], 0, v[134:135]
	s_add_i32 m0, s58, 0x2000
	s_nop 0
	global_load_lds_dwordx4 v[144:145], off
	v_lshl_add_u64 v[144:145], v[204:205], 0, s[88:89]
	s_mov_b32 m0, s64
	s_nop 0
	global_load_lds_dwordx4 v[144:145], off
	v_lshl_add_u64 v[144:145], v[206:207], 0, s[88:89]
	s_mov_b32 m0, s65
	s_nop 0
	global_load_lds_dwordx4 v[144:145], off
	s_waitcnt vmcnt(8)
	s_waitcnt lgkmcnt(0)
	s_barrier
	s_setprio 1
	s_waitcnt lgkmcnt(0)
	v_mfma_f32_16x16x32_bf16 v[60:63], v[164:167], v[200:203], v[60:63]
	v_mfma_f32_16x16x32_bf16 v[56:59], v[172:175], v[200:203], v[56:59]
	v_mfma_f32_16x16x32_bf16 v[44:47], v[164:167], v[220:223], v[44:47]
	v_mfma_f32_16x16x32_bf16 v[40:43], v[172:175], v[220:223], v[40:43]
	v_mfma_f32_16x16x32_bf16 v[28:31], v[164:167], v[228:231], v[28:31]
	v_mfma_f32_16x16x32_bf16 v[24:27], v[172:175], v[228:231], v[24:27]
	v_mfma_f32_16x16x32_bf16 v[12:15], v[164:167], v[236:239], v[12:15]
	v_mfma_f32_16x16x32_bf16 v[8:11], v[172:175], v[236:239], v[8:11]
	v_mfma_f32_16x16x32_bf16 v[60:63], v[168:171], v[216:219], v[60:63]
	v_mfma_f32_16x16x32_bf16 v[56:59], v[176:179], v[216:219], v[56:59]
	v_mfma_f32_16x16x32_bf16 v[44:47], v[168:171], v[224:227], v[44:47]
	v_mfma_f32_16x16x32_bf16 v[40:43], v[176:179], v[224:227], v[40:43]
	v_mfma_f32_16x16x32_bf16 v[28:31], v[168:171], v[232:235], v[28:31]
	v_mfma_f32_16x16x32_bf16 v[24:27], v[176:179], v[232:235], v[24:27]
	v_mfma_f32_16x16x32_bf16 v[12:15], v[168:171], v[240:243], v[12:15]
	v_mfma_f32_16x16x32_bf16 v[8:11], v[176:179], v[240:243], v[8:11]
	s_setprio 0
	s_setprio 1
	v_mfma_f32_16x16x32_bf16 v[52:55], v[180:183], v[200:203], v[52:55]
	v_mfma_f32_16x16x32_bf16 v[48:51], v[188:191], v[200:203], v[48:51]
	v_mfma_f32_16x16x32_bf16 v[36:39], v[180:183], v[220:223], v[36:39]
	v_mfma_f32_16x16x32_bf16 v[32:35], v[188:191], v[220:223], v[32:35]
	v_mfma_f32_16x16x32_bf16 v[20:23], v[180:183], v[228:231], v[20:23]
	v_mfma_f32_16x16x32_bf16 v[16:19], v[188:191], v[228:231], v[16:19]
	v_mfma_f32_16x16x32_bf16 v[4:7], v[180:183], v[236:239], v[4:7]
	v_mfma_f32_16x16x32_bf16 v[0:3], v[188:191], v[236:239], v[0:3]
	v_mfma_f32_16x16x32_bf16 v[52:55], v[184:187], v[216:219], v[52:55]
	v_mfma_f32_16x16x32_bf16 v[48:51], v[192:195], v[216:219], v[48:51]
	v_mfma_f32_16x16x32_bf16 v[36:39], v[184:187], v[224:227], v[36:39]
	v_mfma_f32_16x16x32_bf16 v[32:35], v[192:195], v[224:227], v[32:35]
	v_mfma_f32_16x16x32_bf16 v[20:23], v[184:187], v[232:235], v[20:23]
	v_mfma_f32_16x16x32_bf16 v[16:19], v[192:195], v[232:235], v[16:19]
	v_mfma_f32_16x16x32_bf16 v[4:7], v[184:187], v[240:243], v[4:7]
	v_mfma_f32_16x16x32_bf16 v[0:3], v[192:195], v[240:243], v[0:3]
	s_setprio 0
	s_barrier
	s_add_i32 s70, s70, 2
	s_add_u32 s54, s54, 0x100
	s_addc_u32 s55, s55, 0
	s_add_u32 s68, s68, 0x100
	s_addc_u32 s69, s69, 0
	s_cmp_gt_u32 s70, 13
	s_cbranch_scc0 .LBB0_271
	s_and_b64 vcc, exec, s[22:23]
	s_cbranch_vccz .LBB0_274
	s_barrier
.LBB0_274:
	s_add_u32 s100, s53, 0x40080
	s_addc_u32 s101, s27, 0
	v_lshl_add_u64 v[144:145], s[100:101], 0, v[140:141]
	s_add_i32 m0, s60, 0xc000
	s_nop 0
	global_load_lds_dwordx4 v[144:145], off
	v_lshl_add_u64 v[144:145], s[100:101], 0, v[142:143]
	s_add_i32 m0, s60, 0xe000
	s_nop 0
	global_load_lds_dwordx4 v[144:145], off
	s_cmp_lt_i32 s8, 4
	v_lshl_or_b32 v144, s8, 8, v161
	s_cselect_b64 vcc, -1, 0
	s_lshl_b32 s8, s9, 12
	s_and_b32 s8, s8, 0x1000
	v_add_u32_e32 v165, s8, v160
	ds_read_b128 v[166:169], v165
	v_mov_b32_e32 v145, 0x3e38aa3b
	v_cndmask_b32_e32 v163, 1.0, v145, vcc
	v_ashrrev_i32_e32 v145, 31, v144
	v_lshl_add_u32 v164, s52, 8, v157
	s_waitcnt lgkmcnt(0)
	v_mov_b32_e32 v172, v167
	v_mov_b32_e32 v173, v168
	v_mov_b32_e32 v167, v169
	v_pk_add_f32 v[166:167], v[172:173], v[166:167]
	v_lshl_add_u64 v[144:145], v[144:145], 1, s[74:75]
	v_add_f32_e32 v166, v166, v167
	v_fmamk_f32 v166, v166, 0x3a800000, v198
	v_cmp_gt_f32_e32 vcc, s19, v166
	v_mul_f32_e32 v167, 0x4b800000, v166
	s_movk_i32 s27, 0x1800
	v_cndmask_b32_e32 v166, v166, v167, vcc
	v_rsq_f32_e32 v166, v166
	v_mad_i64_i32 v[170:171], s[52:53], v164, s27, v[144:145]
	s_mov_b64 s[52:53], -1
	v_mul_f32_e32 v167, 0x45800000, v166
	v_cndmask_b32_e32 v166, v166, v167, vcc
	v_mul_f32_e32 v166, v163, v166
	v_pk_mul_f32 v[126:127], v[126:127], v[166:167] op_sel_hi:[1,0]
	v_pk_mul_f32 v[124:125], v[124:125], v[166:167] op_sel_hi:[1,0]
	v_pk_mul_f32 v[168:169], v[122:123], v[166:167] op_sel_hi:[1,0]
	v_pk_mul_f32 v[122:123], v[120:121], v[166:167] op_sel_hi:[1,0]
	v_cvt_pk_bf16_f32 v120, v124, v125
	v_cvt_pk_bf16_f32 v121, v126, v127
	v_pk_mul_f32 v[116:117], v[116:117], v[166:167] op_sel_hi:[1,0]
	v_cvt_pk_bf16_f32 v122, v122, v123
	v_cvt_pk_bf16_f32 v123, v168, v169
	global_store_dwordx4 v[170:171], v[120:123], off
	v_pk_mul_f32 v[118:119], v[118:119], v[166:167] op_sel_hi:[1,0]
	s_mov_b64 s[72:73], s[24:25]
	v_pk_mul_f32 v[120:121], v[114:115], v[166:167] op_sel_hi:[1,0]
	v_pk_mul_f32 v[114:115], v[112:113], v[166:167] op_sel_hi:[1,0]
	v_cvt_pk_bf16_f32 v112, v116, v117
	v_cvt_pk_bf16_f32 v113, v118, v119
	s_nop 0
	v_cvt_pk_bf16_f32 v114, v114, v115
	v_cvt_pk_bf16_f32 v115, v120, v121
	global_store_dwordx4 v[170:171], v[112:115], off offset:256
	s_nop 1
	v_or_b32_e32 v112, 16, v164
	v_mad_i64_i32 v[116:117], s[8:9], v112, s27, v[144:145]
	ds_read_b128 v[112:115], v165 offset:256
	s_waitcnt lgkmcnt(0)
	v_mov_b32_e32 v118, v113
	v_mov_b32_e32 v119, v114
	v_mov_b32_e32 v113, v115
	v_pk_add_f32 v[112:113], v[118:119], v[112:113]
	s_nop 0
	v_add_f32_e32 v112, v112, v113
	v_fmamk_f32 v112, v112, 0x3a800000, v198
	v_cmp_gt_f32_e32 vcc, s19, v112
	v_mul_f32_e32 v113, 0x4b800000, v112
	s_nop 0
	v_cndmask_b32_e32 v112, v112, v113, vcc
	v_rsq_f32_e32 v112, v112
	s_nop 0
	v_mul_f32_e32 v113, 0x45800000, v112
	v_cndmask_b32_e32 v112, v112, v113, vcc
	v_mul_f32_e32 v112, v163, v112
	v_pk_mul_f32 v[110:111], v[110:111], v[112:113] op_sel_hi:[1,0]
	v_pk_mul_f32 v[108:109], v[108:109], v[112:113] op_sel_hi:[1,0]
	v_pk_mul_f32 v[114:115], v[106:107], v[112:113] op_sel_hi:[1,0]
	v_pk_mul_f32 v[106:107], v[104:105], v[112:113] op_sel_hi:[1,0]
	v_cvt_pk_bf16_f32 v104, v108, v109
	v_cvt_pk_bf16_f32 v105, v110, v111
	v_pk_mul_f32 v[100:101], v[100:101], v[112:113] op_sel_hi:[1,0]
	v_cvt_pk_bf16_f32 v106, v106, v107
	v_cvt_pk_bf16_f32 v107, v114, v115
	global_store_dwordx4 v[116:117], v[104:107], off
	v_pk_mul_f32 v[102:103], v[102:103], v[112:113] op_sel_hi:[1,0]
	s_nop 0
	v_pk_mul_f32 v[104:105], v[98:99], v[112:113] op_sel_hi:[1,0]
	v_pk_mul_f32 v[98:99], v[96:97], v[112:113] op_sel_hi:[1,0]
	v_cvt_pk_bf16_f32 v96, v100, v101
	v_cvt_pk_bf16_f32 v97, v102, v103
	s_nop 0
	v_cvt_pk_bf16_f32 v98, v98, v99
	v_cvt_pk_bf16_f32 v99, v104, v105
	global_store_dwordx4 v[116:117], v[96:99], off offset:256
	s_nop 1
	v_or_b32_e32 v96, 32, v164
	v_mad_i64_i32 v[100:101], s[8:9], v96, s27, v[144:145]
	ds_read_b128 v[96:99], v165 offset:512
	s_waitcnt lgkmcnt(0)
	v_mov_b32_e32 v102, v97
	v_mov_b32_e32 v103, v98
	v_mov_b32_e32 v97, v99
	v_pk_add_f32 v[96:97], v[102:103], v[96:97]
	s_nop 0
	v_add_f32_e32 v96, v96, v97
	v_fmamk_f32 v96, v96, 0x3a800000, v198
	v_cmp_gt_f32_e32 vcc, s19, v96
	v_mul_f32_e32 v97, 0x4b800000, v96
	s_nop 0
	v_cndmask_b32_e32 v96, v96, v97, vcc
	v_rsq_f32_e32 v96, v96
	s_nop 0
	v_mul_f32_e32 v97, 0x45800000, v96
	v_cndmask_b32_e32 v96, v96, v97, vcc
	v_mul_f32_e32 v96, v163, v96
	v_pk_mul_f32 v[94:95], v[94:95], v[96:97] op_sel_hi:[1,0]
	v_pk_mul_f32 v[92:93], v[92:93], v[96:97] op_sel_hi:[1,0]
	v_pk_mul_f32 v[98:99], v[90:91], v[96:97] op_sel_hi:[1,0]
	v_pk_mul_f32 v[90:91], v[88:89], v[96:97] op_sel_hi:[1,0]
	v_cvt_pk_bf16_f32 v88, v92, v93
	v_cvt_pk_bf16_f32 v89, v94, v95
	v_pk_mul_f32 v[84:85], v[84:85], v[96:97] op_sel_hi:[1,0]
	v_cvt_pk_bf16_f32 v90, v90, v91
	v_cvt_pk_bf16_f32 v91, v98, v99
	global_store_dwordx4 v[100:101], v[88:91], off
	v_pk_mul_f32 v[86:87], v[86:87], v[96:97] op_sel_hi:[1,0]
	s_nop 0
	v_pk_mul_f32 v[88:89], v[82:83], v[96:97] op_sel_hi:[1,0]
	v_pk_mul_f32 v[82:83], v[80:81], v[96:97] op_sel_hi:[1,0]
	v_cvt_pk_bf16_f32 v80, v84, v85
	v_cvt_pk_bf16_f32 v81, v86, v87
	s_nop 0
	v_cvt_pk_bf16_f32 v82, v82, v83
	v_cvt_pk_bf16_f32 v83, v88, v89
	global_store_dwordx4 v[100:101], v[80:83], off offset:256
	s_nop 1
	v_or_b32_e32 v80, 48, v164
	v_mad_i64_i32 v[84:85], s[8:9], v80, s27, v[144:145]
	ds_read_b128 v[80:83], v165 offset:768
	s_waitcnt lgkmcnt(0)
	v_mov_b32_e32 v86, v81
	v_mov_b32_e32 v87, v82
	v_mov_b32_e32 v81, v83
	v_pk_add_f32 v[80:81], v[86:87], v[80:81]
	s_nop 0
	v_add_f32_e32 v80, v80, v81
	v_fmamk_f32 v80, v80, 0x3a800000, v198
	v_cmp_gt_f32_e32 vcc, s19, v80
	v_mul_f32_e32 v81, 0x4b800000, v80
	s_nop 0
	v_cndmask_b32_e32 v80, v80, v81, vcc
	v_rsq_f32_e32 v80, v80
	s_nop 0
	v_mul_f32_e32 v81, 0x45800000, v80
	v_cndmask_b32_e32 v80, v80, v81, vcc
	v_mul_f32_e32 v80, v163, v80
	v_pk_mul_f32 v[78:79], v[78:79], v[80:81] op_sel_hi:[1,0]
	v_pk_mul_f32 v[76:77], v[76:77], v[80:81] op_sel_hi:[1,0]
	v_pk_mul_f32 v[82:83], v[74:75], v[80:81] op_sel_hi:[1,0]
	v_pk_mul_f32 v[74:75], v[72:73], v[80:81] op_sel_hi:[1,0]
	v_cvt_pk_bf16_f32 v72, v76, v77
	v_cvt_pk_bf16_f32 v73, v78, v79
	v_pk_mul_f32 v[68:69], v[68:69], v[80:81] op_sel_hi:[1,0]
	v_cvt_pk_bf16_f32 v74, v74, v75
	v_cvt_pk_bf16_f32 v75, v82, v83
	global_store_dwordx4 v[84:85], v[72:75], off
	v_pk_mul_f32 v[70:71], v[70:71], v[80:81] op_sel_hi:[1,0]
	s_nop 0
	v_pk_mul_f32 v[72:73], v[66:67], v[80:81] op_sel_hi:[1,0]
	v_pk_mul_f32 v[66:67], v[64:65], v[80:81] op_sel_hi:[1,0]
	v_cvt_pk_bf16_f32 v64, v68, v69
	v_cvt_pk_bf16_f32 v65, v70, v71
	s_nop 0
	v_cvt_pk_bf16_f32 v66, v66, v67
	v_cvt_pk_bf16_f32 v67, v72, v73
	global_store_dwordx4 v[84:85], v[64:67], off offset:256
	s_nop 1
	v_add_u32_e32 v64, 0x80, v164
	v_mad_i64_i32 v[68:69], s[8:9], v64, s27, v[144:145]
	ds_read_b128 v[64:67], v165 offset:2048
	s_waitcnt lgkmcnt(0)
	v_mov_b32_e32 v70, v65
	v_mov_b32_e32 v71, v66
	v_mov_b32_e32 v65, v67
	v_pk_add_f32 v[64:65], v[70:71], v[64:65]
	s_nop 0
	v_add_f32_e32 v64, v64, v65
	v_fmamk_f32 v64, v64, 0x3a800000, v198
	v_cmp_gt_f32_e32 vcc, s19, v64
	v_mul_f32_e32 v65, 0x4b800000, v64
	s_nop 0
	v_cndmask_b32_e32 v64, v64, v65, vcc
	v_rsq_f32_e32 v64, v64
	s_nop 0
	v_mul_f32_e32 v65, 0x45800000, v64
	v_cndmask_b32_e32 v64, v64, v65, vcc
	v_mul_f32_e32 v64, v163, v64
	v_pk_mul_f32 v[62:63], v[62:63], v[64:65] op_sel_hi:[1,0]
	v_pk_mul_f32 v[60:61], v[60:61], v[64:65] op_sel_hi:[1,0]
	v_pk_mul_f32 v[66:67], v[58:59], v[64:65] op_sel_hi:[1,0]
	v_pk_mul_f32 v[58:59], v[56:57], v[64:65] op_sel_hi:[1,0]
	v_cvt_pk_bf16_f32 v56, v60, v61
	v_cvt_pk_bf16_f32 v57, v62, v63
	v_pk_mul_f32 v[52:53], v[52:53], v[64:65] op_sel_hi:[1,0]
	v_cvt_pk_bf16_f32 v58, v58, v59
	v_cvt_pk_bf16_f32 v59, v66, v67
	global_store_dwordx4 v[68:69], v[56:59], off
	v_pk_mul_f32 v[54:55], v[54:55], v[64:65] op_sel_hi:[1,0]
	s_nop 0
	v_pk_mul_f32 v[56:57], v[50:51], v[64:65] op_sel_hi:[1,0]
	v_pk_mul_f32 v[50:51], v[48:49], v[64:65] op_sel_hi:[1,0]
	v_cvt_pk_bf16_f32 v48, v52, v53
	v_cvt_pk_bf16_f32 v49, v54, v55
	s_nop 0
	v_cvt_pk_bf16_f32 v50, v50, v51
	v_cvt_pk_bf16_f32 v51, v56, v57
	global_store_dwordx4 v[68:69], v[48:51], off offset:256
	s_nop 1
	v_add_u32_e32 v48, 0x90, v164
	v_mad_i64_i32 v[52:53], s[8:9], v48, s27, v[144:145]
	ds_read_b128 v[48:51], v165 offset:2304
	s_waitcnt lgkmcnt(0)
	v_mov_b32_e32 v54, v49
	v_mov_b32_e32 v55, v50
	v_mov_b32_e32 v49, v51
	v_pk_add_f32 v[48:49], v[54:55], v[48:49]
	s_nop 0
	v_add_f32_e32 v48, v48, v49
	v_fmamk_f32 v48, v48, 0x3a800000, v198
	v_cmp_gt_f32_e32 vcc, s19, v48
	v_mul_f32_e32 v49, 0x4b800000, v48
	s_nop 0
	v_cndmask_b32_e32 v48, v48, v49, vcc
	v_rsq_f32_e32 v48, v48
	s_nop 0
	v_mul_f32_e32 v49, 0x45800000, v48
	v_cndmask_b32_e32 v48, v48, v49, vcc
	v_mul_f32_e32 v48, v163, v48
	v_pk_mul_f32 v[46:47], v[46:47], v[48:49] op_sel_hi:[1,0]
	v_pk_mul_f32 v[44:45], v[44:45], v[48:49] op_sel_hi:[1,0]
	v_pk_mul_f32 v[50:51], v[42:43], v[48:49] op_sel_hi:[1,0]
	v_pk_mul_f32 v[42:43], v[40:41], v[48:49] op_sel_hi:[1,0]
	v_cvt_pk_bf16_f32 v40, v44, v45
	v_cvt_pk_bf16_f32 v41, v46, v47
	v_pk_mul_f32 v[36:37], v[36:37], v[48:49] op_sel_hi:[1,0]
	v_cvt_pk_bf16_f32 v42, v42, v43
	v_cvt_pk_bf16_f32 v43, v50, v51
	global_store_dwordx4 v[52:53], v[40:43], off
	v_pk_mul_f32 v[38:39], v[38:39], v[48:49] op_sel_hi:[1,0]
	s_nop 0
	v_pk_mul_f32 v[40:41], v[34:35], v[48:49] op_sel_hi:[1,0]
	v_pk_mul_f32 v[34:35], v[32:33], v[48:49] op_sel_hi:[1,0]
	v_cvt_pk_bf16_f32 v32, v36, v37
	v_cvt_pk_bf16_f32 v33, v38, v39
	s_nop 0
	v_cvt_pk_bf16_f32 v34, v34, v35
	v_cvt_pk_bf16_f32 v35, v40, v41
	global_store_dwordx4 v[52:53], v[32:35], off offset:256
	s_nop 1
	v_add_u32_e32 v32, 0xa0, v164
	v_mad_i64_i32 v[36:37], s[8:9], v32, s27, v[144:145]
	ds_read_b128 v[32:35], v165 offset:2560
	s_waitcnt lgkmcnt(0)
	v_mov_b32_e32 v38, v33
	v_mov_b32_e32 v39, v34
	v_mov_b32_e32 v33, v35
	v_pk_add_f32 v[32:33], v[38:39], v[32:33]
	s_nop 0
	v_add_f32_e32 v32, v32, v33
	v_fmamk_f32 v32, v32, 0x3a800000, v198
	v_cmp_gt_f32_e32 vcc, s19, v32
	v_mul_f32_e32 v33, 0x4b800000, v32
	s_nop 0
	v_cndmask_b32_e32 v32, v32, v33, vcc
	v_rsq_f32_e32 v32, v32
	s_nop 0
	v_mul_f32_e32 v33, 0x45800000, v32
	v_cndmask_b32_e32 v32, v32, v33, vcc
	v_mul_f32_e32 v32, v163, v32
	v_pk_mul_f32 v[30:31], v[30:31], v[32:33] op_sel_hi:[1,0]
	v_pk_mul_f32 v[28:29], v[28:29], v[32:33] op_sel_hi:[1,0]
	v_pk_mul_f32 v[34:35], v[26:27], v[32:33] op_sel_hi:[1,0]
	v_pk_mul_f32 v[26:27], v[24:25], v[32:33] op_sel_hi:[1,0]
	v_cvt_pk_bf16_f32 v24, v28, v29
	v_cvt_pk_bf16_f32 v25, v30, v31
	v_pk_mul_f32 v[20:21], v[20:21], v[32:33] op_sel_hi:[1,0]
	v_cvt_pk_bf16_f32 v26, v26, v27
	v_cvt_pk_bf16_f32 v27, v34, v35
	global_store_dwordx4 v[36:37], v[24:27], off
	v_pk_mul_f32 v[22:23], v[22:23], v[32:33] op_sel_hi:[1,0]
	s_nop 0
	v_pk_mul_f32 v[24:25], v[18:19], v[32:33] op_sel_hi:[1,0]
	v_pk_mul_f32 v[18:19], v[16:17], v[32:33] op_sel_hi:[1,0]
	v_cvt_pk_bf16_f32 v16, v20, v21
	v_cvt_pk_bf16_f32 v17, v22, v23
	s_nop 0
	v_cvt_pk_bf16_f32 v18, v18, v19
	v_cvt_pk_bf16_f32 v19, v24, v25
	global_store_dwordx4 v[36:37], v[16:19], off offset:256
	s_nop 1
	v_add_u32_e32 v16, 0xb0, v164
	v_mad_i64_i32 v[20:21], s[8:9], v16, s27, v[144:145]
	ds_read_b128 v[16:19], v165 offset:2816
	s_waitcnt lgkmcnt(0)
	v_mov_b32_e32 v22, v17
	v_mov_b32_e32 v23, v18
	v_mov_b32_e32 v17, v19
	v_pk_add_f32 v[16:17], v[22:23], v[16:17]
	s_nop 0
	v_add_f32_e32 v16, v16, v17
	v_fmamk_f32 v16, v16, 0x3a800000, v198
	v_cmp_gt_f32_e32 vcc, s19, v16
	v_mul_f32_e32 v17, 0x4b800000, v16
	s_nop 0
	v_cndmask_b32_e32 v16, v16, v17, vcc
	v_rsq_f32_e32 v16, v16
	s_nop 0
	v_mul_f32_e32 v17, 0x45800000, v16
	v_cndmask_b32_e32 v16, v16, v17, vcc
	v_mul_f32_e32 v16, v163, v16
	v_pk_mul_f32 v[14:15], v[14:15], v[16:17] op_sel_hi:[1,0]
	v_pk_mul_f32 v[12:13], v[12:13], v[16:17] op_sel_hi:[1,0]
	v_pk_mul_f32 v[18:19], v[10:11], v[16:17] op_sel_hi:[1,0]
	v_pk_mul_f32 v[10:11], v[8:9], v[16:17] op_sel_hi:[1,0]
	v_cvt_pk_bf16_f32 v8, v12, v13
	v_cvt_pk_bf16_f32 v9, v14, v15
	s_andn2_b64 vcc, exec, s[46:47]
	v_cvt_pk_bf16_f32 v10, v10, v11
	v_cvt_pk_bf16_f32 v11, v18, v19
	global_store_dwordx4 v[20:21], v[8:11], off
	v_pk_mul_f32 v[6:7], v[6:7], v[16:17] op_sel_hi:[1,0]
	v_pk_mul_f32 v[4:5], v[4:5], v[16:17] op_sel_hi:[1,0]
	v_pk_mul_f32 v[8:9], v[2:3], v[16:17] op_sel_hi:[1,0]
	v_pk_mul_f32 v[2:3], v[0:1], v[16:17] op_sel_hi:[1,0]
	v_cvt_pk_bf16_f32 v0, v4, v5
	v_cvt_pk_bf16_f32 v1, v6, v7
	s_nop 0
	v_cvt_pk_bf16_f32 v2, v2, v3
	v_cvt_pk_bf16_f32 v3, v8, v9
	global_store_dwordx4 v[20:21], v[0:3], off offset:256
	s_cbranch_vccnz .LBB0_263
	s_andn2_b64 vcc, exec, s[20:21]
	s_cbranch_vccnz .LBB0_262
	s_barrier
	s_branch .LBB0_262

.LBB0_294:
	s_or_b64 exec, exec, s[48:49]
	s_ashr_i32 s27, s26, 31
	s_lshl_b64 s[48:49], s[26:27], 19
	s_add_u32 s48, s80, s48
	s_addc_u32 s49, s81, s49
	s_and_b64 s[50:51], s[46:47], exec
	s_cselect_b32 s27, s49, s55
	s_cselect_b32 s53, s48, s54
	s_ashr_i32 s31, s30, 31
	s_lshl_b64 s[50:51], s[30:31], 19
	s_add_u32 s50, s1, s50
	s_addc_u32 s51, s0, s51
	s_and_b64 s[58:59], s[46:47], exec
	s_cselect_b32 s31, s51, s57
	s_cselect_b32 s67, s50, s56
	s_add_u32 s54, s54, 0x40080
	s_addc_u32 s55, s55, 0
	s_add_u32 s68, s56, 0x100
	v_mov_b32_e32 v0, 0
	s_addc_u32 s69, s57, 0
	s_mov_b32 s70, -2
	v_mov_b32_e32 v1, v0
	v_mov_b32_e32 v2, v0
	v_mov_b32_e32 v3, v0
	v_mov_b32_e32 v4, v0
	v_mov_b32_e32 v5, v0
	v_mov_b32_e32 v6, v0
	v_mov_b32_e32 v7, v0
	v_mov_b32_e32 v16, v0
	v_mov_b32_e32 v17, v0
	v_mov_b32_e32 v18, v0
	v_mov_b32_e32 v19, v0
	v_mov_b32_e32 v20, v0
	v_mov_b32_e32 v21, v0
	v_mov_b32_e32 v22, v0
	v_mov_b32_e32 v23, v0
	v_mov_b32_e32 v32, v0
	v_mov_b32_e32 v33, v0
	v_mov_b32_e32 v34, v0
	v_mov_b32_e32 v35, v0
	v_mov_b32_e32 v36, v0
	v_mov_b32_e32 v37, v0
	v_mov_b32_e32 v38, v0
	v_mov_b32_e32 v39, v0
	v_mov_b32_e32 v48, v0
	v_mov_b32_e32 v49, v0
	v_mov_b32_e32 v50, v0
	v_mov_b32_e32 v51, v0
	v_mov_b32_e32 v52, v0
	v_mov_b32_e32 v53, v0
	v_mov_b32_e32 v54, v0
	v_mov_b32_e32 v55, v0
	v_mov_b32_e32 v8, v0
	v_mov_b32_e32 v9, v0
	v_mov_b32_e32 v10, v0
	v_mov_b32_e32 v11, v0
	v_mov_b32_e32 v12, v0
	v_mov_b32_e32 v13, v0
	v_mov_b32_e32 v14, v0
	v_mov_b32_e32 v15, v0
	v_mov_b32_e32 v24, v0
	v_mov_b32_e32 v25, v0
	v_mov_b32_e32 v26, v0
	v_mov_b32_e32 v27, v0
	v_mov_b32_e32 v28, v0
	v_mov_b32_e32 v29, v0
	v_mov_b32_e32 v30, v0
	v_mov_b32_e32 v31, v0
	v_mov_b32_e32 v40, v0
	v_mov_b32_e32 v41, v0
	v_mov_b32_e32 v42, v0
	v_mov_b32_e32 v43, v0
	v_mov_b32_e32 v44, v0
	v_mov_b32_e32 v45, v0
	v_mov_b32_e32 v46, v0
	v_mov_b32_e32 v47, v0
	v_mov_b32_e32 v56, v0
	v_mov_b32_e32 v57, v0
	v_mov_b32_e32 v58, v0
	v_mov_b32_e32 v59, v0
	v_mov_b32_e32 v60, v0
	v_mov_b32_e32 v61, v0
	v_mov_b32_e32 v62, v0
	v_mov_b32_e32 v63, v0
	v_mov_b32_e32 v64, v0
	v_mov_b32_e32 v65, v0
	v_mov_b32_e32 v66, v0
	v_mov_b32_e32 v67, v0
	v_mov_b32_e32 v68, v0
	v_mov_b32_e32 v69, v0
	v_mov_b32_e32 v70, v0
	v_mov_b32_e32 v71, v0
	v_mov_b32_e32 v80, v0
	v_mov_b32_e32 v81, v0
	v_mov_b32_e32 v82, v0
	v_mov_b32_e32 v83, v0
	v_mov_b32_e32 v84, v0
	v_mov_b32_e32 v85, v0
	v_mov_b32_e32 v86, v0
	v_mov_b32_e32 v87, v0
	v_mov_b32_e32 v96, v0
	v_mov_b32_e32 v97, v0
	v_mov_b32_e32 v98, v0
	v_mov_b32_e32 v99, v0
	v_mov_b32_e32 v100, v0
	v_mov_b32_e32 v101, v0
	v_mov_b32_e32 v102, v0
	v_mov_b32_e32 v103, v0
	v_mov_b32_e32 v112, v0
	v_mov_b32_e32 v113, v0
	v_mov_b32_e32 v114, v0
	v_mov_b32_e32 v115, v0
	v_mov_b32_e32 v116, v0
	v_mov_b32_e32 v117, v0
	v_mov_b32_e32 v118, v0
	v_mov_b32_e32 v119, v0
	v_mov_b32_e32 v72, v0
	v_mov_b32_e32 v73, v0
	v_mov_b32_e32 v74, v0
	v_mov_b32_e32 v75, v0
	v_mov_b32_e32 v76, v0
	v_mov_b32_e32 v77, v0
	v_mov_b32_e32 v78, v0
	v_mov_b32_e32 v79, v0
	v_mov_b32_e32 v88, v0
	v_mov_b32_e32 v89, v0
	v_mov_b32_e32 v90, v0
	v_mov_b32_e32 v91, v0
	v_mov_b32_e32 v92, v0
	v_mov_b32_e32 v93, v0
	v_mov_b32_e32 v94, v0
	v_mov_b32_e32 v95, v0
	v_mov_b32_e32 v104, v0
	v_mov_b32_e32 v105, v0
	v_mov_b32_e32 v106, v0
	v_mov_b32_e32 v107, v0
	v_mov_b32_e32 v108, v0
	v_mov_b32_e32 v109, v0
	v_mov_b32_e32 v110, v0
	v_mov_b32_e32 v111, v0
	v_mov_b32_e32 v120, v0
	v_mov_b32_e32 v121, v0
	v_mov_b32_e32 v122, v0
	v_mov_b32_e32 v123, v0
	v_mov_b32_e32 v124, v0
	v_mov_b32_e32 v125, v0
	v_mov_b32_e32 v126, v0
	v_mov_b32_e32 v127, v0
	s_cmp_eq_u32 s9, 0
	s_cbranch_scc1 .LBB0_295
	s_add_u32 s56, s54, 0xfffc0080
	s_addc_u32 s57, s55, -1
	s_add_i32 s71, 0, 0x10000
	s_cmp_eq_u32 s70, 12
	s_cselect_b32 s59, s27, s57
	s_cselect_b32 s58, s53, s56
	v_add_u32_e32 v144, s71, v158
	s_cselect_b32 s57, s31, s69
	s_cselect_b32 s56, s67, s68
	s_add_i32 s76, 0, 0x14000
	ds_read_b128 v[162:165], v144
	ds_read_b128 v[166:169], v144 offset:1024
	ds_read_b128 v[170:173], v144 offset:2048
	ds_read_b128 v[174:177], v144 offset:3072
	v_add_u32_e32 v144, s76, v158
	ds_read_b128 v[178:181], v144
	ds_read_b128 v[182:185], v144 offset:1024
	ds_read_b128 v[186:189], v144 offset:2048
	ds_read_b128 v[190:193], v144 offset:3072
	ds_read_b128 v[194:197], v160
	ds_read_b128 v[200:203], v160 offset:1024
	ds_read_b128 v[216:219], v160 offset:2048
	ds_read_b128 v[220:223], v160 offset:3072
	ds_read_b128 v[224:227], v160 offset:4096
	ds_read_b128 v[228:231], v160 offset:5120
	ds_read_b128 v[232:235], v160 offset:6144
	ds_read_b128 v[236:239], v160 offset:7168
	s_waitcnt vmcnt(24)
	s_waitcnt lgkmcnt(0)
	s_barrier
	s_setprio 1
	s_waitcnt lgkmcnt(0)
	v_mfma_f32_16x16x32_bf16 v[124:127], v[162:165], v[194:197], v[124:127]
	v_mfma_f32_16x16x32_bf16 v[120:123], v[170:173], v[194:197], v[120:123]
	v_mfma_f32_16x16x32_bf16 v[108:111], v[162:165], v[216:219], v[108:111]
	v_mfma_f32_16x16x32_bf16 v[104:107], v[170:173], v[216:219], v[104:107]
	v_mfma_f32_16x16x32_bf16 v[92:95], v[162:165], v[224:227], v[92:95]
	v_mfma_f32_16x16x32_bf16 v[88:91], v[170:173], v[224:227], v[88:91]
	v_mfma_f32_16x16x32_bf16 v[76:79], v[162:165], v[232:235], v[76:79]
	v_mfma_f32_16x16x32_bf16 v[72:75], v[170:173], v[232:235], v[72:75]
	v_mfma_f32_16x16x32_bf16 v[124:127], v[166:169], v[200:203], v[124:127]
	v_mfma_f32_16x16x32_bf16 v[120:123], v[174:177], v[200:203], v[120:123]
	v_mfma_f32_16x16x32_bf16 v[108:111], v[166:169], v[220:223], v[108:111]
	v_mfma_f32_16x16x32_bf16 v[104:107], v[174:177], v[220:223], v[104:107]
	v_mfma_f32_16x16x32_bf16 v[92:95], v[166:169], v[228:231], v[92:95]
	v_mfma_f32_16x16x32_bf16 v[88:91], v[174:177], v[228:231], v[88:91]
	v_mfma_f32_16x16x32_bf16 v[76:79], v[166:169], v[236:239], v[76:79]
	v_mfma_f32_16x16x32_bf16 v[72:75], v[174:177], v[236:239], v[72:75]
	s_setprio 0
	s_setprio 1
	v_mfma_f32_16x16x32_bf16 v[116:119], v[178:181], v[194:197], v[116:119]
	v_mfma_f32_16x16x32_bf16 v[112:115], v[186:189], v[194:197], v[112:115]
	v_mfma_f32_16x16x32_bf16 v[100:103], v[178:181], v[216:219], v[100:103]
	v_mfma_f32_16x16x32_bf16 v[96:99], v[186:189], v[216:219], v[96:99]
	v_mfma_f32_16x16x32_bf16 v[84:87], v[178:181], v[224:227], v[84:87]
	v_mfma_f32_16x16x32_bf16 v[80:83], v[186:189], v[224:227], v[80:83]
	v_mfma_f32_16x16x32_bf16 v[68:71], v[178:181], v[232:235], v[68:71]
	v_mfma_f32_16x16x32_bf16 v[64:67], v[186:189], v[232:235], v[64:67]
	v_mfma_f32_16x16x32_bf16 v[116:119], v[182:185], v[200:203], v[116:119]
	v_mfma_f32_16x16x32_bf16 v[112:115], v[190:193], v[200:203], v[112:115]
	v_mfma_f32_16x16x32_bf16 v[100:103], v[182:185], v[220:223], v[100:103]
	v_mfma_f32_16x16x32_bf16 v[96:99], v[190:193], v[220:223], v[96:99]
	v_mfma_f32_16x16x32_bf16 v[84:87], v[182:185], v[228:231], v[84:87]
	v_mfma_f32_16x16x32_bf16 v[80:83], v[190:193], v[228:231], v[80:83]
	v_mfma_f32_16x16x32_bf16 v[68:71], v[182:185], v[236:239], v[68:71]
	v_mfma_f32_16x16x32_bf16 v[64:67], v[190:193], v[236:239], v[64:67]
	s_setprio 0
	s_barrier
	s_add_i32 s71, s71, s33
	v_lshl_add_u64 v[144:145], s[56:57], 0, v[128:129]
	s_mov_b32 m0, s71
	ds_read_b128 v[194:197], v160 offset:16384
	ds_read_b128 v[200:203], v160 offset:17408
	ds_read_b128 v[216:219], v160 offset:18432
	ds_read_b128 v[220:223], v160 offset:19456
	ds_read_b128 v[224:227], v160 offset:20480
	ds_read_b128 v[228:231], v160 offset:21504
	ds_read_b128 v[232:235], v160 offset:22528
	ds_read_b128 v[236:239], v160 offset:23552
	global_load_lds_dwordx4 v[144:145], off
	s_add_i32 m0, s71, 0x2000
	s_add_u32 s72, s56, 0x40000
	v_lshl_add_u64 v[204:205], s[56:57], 0, v[134:135]
	s_addc_u32 s73, s57, 0
	s_add_i32 s71, s76, s33
	global_load_lds_dwordx4 v[204:205], off
	v_lshl_add_u64 v[206:207], s[72:73], 0, v[128:129]
	s_mov_b32 m0, s71
	v_lshl_add_u64 v[240:241], s[58:59], 0, v[132:133]
	global_load_lds_dwordx4 v[206:207], off
	v_lshl_add_u64 v[206:207], s[72:73], 0, v[134:135]
	s_add_i32 m0, s71, 0x2000
	s_nop 0
	global_load_lds_dwordx4 v[206:207], off
	v_lshl_add_u64 v[206:207], s[58:59], 0, v[130:131]
	s_mov_b32 m0, s60
	s_nop 0
	global_load_lds_dwordx4 v[206:207], off
	s_mov_b32 m0, s61
	s_nop 0
	global_load_lds_dwordx4 v[240:241], off
	s_waitcnt vmcnt(24)
	s_waitcnt lgkmcnt(0)
	s_barrier
	s_setprio 1
	s_waitcnt lgkmcnt(0)
	v_mfma_f32_16x16x32_bf16 v[60:63], v[162:165], v[194:197], v[60:63]
	v_mfma_f32_16x16x32_bf16 v[56:59], v[170:173], v[194:197], v[56:59]
	v_mfma_f32_16x16x32_bf16 v[44:47], v[162:165], v[216:219], v[44:47]
	v_mfma_f32_16x16x32_bf16 v[40:43], v[170:173], v[216:219], v[40:43]
	v_mfma_f32_16x16x32_bf16 v[28:31], v[162:165], v[224:227], v[28:31]
	v_mfma_f32_16x16x32_bf16 v[24:27], v[170:173], v[224:227], v[24:27]
	v_mfma_f32_16x16x32_bf16 v[12:15], v[162:165], v[232:235], v[12:15]
	v_mfma_f32_16x16x32_bf16 v[8:11], v[170:173], v[232:235], v[8:11]
	v_mfma_f32_16x16x32_bf16 v[60:63], v[166:169], v[200:203], v[60:63]
	v_mfma_f32_16x16x32_bf16 v[56:59], v[174:177], v[200:203], v[56:59]
	v_mfma_f32_16x16x32_bf16 v[44:47], v[166:169], v[220:223], v[44:47]
	v_mfma_f32_16x16x32_bf16 v[40:43], v[174:177], v[220:223], v[40:43]
	v_mfma_f32_16x16x32_bf16 v[28:31], v[166:169], v[228:231], v[28:31]
	v_mfma_f32_16x16x32_bf16 v[24:27], v[174:177], v[228:231], v[24:27]
	v_mfma_f32_16x16x32_bf16 v[12:15], v[166:169], v[236:239], v[12:15]
	v_mfma_f32_16x16x32_bf16 v[8:11], v[174:177], v[236:239], v[8:11]
	s_setprio 0
	s_setprio 1
	v_mfma_f32_16x16x32_bf16 v[52:55], v[178:181], v[194:197], v[52:55]
	v_mfma_f32_16x16x32_bf16 v[48:51], v[186:189], v[194:197], v[48:51]
	v_mfma_f32_16x16x32_bf16 v[36:39], v[178:181], v[216:219], v[36:39]
	v_mfma_f32_16x16x32_bf16 v[32:35], v[186:189], v[216:219], v[32:35]
	v_mfma_f32_16x16x32_bf16 v[20:23], v[178:181], v[224:227], v[20:23]
	v_mfma_f32_16x16x32_bf16 v[16:19], v[186:189], v[224:227], v[16:19]
	v_mfma_f32_16x16x32_bf16 v[4:7], v[178:181], v[232:235], v[4:7]
	v_mfma_f32_16x16x32_bf16 v[0:3], v[186:189], v[232:235], v[0:3]
	v_mfma_f32_16x16x32_bf16 v[52:55], v[182:185], v[200:203], v[52:55]
	v_mfma_f32_16x16x32_bf16 v[48:51], v[190:193], v[200:203], v[48:51]
	v_mfma_f32_16x16x32_bf16 v[36:39], v[182:185], v[220:223], v[36:39]
	v_mfma_f32_16x16x32_bf16 v[32:35], v[190:193], v[220:223], v[32:35]
	v_mfma_f32_16x16x32_bf16 v[20:23], v[182:185], v[228:231], v[20:23]
	v_mfma_f32_16x16x32_bf16 v[16:19], v[190:193], v[228:231], v[16:19]
	v_mfma_f32_16x16x32_bf16 v[4:7], v[182:185], v[236:239], v[4:7]
	v_mfma_f32_16x16x32_bf16 v[0:3], v[190:193], v[236:239], v[0:3]
	s_setprio 0
	s_barrier
	s_add_i32 s71, 0, 0x18000
	v_add_u32_e32 v161, s71, v158
	s_add_i32 s72, 0, 0x1c000
	ds_read_b128 v[162:165], v161
	ds_read_b128 v[166:169], v161 offset:1024
	ds_read_b128 v[170:173], v161 offset:2048
	ds_read_b128 v[174:177], v161 offset:3072
	v_add_u32_e32 v161, s72, v158
	ds_read_b128 v[178:181], v161
	ds_read_b128 v[182:185], v161 offset:1024
	ds_read_b128 v[186:189], v161 offset:2048
	ds_read_b128 v[190:193], v161 offset:3072
	s_add_u32 s58, s58, 0x40000
	s_addc_u32 s59, s59, 0
	s_mov_b32 m0, s62
	v_lshl_add_u64 v[242:243], s[58:59], 0, v[130:131]
	ds_read_b128 v[194:197], v160 offset:32768
	ds_read_b128 v[200:203], v160 offset:33792
	ds_read_b128 v[216:219], v160 offset:34816
	ds_read_b128 v[220:223], v160 offset:35840
	ds_read_b128 v[224:227], v160 offset:36864
	ds_read_b128 v[228:231], v160 offset:37888
	ds_read_b128 v[232:235], v160 offset:38912
	ds_read_b128 v[236:239], v160 offset:39936
	global_load_lds_dwordx4 v[242:243], off
	v_lshl_add_u64 v[242:243], s[58:59], 0, v[132:133]
	s_mov_b32 m0, s63
	s_nop 0
	global_load_lds_dwordx4 v[242:243], off
	s_waitcnt vmcnt(24)
	s_waitcnt lgkmcnt(0)
	s_barrier
	s_setprio 1
	s_waitcnt lgkmcnt(0)
	v_mfma_f32_16x16x32_bf16 v[124:127], v[162:165], v[194:197], v[124:127]
	v_mfma_f32_16x16x32_bf16 v[120:123], v[170:173], v[194:197], v[120:123]
	v_mfma_f32_16x16x32_bf16 v[108:111], v[162:165], v[216:219], v[108:111]
	v_mfma_f32_16x16x32_bf16 v[104:107], v[170:173], v[216:219], v[104:107]
	v_mfma_f32_16x16x32_bf16 v[92:95], v[162:165], v[224:227], v[92:95]
	v_mfma_f32_16x16x32_bf16 v[88:91], v[170:173], v[224:227], v[88:91]
	v_mfma_f32_16x16x32_bf16 v[76:79], v[162:165], v[232:235], v[76:79]
	v_mfma_f32_16x16x32_bf16 v[72:75], v[170:173], v[232:235], v[72:75]
	v_mfma_f32_16x16x32_bf16 v[124:127], v[166:169], v[200:203], v[124:127]
	v_mfma_f32_16x16x32_bf16 v[120:123], v[174:177], v[200:203], v[120:123]
	v_mfma_f32_16x16x32_bf16 v[108:111], v[166:169], v[220:223], v[108:111]
	v_mfma_f32_16x16x32_bf16 v[104:107], v[174:177], v[220:223], v[104:107]
	v_mfma_f32_16x16x32_bf16 v[92:95], v[166:169], v[228:231], v[92:95]
	v_mfma_f32_16x16x32_bf16 v[88:91], v[174:177], v[228:231], v[88:91]
	v_mfma_f32_16x16x32_bf16 v[76:79], v[166:169], v[236:239], v[76:79]
	v_mfma_f32_16x16x32_bf16 v[72:75], v[174:177], v[236:239], v[72:75]
	s_setprio 0
	s_setprio 1
	v_mfma_f32_16x16x32_bf16 v[116:119], v[178:181], v[194:197], v[116:119]
	v_mfma_f32_16x16x32_bf16 v[112:115], v[186:189], v[194:197], v[112:115]
	v_mfma_f32_16x16x32_bf16 v[100:103], v[178:181], v[216:219], v[100:103]
	v_mfma_f32_16x16x32_bf16 v[96:99], v[186:189], v[216:219], v[96:99]
	v_mfma_f32_16x16x32_bf16 v[84:87], v[178:181], v[224:227], v[84:87]
	v_mfma_f32_16x16x32_bf16 v[80:83], v[186:189], v[224:227], v[80:83]
	v_mfma_f32_16x16x32_bf16 v[68:71], v[178:181], v[232:235], v[68:71]
	v_mfma_f32_16x16x32_bf16 v[64:67], v[186:189], v[232:235], v[64:67]
	v_mfma_f32_16x16x32_bf16 v[116:119], v[182:185], v[200:203], v[116:119]
	v_mfma_f32_16x16x32_bf16 v[112:115], v[190:193], v[200:203], v[112:115]
	v_mfma_f32_16x16x32_bf16 v[100:103], v[182:185], v[220:223], v[100:103]
	v_mfma_f32_16x16x32_bf16 v[96:99], v[190:193], v[220:223], v[96:99]
	v_mfma_f32_16x16x32_bf16 v[84:87], v[182:185], v[228:231], v[84:87]
	v_mfma_f32_16x16x32_bf16 v[80:83], v[190:193], v[228:231], v[80:83]
	v_mfma_f32_16x16x32_bf16 v[68:71], v[182:185], v[236:239], v[68:71]
	v_mfma_f32_16x16x32_bf16 v[64:67], v[190:193], v[236:239], v[64:67]
	s_setprio 0
	s_barrier
	s_branch .Lp1o_q3
.LBB0_295:
	s_add_u32 s56, s54, 0xfffc0080
	s_addc_u32 s57, s55, -1
	s_add_i32 s71, 0, 0x10000
	s_cmp_eq_u32 s70, 12
	s_cselect_b32 s59, s27, s57
	s_cselect_b32 s58, s53, s56
	v_add_u32_e32 v144, s71, v158
	s_cselect_b32 s57, s31, s69
	s_cselect_b32 s56, s67, s68
	s_add_i32 s76, 0, 0x14000
	ds_read_b128 v[162:165], v144
	ds_read_b128 v[166:169], v144 offset:1024
	ds_read_b128 v[170:173], v144 offset:2048
	ds_read_b128 v[174:177], v144 offset:3072
	v_add_u32_e32 v144, s76, v158
	ds_read_b128 v[178:181], v144
	ds_read_b128 v[182:185], v144 offset:1024
	ds_read_b128 v[186:189], v144 offset:2048
	ds_read_b128 v[190:193], v144 offset:3072
	v_lshl_add_u64 v[144:145], s[54:55], 0, v[140:141]
	s_add_i32 m0, s60, 0xc000
	ds_read_b128 v[194:197], v160
	ds_read_b128 v[200:203], v160 offset:1024
	ds_read_b128 v[216:219], v160 offset:2048
	ds_read_b128 v[220:223], v160 offset:3072
	ds_read_b128 v[224:227], v160 offset:4096
	ds_read_b128 v[228:231], v160 offset:5120
	ds_read_b128 v[232:235], v160 offset:6144
	ds_read_b128 v[236:239], v160 offset:7168
	global_load_lds_dwordx4 v[144:145], off
	v_lshl_add_u64 v[144:145], s[54:55], 0, v[142:143]
	s_add_i32 m0, s60, 0xe000
	s_nop 0
	global_load_lds_dwordx4 v[144:145], off
	s_waitcnt vmcnt(8)
	s_waitcnt lgkmcnt(0)
	s_barrier
	s_setprio 1
	s_waitcnt lgkmcnt(0)
	v_mfma_f32_16x16x32_bf16 v[124:127], v[162:165], v[194:197], v[124:127]
	v_mfma_f32_16x16x32_bf16 v[120:123], v[170:173], v[194:197], v[120:123]
	v_mfma_f32_16x16x32_bf16 v[108:111], v[162:165], v[216:219], v[108:111]
	v_mfma_f32_16x16x32_bf16 v[104:107], v[170:173], v[216:219], v[104:107]
	v_mfma_f32_16x16x32_bf16 v[92:95], v[162:165], v[224:227], v[92:95]
	v_mfma_f32_16x16x32_bf16 v[88:91], v[170:173], v[224:227], v[88:91]
	v_mfma_f32_16x16x32_bf16 v[76:79], v[162:165], v[232:235], v[76:79]
	v_mfma_f32_16x16x32_bf16 v[72:75], v[170:173], v[232:235], v[72:75]
	v_mfma_f32_16x16x32_bf16 v[124:127], v[166:169], v[200:203], v[124:127]
	v_mfma_f32_16x16x32_bf16 v[120:123], v[174:177], v[200:203], v[120:123]
	v_mfma_f32_16x16x32_bf16 v[108:111], v[166:169], v[220:223], v[108:111]
	v_mfma_f32_16x16x32_bf16 v[104:107], v[174:177], v[220:223], v[104:107]
	v_mfma_f32_16x16x32_bf16 v[92:95], v[166:169], v[228:231], v[92:95]
	v_mfma_f32_16x16x32_bf16 v[88:91], v[174:177], v[228:231], v[88:91]
	v_mfma_f32_16x16x32_bf16 v[76:79], v[166:169], v[236:239], v[76:79]
	v_mfma_f32_16x16x32_bf16 v[72:75], v[174:177], v[236:239], v[72:75]
	s_setprio 0
	s_setprio 1
	v_mfma_f32_16x16x32_bf16 v[116:119], v[178:181], v[194:197], v[116:119]
	v_mfma_f32_16x16x32_bf16 v[112:115], v[186:189], v[194:197], v[112:115]
	v_mfma_f32_16x16x32_bf16 v[100:103], v[178:181], v[216:219], v[100:103]
	v_mfma_f32_16x16x32_bf16 v[96:99], v[186:189], v[216:219], v[96:99]
	v_mfma_f32_16x16x32_bf16 v[84:87], v[178:181], v[224:227], v[84:87]
	v_mfma_f32_16x16x32_bf16 v[80:83], v[186:189], v[224:227], v[80:83]
	v_mfma_f32_16x16x32_bf16 v[68:71], v[178:181], v[232:235], v[68:71]
	v_mfma_f32_16x16x32_bf16 v[64:67], v[186:189], v[232:235], v[64:67]
	v_mfma_f32_16x16x32_bf16 v[116:119], v[182:185], v[200:203], v[116:119]
	v_mfma_f32_16x16x32_bf16 v[112:115], v[190:193], v[200:203], v[112:115]
	v_mfma_f32_16x16x32_bf16 v[100:103], v[182:185], v[220:223], v[100:103]
	v_mfma_f32_16x16x32_bf16 v[96:99], v[190:193], v[220:223], v[96:99]
	v_mfma_f32_16x16x32_bf16 v[84:87], v[182:185], v[228:231], v[84:87]
	v_mfma_f32_16x16x32_bf16 v[80:83], v[190:193], v[228:231], v[80:83]
	v_mfma_f32_16x16x32_bf16 v[68:71], v[182:185], v[236:239], v[68:71]
	v_mfma_f32_16x16x32_bf16 v[64:67], v[190:193], v[236:239], v[64:67]
	s_setprio 0
	s_barrier
	s_add_i32 s71, s71, s33
	v_lshl_add_u64 v[144:145], s[56:57], 0, v[128:129]
	s_mov_b32 m0, s71
	ds_read_b128 v[194:197], v160 offset:16384
	ds_read_b128 v[200:203], v160 offset:17408
	ds_read_b128 v[216:219], v160 offset:18432
	ds_read_b128 v[220:223], v160 offset:19456
	ds_read_b128 v[224:227], v160 offset:20480
	ds_read_b128 v[228:231], v160 offset:21504
	ds_read_b128 v[232:235], v160 offset:22528
	ds_read_b128 v[236:239], v160 offset:23552
	global_load_lds_dwordx4 v[144:145], off
	s_add_i32 m0, s71, 0x2000
	s_add_u32 s72, s56, 0x40000
	v_lshl_add_u64 v[204:205], s[56:57], 0, v[134:135]
	s_addc_u32 s73, s57, 0
	s_add_i32 s71, s76, s33
	global_load_lds_dwordx4 v[204:205], off
	v_lshl_add_u64 v[206:207], s[72:73], 0, v[128:129]
	s_mov_b32 m0, s71
	v_lshl_add_u64 v[240:241], s[58:59], 0, v[132:133]
	global_load_lds_dwordx4 v[206:207], off
	v_lshl_add_u64 v[206:207], s[72:73], 0, v[134:135]
	s_add_i32 m0, s71, 0x2000
	s_nop 0
	global_load_lds_dwordx4 v[206:207], off
	v_lshl_add_u64 v[206:207], s[58:59], 0, v[130:131]
	s_mov_b32 m0, s60
	s_nop 0
	global_load_lds_dwordx4 v[206:207], off
	s_mov_b32 m0, s61
	s_nop 0
	global_load_lds_dwordx4 v[240:241], off
	s_waitcnt vmcnt(8)
	s_waitcnt lgkmcnt(0)
	s_barrier
	s_setprio 1
	s_waitcnt lgkmcnt(0)
	v_mfma_f32_16x16x32_bf16 v[60:63], v[162:165], v[194:197], v[60:63]
	v_mfma_f32_16x16x32_bf16 v[56:59], v[170:173], v[194:197], v[56:59]
	v_mfma_f32_16x16x32_bf16 v[44:47], v[162:165], v[216:219], v[44:47]
	v_mfma_f32_16x16x32_bf16 v[40:43], v[170:173], v[216:219], v[40:43]
	v_mfma_f32_16x16x32_bf16 v[28:31], v[162:165], v[224:227], v[28:31]
	v_mfma_f32_16x16x32_bf16 v[24:27], v[170:173], v[224:227], v[24:27]
	v_mfma_f32_16x16x32_bf16 v[12:15], v[162:165], v[232:235], v[12:15]
	v_mfma_f32_16x16x32_bf16 v[8:11], v[170:173], v[232:235], v[8:11]
	v_mfma_f32_16x16x32_bf16 v[60:63], v[166:169], v[200:203], v[60:63]
	v_mfma_f32_16x16x32_bf16 v[56:59], v[174:177], v[200:203], v[56:59]
	v_mfma_f32_16x16x32_bf16 v[44:47], v[166:169], v[220:223], v[44:47]
	v_mfma_f32_16x16x32_bf16 v[40:43], v[174:177], v[220:223], v[40:43]
	v_mfma_f32_16x16x32_bf16 v[28:31], v[166:169], v[228:231], v[28:31]
	v_mfma_f32_16x16x32_bf16 v[24:27], v[174:177], v[228:231], v[24:27]
	v_mfma_f32_16x16x32_bf16 v[12:15], v[166:169], v[236:239], v[12:15]
	v_mfma_f32_16x16x32_bf16 v[8:11], v[174:177], v[236:239], v[8:11]
	s_setprio 0
	s_setprio 1
	v_mfma_f32_16x16x32_bf16 v[52:55], v[178:181], v[194:197], v[52:55]
	v_mfma_f32_16x16x32_bf16 v[48:51], v[186:189], v[194:197], v[48:51]
	v_mfma_f32_16x16x32_bf16 v[36:39], v[178:181], v[216:219], v[36:39]
	v_mfma_f32_16x16x32_bf16 v[32:35], v[186:189], v[216:219], v[32:35]
	v_mfma_f32_16x16x32_bf16 v[20:23], v[178:181], v[224:227], v[20:23]
	v_mfma_f32_16x16x32_bf16 v[16:19], v[186:189], v[224:227], v[16:19]
	v_mfma_f32_16x16x32_bf16 v[4:7], v[178:181], v[232:235], v[4:7]
	v_mfma_f32_16x16x32_bf16 v[0:3], v[186:189], v[232:235], v[0:3]
	v_mfma_f32_16x16x32_bf16 v[52:55], v[182:185], v[200:203], v[52:55]
	v_mfma_f32_16x16x32_bf16 v[48:51], v[190:193], v[200:203], v[48:51]
	v_mfma_f32_16x16x32_bf16 v[36:39], v[182:185], v[220:223], v[36:39]
	v_mfma_f32_16x16x32_bf16 v[32:35], v[190:193], v[220:223], v[32:35]
	v_mfma_f32_16x16x32_bf16 v[20:23], v[182:185], v[228:231], v[20:23]
	v_mfma_f32_16x16x32_bf16 v[16:19], v[190:193], v[228:231], v[16:19]
	v_mfma_f32_16x16x32_bf16 v[4:7], v[182:185], v[236:239], v[4:7]
	v_mfma_f32_16x16x32_bf16 v[0:3], v[190:193], v[236:239], v[0:3]
	s_setprio 0
	s_barrier
	s_add_i32 s71, 0, 0x18000
	v_add_u32_e32 v161, s71, v158
	s_add_i32 s72, 0, 0x1c000
	ds_read_b128 v[162:165], v161
	ds_read_b128 v[166:169], v161 offset:1024
	ds_read_b128 v[170:173], v161 offset:2048
	ds_read_b128 v[174:177], v161 offset:3072
	v_add_u32_e32 v161, s72, v158
	ds_read_b128 v[178:181], v161
	ds_read_b128 v[182:185], v161 offset:1024
	ds_read_b128 v[186:189], v161 offset:2048
	ds_read_b128 v[190:193], v161 offset:3072
	s_add_u32 s58, s58, 0x40000
	s_addc_u32 s59, s59, 0
	s_mov_b32 m0, s62
	v_lshl_add_u64 v[242:243], s[58:59], 0, v[130:131]
	ds_read_b128 v[194:197], v160 offset:32768
	ds_read_b128 v[200:203], v160 offset:33792
	ds_read_b128 v[216:219], v160 offset:34816
	ds_read_b128 v[220:223], v160 offset:35840
	ds_read_b128 v[224:227], v160 offset:36864
	ds_read_b128 v[228:231], v160 offset:37888
	ds_read_b128 v[232:235], v160 offset:38912
	ds_read_b128 v[236:239], v160 offset:39936
	global_load_lds_dwordx4 v[242:243], off
	v_lshl_add_u64 v[242:243], s[58:59], 0, v[132:133]
	s_mov_b32 m0, s63
	s_nop 0
	global_load_lds_dwordx4 v[242:243], off
	s_waitcnt vmcnt(8)
	s_waitcnt lgkmcnt(0)
	s_barrier
	s_setprio 1
	s_waitcnt lgkmcnt(0)
	v_mfma_f32_16x16x32_bf16 v[124:127], v[162:165], v[194:197], v[124:127]
	v_mfma_f32_16x16x32_bf16 v[120:123], v[170:173], v[194:197], v[120:123]
	v_mfma_f32_16x16x32_bf16 v[108:111], v[162:165], v[216:219], v[108:111]
	v_mfma_f32_16x16x32_bf16 v[104:107], v[170:173], v[216:219], v[104:107]
	v_mfma_f32_16x16x32_bf16 v[92:95], v[162:165], v[224:227], v[92:95]
	v_mfma_f32_16x16x32_bf16 v[88:91], v[170:173], v[224:227], v[88:91]
	v_mfma_f32_16x16x32_bf16 v[76:79], v[162:165], v[232:235], v[76:79]
	v_mfma_f32_16x16x32_bf16 v[72:75], v[170:173], v[232:235], v[72:75]
	v_mfma_f32_16x16x32_bf16 v[124:127], v[166:169], v[200:203], v[124:127]
	v_mfma_f32_16x16x32_bf16 v[120:123], v[174:177], v[200:203], v[120:123]
	v_mfma_f32_16x16x32_bf16 v[108:111], v[166:169], v[220:223], v[108:111]
	v_mfma_f32_16x16x32_bf16 v[104:107], v[174:177], v[220:223], v[104:107]
	v_mfma_f32_16x16x32_bf16 v[92:95], v[166:169], v[228:231], v[92:95]
	v_mfma_f32_16x16x32_bf16 v[88:91], v[174:177], v[228:231], v[88:91]
	v_mfma_f32_16x16x32_bf16 v[76:79], v[166:169], v[236:239], v[76:79]
	v_mfma_f32_16x16x32_bf16 v[72:75], v[174:177], v[236:239], v[72:75]
	s_setprio 0
	s_setprio 1
	v_mfma_f32_16x16x32_bf16 v[116:119], v[178:181], v[194:197], v[116:119]
	v_mfma_f32_16x16x32_bf16 v[112:115], v[186:189], v[194:197], v[112:115]
	v_mfma_f32_16x16x32_bf16 v[100:103], v[178:181], v[216:219], v[100:103]
	v_mfma_f32_16x16x32_bf16 v[96:99], v[186:189], v[216:219], v[96:99]
	v_mfma_f32_16x16x32_bf16 v[84:87], v[178:181], v[224:227], v[84:87]
	v_mfma_f32_16x16x32_bf16 v[80:83], v[186:189], v[224:227], v[80:83]
	v_mfma_f32_16x16x32_bf16 v[68:71], v[178:181], v[232:235], v[68:71]
	v_mfma_f32_16x16x32_bf16 v[64:67], v[186:189], v[232:235], v[64:67]
	v_mfma_f32_16x16x32_bf16 v[116:119], v[182:185], v[200:203], v[116:119]
	v_mfma_f32_16x16x32_bf16 v[112:115], v[190:193], v[200:203], v[112:115]
	v_mfma_f32_16x16x32_bf16 v[100:103], v[182:185], v[220:223], v[100:103]
	v_mfma_f32_16x16x32_bf16 v[96:99], v[190:193], v[220:223], v[96:99]
	v_mfma_f32_16x16x32_bf16 v[84:87], v[182:185], v[228:231], v[84:87]
	v_mfma_f32_16x16x32_bf16 v[80:83], v[190:193], v[228:231], v[80:83]
	v_mfma_f32_16x16x32_bf16 v[68:71], v[182:185], v[236:239], v[68:71]
	v_mfma_f32_16x16x32_bf16 v[64:67], v[190:193], v[236:239], v[64:67]
	s_setprio 0
	s_barrier
.Lp1o_q3:
	s_add_i32 s58, s71, s33
	v_lshl_add_u64 v[144:145], v[144:145], 0, s[88:89]
	s_mov_b32 m0, s58
	ds_read_b128 v[194:197], v160 offset:49152
	ds_read_b128 v[200:203], v160 offset:50176
	ds_read_b128 v[216:219], v160 offset:51200
	ds_read_b128 v[220:223], v160 offset:52224
	ds_read_b128 v[224:227], v160 offset:53248
	ds_read_b128 v[228:231], v160 offset:54272
	ds_read_b128 v[232:235], v160 offset:55296
	ds_read_b128 v[236:239], v160 offset:56320
	global_load_lds_dwordx4 v[144:145], off
	s_add_i32 m0, s58, 0x2000
	s_add_u32 s56, s56, 0x40080
	v_lshl_add_u64 v[144:145], v[204:205], 0, s[88:89]
	s_addc_u32 s57, s57, 0
	s_add_i32 s58, s72, s33
	global_load_lds_dwordx4 v[144:145], off
	v_lshl_add_u64 v[144:145], s[56:57], 0, v[128:129]
	s_mov_b32 m0, s58
	s_nop 0
	global_load_lds_dwordx4 v[144:145], off
	v_lshl_add_u64 v[144:145], s[56:57], 0, v[134:135]
	s_add_i32 m0, s58, 0x2000
	s_nop 0
	global_load_lds_dwordx4 v[144:145], off
	v_lshl_add_u64 v[144:145], v[206:207], 0, s[88:89]
	s_mov_b32 m0, s64
	s_nop 0
	global_load_lds_dwordx4 v[144:145], off
	v_lshl_add_u64 v[144:145], v[240:241], 0, s[88:89]
	s_mov_b32 m0, s65
	s_nop 0
	global_load_lds_dwordx4 v[144:145], off
	s_waitcnt vmcnt(8)
	s_waitcnt lgkmcnt(0)
	s_barrier
	s_setprio 1
	s_waitcnt lgkmcnt(0)
	v_mfma_f32_16x16x32_bf16 v[60:63], v[162:165], v[194:197], v[60:63]
	v_mfma_f32_16x16x32_bf16 v[56:59], v[170:173], v[194:197], v[56:59]
	v_mfma_f32_16x16x32_bf16 v[44:47], v[162:165], v[216:219], v[44:47]
	v_mfma_f32_16x16x32_bf16 v[40:43], v[170:173], v[216:219], v[40:43]
	v_mfma_f32_16x16x32_bf16 v[28:31], v[162:165], v[224:227], v[28:31]
	v_mfma_f32_16x16x32_bf16 v[24:27], v[170:173], v[224:227], v[24:27]
	v_mfma_f32_16x16x32_bf16 v[12:15], v[162:165], v[232:235], v[12:15]
	v_mfma_f32_16x16x32_bf16 v[8:11], v[170:173], v[232:235], v[8:11]
	v_mfma_f32_16x16x32_bf16 v[60:63], v[166:169], v[200:203], v[60:63]
	v_mfma_f32_16x16x32_bf16 v[56:59], v[174:177], v[200:203], v[56:59]
	v_mfma_f32_16x16x32_bf16 v[44:47], v[166:169], v[220:223], v[44:47]
	v_mfma_f32_16x16x32_bf16 v[40:43], v[174:177], v[220:223], v[40:43]
	v_mfma_f32_16x16x32_bf16 v[28:31], v[166:169], v[228:231], v[28:31]
	v_mfma_f32_16x16x32_bf16 v[24:27], v[174:177], v[228:231], v[24:27]
	v_mfma_f32_16x16x32_bf16 v[12:15], v[166:169], v[236:239], v[12:15]
	v_mfma_f32_16x16x32_bf16 v[8:11], v[174:177], v[236:239], v[8:11]
	s_setprio 0
	s_setprio 1
	v_mfma_f32_16x16x32_bf16 v[52:55], v[178:181], v[194:197], v[52:55]
	v_mfma_f32_16x16x32_bf16 v[48:51], v[186:189], v[194:197], v[48:51]
	v_mfma_f32_16x16x32_bf16 v[36:39], v[178:181], v[216:219], v[36:39]
	v_mfma_f32_16x16x32_bf16 v[32:35], v[186:189], v[216:219], v[32:35]
	v_mfma_f32_16x16x32_bf16 v[20:23], v[178:181], v[224:227], v[20:23]
	v_mfma_f32_16x16x32_bf16 v[16:19], v[186:189], v[224:227], v[16:19]
	v_mfma_f32_16x16x32_bf16 v[4:7], v[178:181], v[232:235], v[4:7]
	v_mfma_f32_16x16x32_bf16 v[0:3], v[186:189], v[232:235], v[0:3]
	v_mfma_f32_16x16x32_bf16 v[52:55], v[182:185], v[200:203], v[52:55]
	v_mfma_f32_16x16x32_bf16 v[48:51], v[190:193], v[200:203], v[48:51]
	v_mfma_f32_16x16x32_bf16 v[36:39], v[182:185], v[220:223], v[36:39]
	v_mfma_f32_16x16x32_bf16 v[32:35], v[190:193], v[220:223], v[32:35]
	v_mfma_f32_16x16x32_bf16 v[20:23], v[182:185], v[228:231], v[20:23]
	v_mfma_f32_16x16x32_bf16 v[16:19], v[190:193], v[228:231], v[16:19]
	v_mfma_f32_16x16x32_bf16 v[4:7], v[182:185], v[236:239], v[4:7]
	v_mfma_f32_16x16x32_bf16 v[0:3], v[190:193], v[236:239], v[0:3]
	s_setprio 0
	s_barrier
	s_add_i32 s70, s70, 2
	s_add_u32 s54, s54, 0x100
	s_addc_u32 s55, s55, 0
	s_add_u32 s68, s68, 0x100
	s_addc_u32 s69, s69, 0
	s_cmp_gt_u32 s70, 13
	s_cbranch_scc0 .LBB0_295
	s_and_b64 vcc, exec, s[22:23]
	s_cbranch_vccz .LBB0_298
	s_barrier
.LBB0_298:
	s_add_u32 s100, s53, 0x40080
	s_addc_u32 s101, s27, 0
	v_lshl_add_u64 v[144:145], s[100:101], 0, v[140:141]
	s_add_i32 m0, s60, 0xc000
	s_nop 0
	global_load_lds_dwordx4 v[144:145], off
	v_lshl_add_u64 v[144:145], s[100:101], 0, v[142:143]
	s_add_i32 m0, s60, 0xe000
	s_nop 0
	global_load_lds_dwordx4 v[144:145], off
	v_lshl_or_b32 v144, s8, 8, v159
	s_lshl_b32 s8, s9, 12
	s_and_b32 s8, s8, 0x1000
	v_add_u32_e32 v162, s8, v156
	ds_read_b128 v[164:167], v162
	v_ashrrev_i32_e32 v145, 31, v144
	v_lshl_add_u32 v161, s52, 8, v157
	v_lshl_add_u64 v[144:145], v[144:145], 1, s[74:75]
	v_mad_i64_i32 v[168:169], s[52:53], v161, s11, v[144:145]
	s_waitcnt lgkmcnt(0)
	v_mov_b32_e32 v170, v165
	v_mov_b32_e32 v171, v166
	v_mov_b32_e32 v165, v167
	v_pk_add_f32 v[164:165], v[170:171], v[164:165]
	s_mov_b64 s[52:53], -1
	v_add_f32_e32 v163, v164, v165
	v_fmamk_f32 v163, v163, 0x3a800000, v198
	v_cmp_gt_f32_e32 vcc, s19, v163
	v_mul_f32_e32 v164, 0x4b800000, v163
	s_mov_b64 s[72:73], s[24:25]
	v_cndmask_b32_e32 v163, v163, v164, vcc
	v_rsq_f32_e32 v163, v163
	s_nop 0
	v_mul_f32_e32 v164, 0x45800000, v163
	v_cndmask_b32_e32 v164, v163, v164, vcc
	v_pk_mul_f32 v[126:127], v[126:127], v[164:165] op_sel_hi:[1,0]
	v_pk_mul_f32 v[124:125], v[124:125], v[164:165] op_sel_hi:[1,0]
	v_pk_mul_f32 v[166:167], v[122:123], v[164:165] op_sel_hi:[1,0]
	v_pk_mul_f32 v[122:123], v[120:121], v[164:165] op_sel_hi:[1,0]
	v_cvt_pk_bf16_f32 v120, v124, v125
	v_cvt_pk_bf16_f32 v121, v126, v127
	v_pk_mul_f32 v[116:117], v[116:117], v[164:165] op_sel_hi:[1,0]
	v_cvt_pk_bf16_f32 v122, v122, v123
	v_cvt_pk_bf16_f32 v123, v166, v167
	global_store_dwordx4 v[168:169], v[120:123], off
	v_pk_mul_f32 v[118:119], v[118:119], v[164:165] op_sel_hi:[1,0]
	s_nop 0
	v_pk_mul_f32 v[120:121], v[114:115], v[164:165] op_sel_hi:[1,0]
	v_pk_mul_f32 v[114:115], v[112:113], v[164:165] op_sel_hi:[1,0]
	v_cvt_pk_bf16_f32 v112, v116, v117
	v_cvt_pk_bf16_f32 v113, v118, v119
	s_nop 0
	v_cvt_pk_bf16_f32 v114, v114, v115
	v_cvt_pk_bf16_f32 v115, v120, v121
	global_store_dwordx4 v[168:169], v[112:115], off offset:256
	s_nop 1
	v_or_b32_e32 v112, 16, v161
	v_mad_i64_i32 v[116:117], s[8:9], v112, s11, v[144:145]
	ds_read_b128 v[112:115], v162 offset:256
	s_waitcnt lgkmcnt(0)
	v_mov_b32_e32 v118, v113
	v_mov_b32_e32 v119, v114
	v_mov_b32_e32 v113, v115
	v_pk_add_f32 v[112:113], v[118:119], v[112:113]
	s_nop 0
	v_add_f32_e32 v112, v112, v113
	v_fmamk_f32 v112, v112, 0x3a800000, v198
	v_cmp_gt_f32_e32 vcc, s19, v112
	v_mul_f32_e32 v113, 0x4b800000, v112
	s_nop 0
	v_cndmask_b32_e32 v112, v112, v113, vcc
	v_rsq_f32_e32 v112, v112
	s_nop 0
	v_mul_f32_e32 v113, 0x45800000, v112
	v_cndmask_b32_e32 v112, v112, v113, vcc
	v_pk_mul_f32 v[110:111], v[110:111], v[112:113] op_sel_hi:[1,0]
	v_pk_mul_f32 v[108:109], v[108:109], v[112:113] op_sel_hi:[1,0]
	v_pk_mul_f32 v[114:115], v[106:107], v[112:113] op_sel_hi:[1,0]
	v_pk_mul_f32 v[106:107], v[104:105], v[112:113] op_sel_hi:[1,0]
	v_cvt_pk_bf16_f32 v104, v108, v109
	v_cvt_pk_bf16_f32 v105, v110, v111
	v_pk_mul_f32 v[100:101], v[100:101], v[112:113] op_sel_hi:[1,0]
	v_cvt_pk_bf16_f32 v106, v106, v107
	v_cvt_pk_bf16_f32 v107, v114, v115
	global_store_dwordx4 v[116:117], v[104:107], off
	v_pk_mul_f32 v[102:103], v[102:103], v[112:113] op_sel_hi:[1,0]
	s_nop 0
	v_pk_mul_f32 v[104:105], v[98:99], v[112:113] op_sel_hi:[1,0]
	v_pk_mul_f32 v[98:99], v[96:97], v[112:113] op_sel_hi:[1,0]
	v_cvt_pk_bf16_f32 v96, v100, v101
	v_cvt_pk_bf16_f32 v97, v102, v103
	s_nop 0
	v_cvt_pk_bf16_f32 v98, v98, v99
	v_cvt_pk_bf16_f32 v99, v104, v105
	global_store_dwordx4 v[116:117], v[96:99], off offset:256
	s_nop 1
	v_or_b32_e32 v96, 32, v161
	v_mad_i64_i32 v[100:101], s[8:9], v96, s11, v[144:145]
	ds_read_b128 v[96:99], v162 offset:512
	s_waitcnt lgkmcnt(0)
	v_mov_b32_e32 v102, v97
	v_mov_b32_e32 v103, v98
	v_mov_b32_e32 v97, v99
	v_pk_add_f32 v[96:97], v[102:103], v[96:97]
	s_nop 0
	v_add_f32_e32 v96, v96, v97
	v_fmamk_f32 v96, v96, 0x3a800000, v198
	v_cmp_gt_f32_e32 vcc, s19, v96
	v_mul_f32_e32 v97, 0x4b800000, v96
	s_nop 0
	v_cndmask_b32_e32 v96, v96, v97, vcc
	v_rsq_f32_e32 v96, v96
	s_nop 0
	v_mul_f32_e32 v97, 0x45800000, v96
	v_cndmask_b32_e32 v96, v96, v97, vcc
	v_pk_mul_f32 v[94:95], v[94:95], v[96:97] op_sel_hi:[1,0]
	v_pk_mul_f32 v[92:93], v[92:93], v[96:97] op_sel_hi:[1,0]
	v_pk_mul_f32 v[98:99], v[90:91], v[96:97] op_sel_hi:[1,0]
	v_pk_mul_f32 v[90:91], v[88:89], v[96:97] op_sel_hi:[1,0]
	v_cvt_pk_bf16_f32 v88, v92, v93
	v_cvt_pk_bf16_f32 v89, v94, v95
	v_pk_mul_f32 v[84:85], v[84:85], v[96:97] op_sel_hi:[1,0]
	v_cvt_pk_bf16_f32 v90, v90, v91
	v_cvt_pk_bf16_f32 v91, v98, v99
	global_store_dwordx4 v[100:101], v[88:91], off
	v_pk_mul_f32 v[86:87], v[86:87], v[96:97] op_sel_hi:[1,0]
	s_nop 0
	v_pk_mul_f32 v[88:89], v[82:83], v[96:97] op_sel_hi:[1,0]
	v_pk_mul_f32 v[82:83], v[80:81], v[96:97] op_sel_hi:[1,0]
	v_cvt_pk_bf16_f32 v80, v84, v85
	v_cvt_pk_bf16_f32 v81, v86, v87
	s_nop 0
	v_cvt_pk_bf16_f32 v82, v82, v83
	v_cvt_pk_bf16_f32 v83, v88, v89
	global_store_dwordx4 v[100:101], v[80:83], off offset:256
	s_nop 1
	v_or_b32_e32 v80, 48, v161
	v_mad_i64_i32 v[84:85], s[8:9], v80, s11, v[144:145]
	ds_read_b128 v[80:83], v162 offset:768
	s_waitcnt lgkmcnt(0)
	v_mov_b32_e32 v86, v81
	v_mov_b32_e32 v87, v82
	v_mov_b32_e32 v81, v83
	v_pk_add_f32 v[80:81], v[86:87], v[80:81]
	s_nop 0
	v_add_f32_e32 v80, v80, v81
	v_fmamk_f32 v80, v80, 0x3a800000, v198
	v_cmp_gt_f32_e32 vcc, s19, v80
	v_mul_f32_e32 v81, 0x4b800000, v80
	s_nop 0
	v_cndmask_b32_e32 v80, v80, v81, vcc
	v_rsq_f32_e32 v80, v80
	s_nop 0
	v_mul_f32_e32 v81, 0x45800000, v80
	v_cndmask_b32_e32 v80, v80, v81, vcc
	v_pk_mul_f32 v[78:79], v[78:79], v[80:81] op_sel_hi:[1,0]
	v_pk_mul_f32 v[76:77], v[76:77], v[80:81] op_sel_hi:[1,0]
	v_pk_mul_f32 v[82:83], v[74:75], v[80:81] op_sel_hi:[1,0]
	v_pk_mul_f32 v[74:75], v[72:73], v[80:81] op_sel_hi:[1,0]
	v_cvt_pk_bf16_f32 v72, v76, v77
	v_cvt_pk_bf16_f32 v73, v78, v79
	v_pk_mul_f32 v[68:69], v[68:69], v[80:81] op_sel_hi:[1,0]
	v_cvt_pk_bf16_f32 v74, v74, v75
	v_cvt_pk_bf16_f32 v75, v82, v83
	global_store_dwordx4 v[84:85], v[72:75], off
	v_pk_mul_f32 v[70:71], v[70:71], v[80:81] op_sel_hi:[1,0]
	s_nop 0
	v_pk_mul_f32 v[72:73], v[66:67], v[80:81] op_sel_hi:[1,0]
	v_pk_mul_f32 v[66:67], v[64:65], v[80:81] op_sel_hi:[1,0]
	v_cvt_pk_bf16_f32 v64, v68, v69
	v_cvt_pk_bf16_f32 v65, v70, v71
	s_nop 0
	v_cvt_pk_bf16_f32 v66, v66, v67
	v_cvt_pk_bf16_f32 v67, v72, v73
	global_store_dwordx4 v[84:85], v[64:67], off offset:256
	s_nop 1
	v_add_u32_e32 v64, 0x80, v161
	v_mad_i64_i32 v[68:69], s[8:9], v64, s11, v[144:145]
	ds_read_b128 v[64:67], v162 offset:2048
	s_waitcnt lgkmcnt(0)
	v_mov_b32_e32 v70, v65
	v_mov_b32_e32 v71, v66
	v_mov_b32_e32 v65, v67
	v_pk_add_f32 v[64:65], v[70:71], v[64:65]
	s_nop 0
	v_add_f32_e32 v64, v64, v65
	v_fmamk_f32 v64, v64, 0x3a800000, v198
	v_cmp_gt_f32_e32 vcc, s19, v64
	v_mul_f32_e32 v65, 0x4b800000, v64
	s_nop 0
	v_cndmask_b32_e32 v64, v64, v65, vcc
	v_rsq_f32_e32 v64, v64
	s_nop 0
	v_mul_f32_e32 v65, 0x45800000, v64
	v_cndmask_b32_e32 v64, v64, v65, vcc
	v_pk_mul_f32 v[62:63], v[62:63], v[64:65] op_sel_hi:[1,0]
	v_pk_mul_f32 v[60:61], v[60:61], v[64:65] op_sel_hi:[1,0]
	v_pk_mul_f32 v[66:67], v[58:59], v[64:65] op_sel_hi:[1,0]
	v_pk_mul_f32 v[58:59], v[56:57], v[64:65] op_sel_hi:[1,0]
	v_cvt_pk_bf16_f32 v56, v60, v61
	v_cvt_pk_bf16_f32 v57, v62, v63
	v_pk_mul_f32 v[52:53], v[52:53], v[64:65] op_sel_hi:[1,0]
	v_cvt_pk_bf16_f32 v58, v58, v59
	v_cvt_pk_bf16_f32 v59, v66, v67
	global_store_dwordx4 v[68:69], v[56:59], off
	v_pk_mul_f32 v[54:55], v[54:55], v[64:65] op_sel_hi:[1,0]
	s_nop 0
	v_pk_mul_f32 v[56:57], v[50:51], v[64:65] op_sel_hi:[1,0]
	v_pk_mul_f32 v[50:51], v[48:49], v[64:65] op_sel_hi:[1,0]
	v_cvt_pk_bf16_f32 v48, v52, v53
	v_cvt_pk_bf16_f32 v49, v54, v55
	s_nop 0
	v_cvt_pk_bf16_f32 v50, v50, v51
	v_cvt_pk_bf16_f32 v51, v56, v57
	global_store_dwordx4 v[68:69], v[48:51], off offset:256
	s_nop 1
	v_add_u32_e32 v48, 0x90, v161
	v_mad_i64_i32 v[52:53], s[8:9], v48, s11, v[144:145]
	ds_read_b128 v[48:51], v162 offset:2304
	s_waitcnt lgkmcnt(0)
	v_mov_b32_e32 v54, v49
	v_mov_b32_e32 v55, v50
	v_mov_b32_e32 v49, v51
	v_pk_add_f32 v[48:49], v[54:55], v[48:49]
	s_nop 0
	v_add_f32_e32 v48, v48, v49
	v_fmamk_f32 v48, v48, 0x3a800000, v198
	v_cmp_gt_f32_e32 vcc, s19, v48
	v_mul_f32_e32 v49, 0x4b800000, v48
	s_nop 0
	v_cndmask_b32_e32 v48, v48, v49, vcc
	v_rsq_f32_e32 v48, v48
	s_nop 0
	v_mul_f32_e32 v49, 0x45800000, v48
	v_cndmask_b32_e32 v48, v48, v49, vcc
	v_pk_mul_f32 v[46:47], v[46:47], v[48:49] op_sel_hi:[1,0]
	v_pk_mul_f32 v[44:45], v[44:45], v[48:49] op_sel_hi:[1,0]
	v_pk_mul_f32 v[50:51], v[42:43], v[48:49] op_sel_hi:[1,0]
	v_pk_mul_f32 v[42:43], v[40:41], v[48:49] op_sel_hi:[1,0]
	v_cvt_pk_bf16_f32 v40, v44, v45
	v_cvt_pk_bf16_f32 v41, v46, v47
	v_pk_mul_f32 v[36:37], v[36:37], v[48:49] op_sel_hi:[1,0]
	v_cvt_pk_bf16_f32 v42, v42, v43
	v_cvt_pk_bf16_f32 v43, v50, v51
	global_store_dwordx4 v[52:53], v[40:43], off
	v_pk_mul_f32 v[38:39], v[38:39], v[48:49] op_sel_hi:[1,0]
	s_nop 0
	v_pk_mul_f32 v[40:41], v[34:35], v[48:49] op_sel_hi:[1,0]
	v_pk_mul_f32 v[34:35], v[32:33], v[48:49] op_sel_hi:[1,0]
	v_cvt_pk_bf16_f32 v32, v36, v37
	v_cvt_pk_bf16_f32 v33, v38, v39
	s_nop 0
	v_cvt_pk_bf16_f32 v34, v34, v35
	v_cvt_pk_bf16_f32 v35, v40, v41
	global_store_dwordx4 v[52:53], v[32:35], off offset:256
	s_nop 1
	v_add_u32_e32 v32, 0xa0, v161
	v_mad_i64_i32 v[36:37], s[8:9], v32, s11, v[144:145]
	ds_read_b128 v[32:35], v162 offset:2560
	s_waitcnt lgkmcnt(0)
	v_mov_b32_e32 v38, v33
	v_mov_b32_e32 v39, v34
	v_mov_b32_e32 v33, v35
	v_pk_add_f32 v[32:33], v[38:39], v[32:33]
	s_nop 0
	v_add_f32_e32 v32, v32, v33
	v_fmamk_f32 v32, v32, 0x3a800000, v198
	v_cmp_gt_f32_e32 vcc, s19, v32
	v_mul_f32_e32 v33, 0x4b800000, v32
	s_nop 0
	v_cndmask_b32_e32 v32, v32, v33, vcc
	v_rsq_f32_e32 v32, v32
	s_nop 0
	v_mul_f32_e32 v33, 0x45800000, v32
	v_cndmask_b32_e32 v32, v32, v33, vcc
	v_pk_mul_f32 v[30:31], v[30:31], v[32:33] op_sel_hi:[1,0]
	v_pk_mul_f32 v[28:29], v[28:29], v[32:33] op_sel_hi:[1,0]
	v_pk_mul_f32 v[34:35], v[26:27], v[32:33] op_sel_hi:[1,0]
	v_pk_mul_f32 v[26:27], v[24:25], v[32:33] op_sel_hi:[1,0]
	v_cvt_pk_bf16_f32 v24, v28, v29
	v_cvt_pk_bf16_f32 v25, v30, v31
	v_pk_mul_f32 v[20:21], v[20:21], v[32:33] op_sel_hi:[1,0]
	v_cvt_pk_bf16_f32 v26, v26, v27
	v_cvt_pk_bf16_f32 v27, v34, v35
	global_store_dwordx4 v[36:37], v[24:27], off
	v_pk_mul_f32 v[22:23], v[22:23], v[32:33] op_sel_hi:[1,0]
	s_nop 0
	v_pk_mul_f32 v[24:25], v[18:19], v[32:33] op_sel_hi:[1,0]
	v_pk_mul_f32 v[18:19], v[16:17], v[32:33] op_sel_hi:[1,0]
	v_cvt_pk_bf16_f32 v16, v20, v21
	v_cvt_pk_bf16_f32 v17, v22, v23
	s_nop 0
	v_cvt_pk_bf16_f32 v18, v18, v19
	v_cvt_pk_bf16_f32 v19, v24, v25
	global_store_dwordx4 v[36:37], v[16:19], off offset:256
	s_nop 1
	v_add_u32_e32 v16, 0xb0, v161
	v_mad_i64_i32 v[20:21], s[8:9], v16, s11, v[144:145]
	ds_read_b128 v[16:19], v162 offset:2816
	s_waitcnt lgkmcnt(0)
	v_mov_b32_e32 v22, v17
	v_mov_b32_e32 v23, v18
	v_mov_b32_e32 v17, v19
	v_pk_add_f32 v[16:17], v[22:23], v[16:17]
	s_nop 0
	v_add_f32_e32 v16, v16, v17
	v_fmamk_f32 v16, v16, 0x3a800000, v198
	v_cmp_gt_f32_e32 vcc, s19, v16
	v_mul_f32_e32 v17, 0x4b800000, v16
	s_nop 0
	v_cndmask_b32_e32 v16, v16, v17, vcc
	v_rsq_f32_e32 v16, v16
	s_nop 0
	v_mul_f32_e32 v17, 0x45800000, v16
	v_cndmask_b32_e32 v16, v16, v17, vcc
	v_pk_mul_f32 v[14:15], v[14:15], v[16:17] op_sel_hi:[1,0]
	v_pk_mul_f32 v[12:13], v[12:13], v[16:17] op_sel_hi:[1,0]
	v_pk_mul_f32 v[18:19], v[10:11], v[16:17] op_sel_hi:[1,0]
	v_pk_mul_f32 v[10:11], v[8:9], v[16:17] op_sel_hi:[1,0]
	v_cvt_pk_bf16_f32 v8, v12, v13
	v_cvt_pk_bf16_f32 v9, v14, v15
	s_andn2_b64 vcc, exec, s[46:47]
	v_cvt_pk_bf16_f32 v10, v10, v11
	v_cvt_pk_bf16_f32 v11, v18, v19
	global_store_dwordx4 v[20:21], v[8:11], off
	v_pk_mul_f32 v[6:7], v[6:7], v[16:17] op_sel_hi:[1,0]
	v_pk_mul_f32 v[4:5], v[4:5], v[16:17] op_sel_hi:[1,0]
	v_pk_mul_f32 v[8:9], v[2:3], v[16:17] op_sel_hi:[1,0]
	v_pk_mul_f32 v[2:3], v[0:1], v[16:17] op_sel_hi:[1,0]
	v_cvt_pk_bf16_f32 v0, v4, v5
	v_cvt_pk_bf16_f32 v1, v6, v7
	s_nop 0
	v_cvt_pk_bf16_f32 v2, v2, v3
	v_cvt_pk_bf16_f32 v3, v8, v9
	global_store_dwordx4 v[20:21], v[0:3], off offset:256
	s_cbranch_vccnz .LBB0_287
	s_andn2_b64 vcc, exec, s[20:21]
	s_cbranch_vccnz .LBB0_286
	s_barrier
	s_branch .LBB0_286

.LBB0_1439:
	s_or_b64 exec, exec, s[62:63]
	s_add_u32 s58, s58, 0x40080
	s_addc_u32 s59, s59, 0
	s_add_u32 s9, s60, 0x100
	v_mov_b32_e32 v0, 0
	s_addc_u32 s27, s61, 0
	s_mov_b32 s31, -2
	v_mov_b32_e32 v1, v0
	v_mov_b32_e32 v2, v0
	v_mov_b32_e32 v3, v0
	v_mov_b32_e32 v4, v0
	v_mov_b32_e32 v5, v0
	v_mov_b32_e32 v6, v0
	v_mov_b32_e32 v7, v0
	v_mov_b32_e32 v16, v0
	v_mov_b32_e32 v17, v0
	v_mov_b32_e32 v18, v0
	v_mov_b32_e32 v19, v0
	v_mov_b32_e32 v20, v0
	v_mov_b32_e32 v21, v0
	v_mov_b32_e32 v22, v0
	v_mov_b32_e32 v23, v0
	v_mov_b32_e32 v32, v0
	v_mov_b32_e32 v33, v0
	v_mov_b32_e32 v34, v0
	v_mov_b32_e32 v35, v0
	v_mov_b32_e32 v36, v0
	v_mov_b32_e32 v37, v0
	v_mov_b32_e32 v38, v0
	v_mov_b32_e32 v39, v0
	v_mov_b32_e32 v48, v0
	v_mov_b32_e32 v49, v0
	v_mov_b32_e32 v50, v0
	v_mov_b32_e32 v51, v0
	v_mov_b32_e32 v52, v0
	v_mov_b32_e32 v53, v0
	v_mov_b32_e32 v54, v0
	v_mov_b32_e32 v55, v0
	v_mov_b32_e32 v8, v0
	v_mov_b32_e32 v9, v0
	v_mov_b32_e32 v10, v0
	v_mov_b32_e32 v11, v0
	v_mov_b32_e32 v12, v0
	v_mov_b32_e32 v13, v0
	v_mov_b32_e32 v14, v0
	v_mov_b32_e32 v15, v0
	v_mov_b32_e32 v24, v0
	v_mov_b32_e32 v25, v0
	v_mov_b32_e32 v26, v0
	v_mov_b32_e32 v27, v0
	v_mov_b32_e32 v28, v0
	v_mov_b32_e32 v29, v0
	v_mov_b32_e32 v30, v0
	v_mov_b32_e32 v31, v0
	v_mov_b32_e32 v40, v0
	v_mov_b32_e32 v41, v0
	v_mov_b32_e32 v42, v0
	v_mov_b32_e32 v43, v0
	v_mov_b32_e32 v44, v0
	v_mov_b32_e32 v45, v0
	v_mov_b32_e32 v46, v0
	v_mov_b32_e32 v47, v0
	v_mov_b32_e32 v56, v0
	v_mov_b32_e32 v57, v0
	v_mov_b32_e32 v58, v0
	v_mov_b32_e32 v59, v0
	v_mov_b32_e32 v60, v0
	v_mov_b32_e32 v61, v0
	v_mov_b32_e32 v62, v0
	v_mov_b32_e32 v63, v0
	v_mov_b32_e32 v64, v0
	v_mov_b32_e32 v65, v0
	v_mov_b32_e32 v66, v0
	v_mov_b32_e32 v67, v0
	v_mov_b32_e32 v68, v0
	v_mov_b32_e32 v69, v0
	v_mov_b32_e32 v70, v0
	v_mov_b32_e32 v71, v0
	v_mov_b32_e32 v80, v0
	v_mov_b32_e32 v81, v0
	v_mov_b32_e32 v82, v0
	v_mov_b32_e32 v83, v0
	v_mov_b32_e32 v84, v0
	v_mov_b32_e32 v85, v0
	v_mov_b32_e32 v86, v0
	v_mov_b32_e32 v87, v0
	v_mov_b32_e32 v96, v0
	v_mov_b32_e32 v97, v0
	v_mov_b32_e32 v98, v0
	v_mov_b32_e32 v99, v0
	v_mov_b32_e32 v100, v0
	v_mov_b32_e32 v101, v0
	v_mov_b32_e32 v102, v0
	v_mov_b32_e32 v103, v0
	v_mov_b32_e32 v112, v0
	v_mov_b32_e32 v113, v0
	v_mov_b32_e32 v114, v0
	v_mov_b32_e32 v115, v0
	v_mov_b32_e32 v116, v0
	v_mov_b32_e32 v117, v0
	v_mov_b32_e32 v118, v0
	v_mov_b32_e32 v119, v0
	v_mov_b32_e32 v72, v0
	v_mov_b32_e32 v73, v0
	v_mov_b32_e32 v74, v0
	v_mov_b32_e32 v75, v0
	v_mov_b32_e32 v76, v0
	v_mov_b32_e32 v77, v0
	v_mov_b32_e32 v78, v0
	v_mov_b32_e32 v79, v0
	v_mov_b32_e32 v88, v0
	v_mov_b32_e32 v89, v0
	v_mov_b32_e32 v90, v0
	v_mov_b32_e32 v91, v0
	v_mov_b32_e32 v92, v0
	v_mov_b32_e32 v93, v0
	v_mov_b32_e32 v94, v0
	v_mov_b32_e32 v95, v0
	v_mov_b32_e32 v104, v0
	v_mov_b32_e32 v105, v0
	v_mov_b32_e32 v106, v0
	v_mov_b32_e32 v107, v0
	v_mov_b32_e32 v108, v0
	v_mov_b32_e32 v109, v0
	v_mov_b32_e32 v110, v0
	v_mov_b32_e32 v111, v0
	v_mov_b32_e32 v120, v0
	v_mov_b32_e32 v121, v0
	v_mov_b32_e32 v122, v0
	v_mov_b32_e32 v123, v0
	v_mov_b32_e32 v124, v0
	v_mov_b32_e32 v125, v0
	v_mov_b32_e32 v126, v0
	v_mov_b32_e32 v127, v0
	s_cmp_eq_u32 s8, 0
	s_cbranch_scc1 .LBB0_1440
	s_add_u32 s47, s58, 0xfffc0080
	s_addc_u32 s53, s59, -1
	s_add_i32 s55, 0, 0x10000
	s_cmp_eq_u32 s31, 12
	s_cselect_b32 s63, s49, s53
	s_cselect_b32 s62, s48, s47
	v_add_u32_e32 v150, s55, v153
	s_cselect_b32 s61, s51, s27
	s_cselect_b32 s60, s50, s9
	s_add_i32 s47, 0, 0x14000
	ds_read_b128 v[142:145], v150
	ds_read_b128 v[146:149], v150 offset:1024
	ds_read_b128 v[182:185], v150 offset:2048
	ds_read_b128 v[186:189], v150 offset:3072
	v_add_u32_e32 v150, s47, v153
	ds_read_b128 v[190:193], v150
	ds_read_b128 v[194:197], v150 offset:1024
	ds_read_b128 v[200:203], v150 offset:2048
	ds_read_b128 v[216:219], v150 offset:3072
	ds_read_b128 v[220:223], v165
	ds_read_b128 v[224:227], v165 offset:1024
	ds_read_b128 v[228:231], v165 offset:2048
	ds_read_b128 v[232:235], v165 offset:3072
	ds_read_b128 v[236:239], v165 offset:4096
	ds_read_b128 v[240:243], v165 offset:5120
	ds_read_b128 v[244:247], v165 offset:6144
	ds_read_b128 v[204:207], v165 offset:7168
	s_waitcnt vmcnt(24)
	s_waitcnt lgkmcnt(0)
	s_barrier
	s_setprio 1
	s_waitcnt lgkmcnt(0)
	v_mfma_f32_16x16x32_bf16 v[124:127], v[142:145], v[220:223], v[124:127]
	v_mfma_f32_16x16x32_bf16 v[120:123], v[182:185], v[220:223], v[120:123]
	v_mfma_f32_16x16x32_bf16 v[108:111], v[142:145], v[228:231], v[108:111]
	v_mfma_f32_16x16x32_bf16 v[104:107], v[182:185], v[228:231], v[104:107]
	v_mfma_f32_16x16x32_bf16 v[92:95], v[142:145], v[236:239], v[92:95]
	v_mfma_f32_16x16x32_bf16 v[88:91], v[182:185], v[236:239], v[88:91]
	v_mfma_f32_16x16x32_bf16 v[76:79], v[142:145], v[244:247], v[76:79]
	v_mfma_f32_16x16x32_bf16 v[72:75], v[182:185], v[244:247], v[72:75]
	v_mfma_f32_16x16x32_bf16 v[124:127], v[146:149], v[224:227], v[124:127]
	v_mfma_f32_16x16x32_bf16 v[120:123], v[186:189], v[224:227], v[120:123]
	v_mfma_f32_16x16x32_bf16 v[108:111], v[146:149], v[232:235], v[108:111]
	v_mfma_f32_16x16x32_bf16 v[104:107], v[186:189], v[232:235], v[104:107]
	v_mfma_f32_16x16x32_bf16 v[92:95], v[146:149], v[240:243], v[92:95]
	v_mfma_f32_16x16x32_bf16 v[88:91], v[186:189], v[240:243], v[88:91]
	v_mfma_f32_16x16x32_bf16 v[76:79], v[146:149], v[204:207], v[76:79]
	v_mfma_f32_16x16x32_bf16 v[72:75], v[186:189], v[204:207], v[72:75]
	s_setprio 0
	s_setprio 1
	v_mfma_f32_16x16x32_bf16 v[116:119], v[190:193], v[220:223], v[116:119]
	v_mfma_f32_16x16x32_bf16 v[112:115], v[200:203], v[220:223], v[112:115]
	v_mfma_f32_16x16x32_bf16 v[100:103], v[190:193], v[228:231], v[100:103]
	v_mfma_f32_16x16x32_bf16 v[96:99], v[200:203], v[228:231], v[96:99]
	v_mfma_f32_16x16x32_bf16 v[84:87], v[190:193], v[236:239], v[84:87]
	v_mfma_f32_16x16x32_bf16 v[80:83], v[200:203], v[236:239], v[80:83]
	v_mfma_f32_16x16x32_bf16 v[68:71], v[190:193], v[244:247], v[68:71]
	v_mfma_f32_16x16x32_bf16 v[64:67], v[200:203], v[244:247], v[64:67]
	v_mfma_f32_16x16x32_bf16 v[116:119], v[194:197], v[224:227], v[116:119]
	v_mfma_f32_16x16x32_bf16 v[112:115], v[216:219], v[224:227], v[112:115]
	v_mfma_f32_16x16x32_bf16 v[100:103], v[194:197], v[232:235], v[100:103]
	v_mfma_f32_16x16x32_bf16 v[96:99], v[216:219], v[232:235], v[96:99]
	v_mfma_f32_16x16x32_bf16 v[84:87], v[194:197], v[240:243], v[84:87]
	v_mfma_f32_16x16x32_bf16 v[80:83], v[216:219], v[240:243], v[80:83]
	v_mfma_f32_16x16x32_bf16 v[68:71], v[194:197], v[204:207], v[68:71]
	v_mfma_f32_16x16x32_bf16 v[64:67], v[216:219], v[204:207], v[64:67]
	s_setprio 0
	s_barrier
	s_add_i32 s53, s55, s0
	v_lshl_add_u64 v[150:151], s[60:61], 0, v[128:129]
	s_mov_b32 m0, s53
	ds_read_b128 v[204:207], v165 offset:16384
	ds_read_b128 v[220:223], v165 offset:17408
	ds_read_b128 v[224:227], v165 offset:18432
	ds_read_b128 v[228:231], v165 offset:19456
	ds_read_b128 v[232:235], v165 offset:20480
	ds_read_b128 v[236:239], v165 offset:21504
	ds_read_b128 v[240:243], v165 offset:22528
	ds_read_b128 v[244:247], v165 offset:23552
	global_load_lds_dwordx4 v[150:151], off
	s_add_i32 m0, s53, 0x2000
	s_add_u32 s70, s60, 0x40000
	v_lshl_add_u64 v[208:209], s[60:61], 0, v[134:135]
	s_addc_u32 s71, s61, 0
	s_add_i32 s47, s47, s0
	global_load_lds_dwordx4 v[208:209], off
	v_lshl_add_u64 v[248:249], s[70:71], 0, v[128:129]
	s_mov_b32 m0, s47
	v_lshl_add_u64 v[210:211], s[62:63], 0, v[132:133]
	global_load_lds_dwordx4 v[248:249], off
	v_lshl_add_u64 v[248:249], s[70:71], 0, v[134:135]
	s_add_i32 m0, s47, 0x2000
	s_nop 0
	global_load_lds_dwordx4 v[248:249], off
	v_lshl_add_u64 v[248:249], s[62:63], 0, v[130:131]
	s_mov_b32 m0, s1
	s_nop 0
	global_load_lds_dwordx4 v[248:249], off
	s_mov_b32 m0, s57
	s_nop 0
	global_load_lds_dwordx4 v[210:211], off
	s_waitcnt vmcnt(24)
	s_waitcnt lgkmcnt(0)
	s_barrier
	s_setprio 1
	s_waitcnt lgkmcnt(0)
	v_mfma_f32_16x16x32_bf16 v[60:63], v[142:145], v[204:207], v[60:63]
	v_mfma_f32_16x16x32_bf16 v[56:59], v[182:185], v[204:207], v[56:59]
	v_mfma_f32_16x16x32_bf16 v[44:47], v[142:145], v[224:227], v[44:47]
	v_mfma_f32_16x16x32_bf16 v[40:43], v[182:185], v[224:227], v[40:43]
	v_mfma_f32_16x16x32_bf16 v[28:31], v[142:145], v[232:235], v[28:31]
	v_mfma_f32_16x16x32_bf16 v[24:27], v[182:185], v[232:235], v[24:27]
	v_mfma_f32_16x16x32_bf16 v[12:15], v[142:145], v[240:243], v[12:15]
	v_mfma_f32_16x16x32_bf16 v[8:11], v[182:185], v[240:243], v[8:11]
	v_mfma_f32_16x16x32_bf16 v[60:63], v[146:149], v[220:223], v[60:63]
	v_mfma_f32_16x16x32_bf16 v[56:59], v[186:189], v[220:223], v[56:59]
	v_mfma_f32_16x16x32_bf16 v[44:47], v[146:149], v[228:231], v[44:47]
	v_mfma_f32_16x16x32_bf16 v[40:43], v[186:189], v[228:231], v[40:43]
	v_mfma_f32_16x16x32_bf16 v[28:31], v[146:149], v[236:239], v[28:31]
	v_mfma_f32_16x16x32_bf16 v[24:27], v[186:189], v[236:239], v[24:27]
	v_mfma_f32_16x16x32_bf16 v[12:15], v[146:149], v[244:247], v[12:15]
	v_mfma_f32_16x16x32_bf16 v[8:11], v[186:189], v[244:247], v[8:11]
	s_setprio 0
	s_setprio 1
	v_mfma_f32_16x16x32_bf16 v[52:55], v[190:193], v[204:207], v[52:55]
	v_mfma_f32_16x16x32_bf16 v[48:51], v[200:203], v[204:207], v[48:51]
	v_mfma_f32_16x16x32_bf16 v[36:39], v[190:193], v[224:227], v[36:39]
	v_mfma_f32_16x16x32_bf16 v[32:35], v[200:203], v[224:227], v[32:35]
	v_mfma_f32_16x16x32_bf16 v[20:23], v[190:193], v[232:235], v[20:23]
	v_mfma_f32_16x16x32_bf16 v[16:19], v[200:203], v[232:235], v[16:19]
	v_mfma_f32_16x16x32_bf16 v[4:7], v[190:193], v[240:243], v[4:7]
	v_mfma_f32_16x16x32_bf16 v[0:3], v[200:203], v[240:243], v[0:3]
	v_mfma_f32_16x16x32_bf16 v[52:55], v[194:197], v[220:223], v[52:55]
	v_mfma_f32_16x16x32_bf16 v[48:51], v[216:219], v[220:223], v[48:51]
	v_mfma_f32_16x16x32_bf16 v[36:39], v[194:197], v[228:231], v[36:39]
	v_mfma_f32_16x16x32_bf16 v[32:35], v[216:219], v[228:231], v[32:35]
	v_mfma_f32_16x16x32_bf16 v[20:23], v[194:197], v[236:239], v[20:23]
	v_mfma_f32_16x16x32_bf16 v[16:19], v[216:219], v[236:239], v[16:19]
	v_mfma_f32_16x16x32_bf16 v[4:7], v[194:197], v[244:247], v[4:7]
	v_mfma_f32_16x16x32_bf16 v[0:3], v[216:219], v[244:247], v[0:3]
	s_setprio 0
	s_barrier
	s_add_i32 s47, 0, 0x18000
	v_add_u32_e32 v181, s47, v153
	s_add_i32 s53, 0, 0x1c000
	ds_read_b128 v[142:145], v181
	ds_read_b128 v[146:149], v181 offset:1024
	ds_read_b128 v[182:185], v181 offset:2048
	ds_read_b128 v[186:189], v181 offset:3072
	v_add_u32_e32 v181, s53, v153
	ds_read_b128 v[190:193], v181
	ds_read_b128 v[194:197], v181 offset:1024
	ds_read_b128 v[200:203], v181 offset:2048
	ds_read_b128 v[204:207], v181 offset:3072
	s_add_u32 s62, s62, 0x40000
	s_addc_u32 s63, s63, 0
	s_mov_b32 m0, s64
	v_lshl_add_u64 v[214:215], s[62:63], 0, v[130:131]
	ds_read_b128 v[216:219], v165 offset:32768
	ds_read_b128 v[220:223], v165 offset:33792
	ds_read_b128 v[224:227], v165 offset:34816
	ds_read_b128 v[228:231], v165 offset:35840
	ds_read_b128 v[232:235], v165 offset:36864
	ds_read_b128 v[236:239], v165 offset:37888
	ds_read_b128 v[240:243], v165 offset:38912
	ds_read_b128 v[244:247], v165 offset:39936
	global_load_lds_dwordx4 v[214:215], off
	v_lshl_add_u64 v[214:215], s[62:63], 0, v[132:133]
	s_mov_b32 m0, s65
	s_nop 0
	global_load_lds_dwordx4 v[214:215], off
	s_waitcnt vmcnt(24)
	s_waitcnt lgkmcnt(0)
	s_barrier
	s_setprio 1
	s_waitcnt lgkmcnt(0)
	v_mfma_f32_16x16x32_bf16 v[124:127], v[142:145], v[216:219], v[124:127]
	v_mfma_f32_16x16x32_bf16 v[120:123], v[182:185], v[216:219], v[120:123]
	v_mfma_f32_16x16x32_bf16 v[108:111], v[142:145], v[224:227], v[108:111]
	v_mfma_f32_16x16x32_bf16 v[104:107], v[182:185], v[224:227], v[104:107]
	v_mfma_f32_16x16x32_bf16 v[92:95], v[142:145], v[232:235], v[92:95]
	v_mfma_f32_16x16x32_bf16 v[88:91], v[182:185], v[232:235], v[88:91]
	v_mfma_f32_16x16x32_bf16 v[76:79], v[142:145], v[240:243], v[76:79]
	v_mfma_f32_16x16x32_bf16 v[72:75], v[182:185], v[240:243], v[72:75]
	v_mfma_f32_16x16x32_bf16 v[124:127], v[146:149], v[220:223], v[124:127]
	v_mfma_f32_16x16x32_bf16 v[120:123], v[186:189], v[220:223], v[120:123]
	v_mfma_f32_16x16x32_bf16 v[108:111], v[146:149], v[228:231], v[108:111]
	v_mfma_f32_16x16x32_bf16 v[104:107], v[186:189], v[228:231], v[104:107]
	v_mfma_f32_16x16x32_bf16 v[92:95], v[146:149], v[236:239], v[92:95]
	v_mfma_f32_16x16x32_bf16 v[88:91], v[186:189], v[236:239], v[88:91]
	v_mfma_f32_16x16x32_bf16 v[76:79], v[146:149], v[244:247], v[76:79]
	v_mfma_f32_16x16x32_bf16 v[72:75], v[186:189], v[244:247], v[72:75]
	s_setprio 0
	s_setprio 1
	v_mfma_f32_16x16x32_bf16 v[116:119], v[190:193], v[216:219], v[116:119]
	v_mfma_f32_16x16x32_bf16 v[112:115], v[200:203], v[216:219], v[112:115]
	v_mfma_f32_16x16x32_bf16 v[100:103], v[190:193], v[224:227], v[100:103]
	v_mfma_f32_16x16x32_bf16 v[96:99], v[200:203], v[224:227], v[96:99]
	v_mfma_f32_16x16x32_bf16 v[84:87], v[190:193], v[232:235], v[84:87]
	v_mfma_f32_16x16x32_bf16 v[80:83], v[200:203], v[232:235], v[80:83]
	v_mfma_f32_16x16x32_bf16 v[68:71], v[190:193], v[240:243], v[68:71]
	v_mfma_f32_16x16x32_bf16 v[64:67], v[200:203], v[240:243], v[64:67]
	v_mfma_f32_16x16x32_bf16 v[116:119], v[194:197], v[220:223], v[116:119]
	v_mfma_f32_16x16x32_bf16 v[112:115], v[204:207], v[220:223], v[112:115]
	v_mfma_f32_16x16x32_bf16 v[100:103], v[194:197], v[228:231], v[100:103]
	v_mfma_f32_16x16x32_bf16 v[96:99], v[204:207], v[228:231], v[96:99]
	v_mfma_f32_16x16x32_bf16 v[84:87], v[194:197], v[236:239], v[84:87]
	v_mfma_f32_16x16x32_bf16 v[80:83], v[204:207], v[236:239], v[80:83]
	v_mfma_f32_16x16x32_bf16 v[68:71], v[194:197], v[244:247], v[68:71]
	v_mfma_f32_16x16x32_bf16 v[64:67], v[204:207], v[244:247], v[64:67]
	s_setprio 0
	s_barrier
	s_branch .Lp8_q3
.LBB0_1440:
	s_add_u32 s47, s58, 0xfffc0080
	s_addc_u32 s53, s59, -1
	s_add_i32 s55, 0, 0x10000
	s_cmp_eq_u32 s31, 12
	s_cselect_b32 s63, s49, s53
	s_cselect_b32 s62, s48, s47
	v_add_u32_e32 v150, s55, v153
	s_cselect_b32 s61, s51, s27
	s_cselect_b32 s60, s50, s9
	s_add_i32 s47, 0, 0x14000
	ds_read_b128 v[142:145], v150
	ds_read_b128 v[146:149], v150 offset:1024
	ds_read_b128 v[182:185], v150 offset:2048
	ds_read_b128 v[186:189], v150 offset:3072
	v_add_u32_e32 v150, s47, v153
	ds_read_b128 v[190:193], v150
	ds_read_b128 v[194:197], v150 offset:1024
	ds_read_b128 v[200:203], v150 offset:2048
	ds_read_b128 v[216:219], v150 offset:3072
	v_lshl_add_u64 v[150:151], s[58:59], 0, v[138:139]
	s_add_i32 m0, s1, 0xc000
	ds_read_b128 v[220:223], v165
	ds_read_b128 v[224:227], v165 offset:1024
	ds_read_b128 v[228:231], v165 offset:2048
	ds_read_b128 v[232:235], v165 offset:3072
	ds_read_b128 v[236:239], v165 offset:4096
	ds_read_b128 v[240:243], v165 offset:5120
	ds_read_b128 v[244:247], v165 offset:6144
	ds_read_b128 v[204:207], v165 offset:7168
	global_load_lds_dwordx4 v[150:151], off
	v_lshl_add_u64 v[150:151], s[58:59], 0, v[140:141]
	s_add_i32 m0, s1, 0xe000
	s_nop 0
	global_load_lds_dwordx4 v[150:151], off
	s_waitcnt vmcnt(8)
	s_waitcnt lgkmcnt(0)
	s_barrier
	s_setprio 1
	s_waitcnt lgkmcnt(0)
	v_mfma_f32_16x16x32_bf16 v[124:127], v[142:145], v[220:223], v[124:127]
	v_mfma_f32_16x16x32_bf16 v[120:123], v[182:185], v[220:223], v[120:123]
	v_mfma_f32_16x16x32_bf16 v[108:111], v[142:145], v[228:231], v[108:111]
	v_mfma_f32_16x16x32_bf16 v[104:107], v[182:185], v[228:231], v[104:107]
	v_mfma_f32_16x16x32_bf16 v[92:95], v[142:145], v[236:239], v[92:95]
	v_mfma_f32_16x16x32_bf16 v[88:91], v[182:185], v[236:239], v[88:91]
	v_mfma_f32_16x16x32_bf16 v[76:79], v[142:145], v[244:247], v[76:79]
	v_mfma_f32_16x16x32_bf16 v[72:75], v[182:185], v[244:247], v[72:75]
	v_mfma_f32_16x16x32_bf16 v[124:127], v[146:149], v[224:227], v[124:127]
	v_mfma_f32_16x16x32_bf16 v[120:123], v[186:189], v[224:227], v[120:123]
	v_mfma_f32_16x16x32_bf16 v[108:111], v[146:149], v[232:235], v[108:111]
	v_mfma_f32_16x16x32_bf16 v[104:107], v[186:189], v[232:235], v[104:107]
	v_mfma_f32_16x16x32_bf16 v[92:95], v[146:149], v[240:243], v[92:95]
	v_mfma_f32_16x16x32_bf16 v[88:91], v[186:189], v[240:243], v[88:91]
	v_mfma_f32_16x16x32_bf16 v[76:79], v[146:149], v[204:207], v[76:79]
	v_mfma_f32_16x16x32_bf16 v[72:75], v[186:189], v[204:207], v[72:75]
	s_setprio 0
	s_setprio 1
	v_mfma_f32_16x16x32_bf16 v[116:119], v[190:193], v[220:223], v[116:119]
	v_mfma_f32_16x16x32_bf16 v[112:115], v[200:203], v[220:223], v[112:115]
	v_mfma_f32_16x16x32_bf16 v[100:103], v[190:193], v[228:231], v[100:103]
	v_mfma_f32_16x16x32_bf16 v[96:99], v[200:203], v[228:231], v[96:99]
	v_mfma_f32_16x16x32_bf16 v[84:87], v[190:193], v[236:239], v[84:87]
	v_mfma_f32_16x16x32_bf16 v[80:83], v[200:203], v[236:239], v[80:83]
	v_mfma_f32_16x16x32_bf16 v[68:71], v[190:193], v[244:247], v[68:71]
	v_mfma_f32_16x16x32_bf16 v[64:67], v[200:203], v[244:247], v[64:67]
	v_mfma_f32_16x16x32_bf16 v[116:119], v[194:197], v[224:227], v[116:119]
	v_mfma_f32_16x16x32_bf16 v[112:115], v[216:219], v[224:227], v[112:115]
	v_mfma_f32_16x16x32_bf16 v[100:103], v[194:197], v[232:235], v[100:103]
	v_mfma_f32_16x16x32_bf16 v[96:99], v[216:219], v[232:235], v[96:99]
	v_mfma_f32_16x16x32_bf16 v[84:87], v[194:197], v[240:243], v[84:87]
	v_mfma_f32_16x16x32_bf16 v[80:83], v[216:219], v[240:243], v[80:83]
	v_mfma_f32_16x16x32_bf16 v[68:71], v[194:197], v[204:207], v[68:71]
	v_mfma_f32_16x16x32_bf16 v[64:67], v[216:219], v[204:207], v[64:67]
	s_setprio 0
	s_barrier
	s_add_i32 s53, s55, s0
	v_lshl_add_u64 v[150:151], s[60:61], 0, v[128:129]
	s_mov_b32 m0, s53
	ds_read_b128 v[204:207], v165 offset:16384
	ds_read_b128 v[220:223], v165 offset:17408
	ds_read_b128 v[224:227], v165 offset:18432
	ds_read_b128 v[228:231], v165 offset:19456
	ds_read_b128 v[232:235], v165 offset:20480
	ds_read_b128 v[236:239], v165 offset:21504
	ds_read_b128 v[240:243], v165 offset:22528
	ds_read_b128 v[244:247], v165 offset:23552
	global_load_lds_dwordx4 v[150:151], off
	s_add_i32 m0, s53, 0x2000
	s_add_u32 s70, s60, 0x40000
	v_lshl_add_u64 v[208:209], s[60:61], 0, v[134:135]
	s_addc_u32 s71, s61, 0
	s_add_i32 s47, s47, s0
	global_load_lds_dwordx4 v[208:209], off
	v_lshl_add_u64 v[248:249], s[70:71], 0, v[128:129]
	s_mov_b32 m0, s47
	v_lshl_add_u64 v[210:211], s[62:63], 0, v[132:133]
	global_load_lds_dwordx4 v[248:249], off
	v_lshl_add_u64 v[248:249], s[70:71], 0, v[134:135]
	s_add_i32 m0, s47, 0x2000
	s_nop 0
	global_load_lds_dwordx4 v[248:249], off
	v_lshl_add_u64 v[248:249], s[62:63], 0, v[130:131]
	s_mov_b32 m0, s1
	s_nop 0
	global_load_lds_dwordx4 v[248:249], off
	s_mov_b32 m0, s57
	s_nop 0
	global_load_lds_dwordx4 v[210:211], off
	s_waitcnt vmcnt(8)
	s_waitcnt lgkmcnt(0)
	s_barrier
	s_setprio 1
	s_waitcnt lgkmcnt(0)
	v_mfma_f32_16x16x32_bf16 v[60:63], v[142:145], v[204:207], v[60:63]
	v_mfma_f32_16x16x32_bf16 v[56:59], v[182:185], v[204:207], v[56:59]
	v_mfma_f32_16x16x32_bf16 v[44:47], v[142:145], v[224:227], v[44:47]
	v_mfma_f32_16x16x32_bf16 v[40:43], v[182:185], v[224:227], v[40:43]
	v_mfma_f32_16x16x32_bf16 v[28:31], v[142:145], v[232:235], v[28:31]
	v_mfma_f32_16x16x32_bf16 v[24:27], v[182:185], v[232:235], v[24:27]
	v_mfma_f32_16x16x32_bf16 v[12:15], v[142:145], v[240:243], v[12:15]
	v_mfma_f32_16x16x32_bf16 v[8:11], v[182:185], v[240:243], v[8:11]
	v_mfma_f32_16x16x32_bf16 v[60:63], v[146:149], v[220:223], v[60:63]
	v_mfma_f32_16x16x32_bf16 v[56:59], v[186:189], v[220:223], v[56:59]
	v_mfma_f32_16x16x32_bf16 v[44:47], v[146:149], v[228:231], v[44:47]
	v_mfma_f32_16x16x32_bf16 v[40:43], v[186:189], v[228:231], v[40:43]
	v_mfma_f32_16x16x32_bf16 v[28:31], v[146:149], v[236:239], v[28:31]
	v_mfma_f32_16x16x32_bf16 v[24:27], v[186:189], v[236:239], v[24:27]
	v_mfma_f32_16x16x32_bf16 v[12:15], v[146:149], v[244:247], v[12:15]
	v_mfma_f32_16x16x32_bf16 v[8:11], v[186:189], v[244:247], v[8:11]
	s_setprio 0
	s_setprio 1
	v_mfma_f32_16x16x32_bf16 v[52:55], v[190:193], v[204:207], v[52:55]
	v_mfma_f32_16x16x32_bf16 v[48:51], v[200:203], v[204:207], v[48:51]
	v_mfma_f32_16x16x32_bf16 v[36:39], v[190:193], v[224:227], v[36:39]
	v_mfma_f32_16x16x32_bf16 v[32:35], v[200:203], v[224:227], v[32:35]
	v_mfma_f32_16x16x32_bf16 v[20:23], v[190:193], v[232:235], v[20:23]
	v_mfma_f32_16x16x32_bf16 v[16:19], v[200:203], v[232:235], v[16:19]
	v_mfma_f32_16x16x32_bf16 v[4:7], v[190:193], v[240:243], v[4:7]
	v_mfma_f32_16x16x32_bf16 v[0:3], v[200:203], v[240:243], v[0:3]
	v_mfma_f32_16x16x32_bf16 v[52:55], v[194:197], v[220:223], v[52:55]
	v_mfma_f32_16x16x32_bf16 v[48:51], v[216:219], v[220:223], v[48:51]
	v_mfma_f32_16x16x32_bf16 v[36:39], v[194:197], v[228:231], v[36:39]
	v_mfma_f32_16x16x32_bf16 v[32:35], v[216:219], v[228:231], v[32:35]
	v_mfma_f32_16x16x32_bf16 v[20:23], v[194:197], v[236:239], v[20:23]
	v_mfma_f32_16x16x32_bf16 v[16:19], v[216:219], v[236:239], v[16:19]
	v_mfma_f32_16x16x32_bf16 v[4:7], v[194:197], v[244:247], v[4:7]
	v_mfma_f32_16x16x32_bf16 v[0:3], v[216:219], v[244:247], v[0:3]
	s_setprio 0
	s_barrier
	s_add_i32 s47, 0, 0x18000
	v_add_u32_e32 v181, s47, v153
	s_add_i32 s53, 0, 0x1c000
	ds_read_b128 v[142:145], v181
	ds_read_b128 v[146:149], v181 offset:1024
	ds_read_b128 v[182:185], v181 offset:2048
	ds_read_b128 v[186:189], v181 offset:3072
	v_add_u32_e32 v181, s53, v153
	ds_read_b128 v[190:193], v181
	ds_read_b128 v[194:197], v181 offset:1024
	ds_read_b128 v[200:203], v181 offset:2048
	ds_read_b128 v[204:207], v181 offset:3072
	s_add_u32 s62, s62, 0x40000
	s_addc_u32 s63, s63, 0
	s_mov_b32 m0, s64
	v_lshl_add_u64 v[214:215], s[62:63], 0, v[130:131]
	ds_read_b128 v[216:219], v165 offset:32768
	ds_read_b128 v[220:223], v165 offset:33792
	ds_read_b128 v[224:227], v165 offset:34816
	ds_read_b128 v[228:231], v165 offset:35840
	ds_read_b128 v[232:235], v165 offset:36864
	ds_read_b128 v[236:239], v165 offset:37888
	ds_read_b128 v[240:243], v165 offset:38912
	ds_read_b128 v[244:247], v165 offset:39936
	global_load_lds_dwordx4 v[214:215], off
	v_lshl_add_u64 v[214:215], s[62:63], 0, v[132:133]
	s_mov_b32 m0, s65
	s_nop 0
	global_load_lds_dwordx4 v[214:215], off
	s_waitcnt vmcnt(8)
	s_waitcnt lgkmcnt(0)
	s_barrier
	s_setprio 1
	s_waitcnt lgkmcnt(0)
	v_mfma_f32_16x16x32_bf16 v[124:127], v[142:145], v[216:219], v[124:127]
	v_mfma_f32_16x16x32_bf16 v[120:123], v[182:185], v[216:219], v[120:123]
	v_mfma_f32_16x16x32_bf16 v[108:111], v[142:145], v[224:227], v[108:111]
	v_mfma_f32_16x16x32_bf16 v[104:107], v[182:185], v[224:227], v[104:107]
	v_mfma_f32_16x16x32_bf16 v[92:95], v[142:145], v[232:235], v[92:95]
	v_mfma_f32_16x16x32_bf16 v[88:91], v[182:185], v[232:235], v[88:91]
	v_mfma_f32_16x16x32_bf16 v[76:79], v[142:145], v[240:243], v[76:79]
	v_mfma_f32_16x16x32_bf16 v[72:75], v[182:185], v[240:243], v[72:75]
	v_mfma_f32_16x16x32_bf16 v[124:127], v[146:149], v[220:223], v[124:127]
	v_mfma_f32_16x16x32_bf16 v[120:123], v[186:189], v[220:223], v[120:123]
	v_mfma_f32_16x16x32_bf16 v[108:111], v[146:149], v[228:231], v[108:111]
	v_mfma_f32_16x16x32_bf16 v[104:107], v[186:189], v[228:231], v[104:107]
	v_mfma_f32_16x16x32_bf16 v[92:95], v[146:149], v[236:239], v[92:95]
	v_mfma_f32_16x16x32_bf16 v[88:91], v[186:189], v[236:239], v[88:91]
	v_mfma_f32_16x16x32_bf16 v[76:79], v[146:149], v[244:247], v[76:79]
	v_mfma_f32_16x16x32_bf16 v[72:75], v[186:189], v[244:247], v[72:75]
	s_setprio 0
	s_setprio 1
	v_mfma_f32_16x16x32_bf16 v[116:119], v[190:193], v[216:219], v[116:119]
	v_mfma_f32_16x16x32_bf16 v[112:115], v[200:203], v[216:219], v[112:115]
	v_mfma_f32_16x16x32_bf16 v[100:103], v[190:193], v[224:227], v[100:103]
	v_mfma_f32_16x16x32_bf16 v[96:99], v[200:203], v[224:227], v[96:99]
	v_mfma_f32_16x16x32_bf16 v[84:87], v[190:193], v[232:235], v[84:87]
	v_mfma_f32_16x16x32_bf16 v[80:83], v[200:203], v[232:235], v[80:83]
	v_mfma_f32_16x16x32_bf16 v[68:71], v[190:193], v[240:243], v[68:71]
	v_mfma_f32_16x16x32_bf16 v[64:67], v[200:203], v[240:243], v[64:67]
	v_mfma_f32_16x16x32_bf16 v[116:119], v[194:197], v[220:223], v[116:119]
	v_mfma_f32_16x16x32_bf16 v[112:115], v[204:207], v[220:223], v[112:115]
	v_mfma_f32_16x16x32_bf16 v[100:103], v[194:197], v[228:231], v[100:103]
	v_mfma_f32_16x16x32_bf16 v[96:99], v[204:207], v[228:231], v[96:99]
	v_mfma_f32_16x16x32_bf16 v[84:87], v[194:197], v[236:239], v[84:87]
	v_mfma_f32_16x16x32_bf16 v[80:83], v[204:207], v[236:239], v[80:83]
	v_mfma_f32_16x16x32_bf16 v[68:71], v[194:197], v[244:247], v[68:71]
	v_mfma_f32_16x16x32_bf16 v[64:67], v[204:207], v[244:247], v[64:67]
	s_setprio 0
	s_barrier
.Lp8_q3:
	s_add_i32 s47, s47, s0
	v_lshl_add_u64 v[150:151], v[150:151], 0, s[88:89]
	s_mov_b32 m0, s47
	ds_read_b128 v[216:219], v165 offset:49152
	ds_read_b128 v[220:223], v165 offset:50176
	ds_read_b128 v[224:227], v165 offset:51200
	ds_read_b128 v[228:231], v165 offset:52224
	ds_read_b128 v[232:235], v165 offset:53248
	ds_read_b128 v[236:239], v165 offset:54272
	ds_read_b128 v[240:243], v165 offset:55296
	ds_read_b128 v[244:247], v165 offset:56320
	global_load_lds_dwordx4 v[150:151], off
	s_add_i32 m0, s47, 0x2000
	s_add_u32 s60, s60, 0x40080
	v_lshl_add_u64 v[150:151], v[208:209], 0, s[88:89]
	s_addc_u32 s61, s61, 0
	s_add_i32 s47, s53, s0
	global_load_lds_dwordx4 v[150:151], off
	v_lshl_add_u64 v[150:151], s[60:61], 0, v[128:129]
	s_mov_b32 m0, s47
	s_nop 0
	global_load_lds_dwordx4 v[150:151], off
	v_lshl_add_u64 v[150:151], s[60:61], 0, v[134:135]
	s_add_i32 m0, s47, 0x2000
	s_nop 0
	global_load_lds_dwordx4 v[150:151], off
	v_lshl_add_u64 v[150:151], v[248:249], 0, s[88:89]
	s_mov_b32 m0, s67
	s_nop 0
	global_load_lds_dwordx4 v[150:151], off
	v_lshl_add_u64 v[150:151], v[210:211], 0, s[88:89]
	s_mov_b32 m0, s68
	s_nop 0
	global_load_lds_dwordx4 v[150:151], off
	s_waitcnt vmcnt(8)
	s_waitcnt lgkmcnt(0)
	s_barrier
	s_setprio 1
	s_waitcnt lgkmcnt(0)
	v_mfma_f32_16x16x32_bf16 v[60:63], v[142:145], v[216:219], v[60:63]
	v_mfma_f32_16x16x32_bf16 v[56:59], v[182:185], v[216:219], v[56:59]
	v_mfma_f32_16x16x32_bf16 v[44:47], v[142:145], v[224:227], v[44:47]
	v_mfma_f32_16x16x32_bf16 v[40:43], v[182:185], v[224:227], v[40:43]
	v_mfma_f32_16x16x32_bf16 v[28:31], v[142:145], v[232:235], v[28:31]
	v_mfma_f32_16x16x32_bf16 v[24:27], v[182:185], v[232:235], v[24:27]
	v_mfma_f32_16x16x32_bf16 v[12:15], v[142:145], v[240:243], v[12:15]
	v_mfma_f32_16x16x32_bf16 v[8:11], v[182:185], v[240:243], v[8:11]
	v_mfma_f32_16x16x32_bf16 v[60:63], v[146:149], v[220:223], v[60:63]
	v_mfma_f32_16x16x32_bf16 v[56:59], v[186:189], v[220:223], v[56:59]
	v_mfma_f32_16x16x32_bf16 v[44:47], v[146:149], v[228:231], v[44:47]
	v_mfma_f32_16x16x32_bf16 v[40:43], v[186:189], v[228:231], v[40:43]
	v_mfma_f32_16x16x32_bf16 v[28:31], v[146:149], v[236:239], v[28:31]
	v_mfma_f32_16x16x32_bf16 v[24:27], v[186:189], v[236:239], v[24:27]
	v_mfma_f32_16x16x32_bf16 v[12:15], v[146:149], v[244:247], v[12:15]
	v_mfma_f32_16x16x32_bf16 v[8:11], v[186:189], v[244:247], v[8:11]
	s_setprio 0
	s_setprio 1
	v_mfma_f32_16x16x32_bf16 v[52:55], v[190:193], v[216:219], v[52:55]
	v_mfma_f32_16x16x32_bf16 v[48:51], v[200:203], v[216:219], v[48:51]
	v_mfma_f32_16x16x32_bf16 v[36:39], v[190:193], v[224:227], v[36:39]
	v_mfma_f32_16x16x32_bf16 v[32:35], v[200:203], v[224:227], v[32:35]
	v_mfma_f32_16x16x32_bf16 v[20:23], v[190:193], v[232:235], v[20:23]
	v_mfma_f32_16x16x32_bf16 v[16:19], v[200:203], v[232:235], v[16:19]
	v_mfma_f32_16x16x32_bf16 v[4:7], v[190:193], v[240:243], v[4:7]
	v_mfma_f32_16x16x32_bf16 v[0:3], v[200:203], v[240:243], v[0:3]
	v_mfma_f32_16x16x32_bf16 v[52:55], v[194:197], v[220:223], v[52:55]
	v_mfma_f32_16x16x32_bf16 v[48:51], v[204:207], v[220:223], v[48:51]
	v_mfma_f32_16x16x32_bf16 v[36:39], v[194:197], v[228:231], v[36:39]
	v_mfma_f32_16x16x32_bf16 v[32:35], v[204:207], v[228:231], v[32:35]
	v_mfma_f32_16x16x32_bf16 v[20:23], v[194:197], v[236:239], v[20:23]
	v_mfma_f32_16x16x32_bf16 v[16:19], v[204:207], v[236:239], v[16:19]
	v_mfma_f32_16x16x32_bf16 v[4:7], v[194:197], v[244:247], v[4:7]
	v_mfma_f32_16x16x32_bf16 v[0:3], v[204:207], v[244:247], v[0:3]
	s_setprio 0
	s_barrier
	s_add_i32 s31, s31, 2
	s_add_u32 s58, s58, 0x100
	s_addc_u32 s59, s59, 0
	s_add_u32 s9, s9, 0x100
	s_addc_u32 s27, s27, 0
	s_cmp_gt_u32 s31, 13
	s_cbranch_scc0 .LBB0_1440
	s_and_b64 vcc, exec, s[22:23]
	s_cbranch_vccz .LBB0_1443
	s_barrier
.LBB0_1443:
	s_add_u32 s100, s48, 0x40080
	s_addc_u32 s101, s49, 0
	v_lshl_add_u64 v[150:151], s[100:101], 0, v[138:139]
	s_add_i32 m0, s1, 0xc000
	s_nop 0
	global_load_lds_dwordx4 v[150:151], off
	v_lshl_add_u64 v[150:151], s[100:101], 0, v[140:141]
	s_add_i32 m0, s1, 0xe000
	s_nop 0
	global_load_lds_dwordx4 v[150:151], off
	s_lshl_b32 s8, s8, 12
	s_and_b32 s8, s8, 0x1000
	v_add_u32_e32 v144, s8, v164
	ds_read_b128 v[146:149], v144
	s_mov_b32 s8, 0xff61b1e6
	s_waitcnt lgkmcnt(0)
	v_mov_b32_e32 v142, v147
	v_mov_b32_e32 v143, v148
	v_mov_b32_e32 v147, v149
	v_pk_add_f32 v[142:143], v[142:143], v[146:147]
	s_nop 0
	v_add_f32_e32 v142, v142, v143
	v_fmamk_f32 v142, v142, 0x3a800000, v198
	v_cmp_gt_f32_e32 vcc, s19, v142
	v_mul_f32_e32 v143, 0x4b800000, v142
	s_nop 0
	v_cndmask_b32_e32 v142, v142, v143, vcc
	v_rsq_f32_e32 v142, v142
	s_nop 0
	v_mul_f32_e32 v143, 0x45800000, v142
	v_cndmask_b32_e32 v143, v142, v143, vcc
	v_mul_f32_e32 v142, v124, v143
	v_mul_f32_e32 v145, v125, v143
	v_max3_f32 v142, v142, s8, v145
	v_mul_f32_e32 v145, v126, v143
	v_mul_f32_e32 v146, v127, v143
	v_max3_f32 v142, v142, v145, v146
	v_mul_f32_e32 v145, v120, v143
	v_mul_f32_e32 v146, v121, v143
	v_max3_f32 v142, v142, v145, v146
	v_mul_f32_e32 v145, v122, v143
	v_mul_f32_e32 v146, v123, v143
	v_max3_f32 v142, v142, v145, v146
	v_mul_f32_e32 v145, v116, v143
	v_mul_f32_e32 v146, v117, v143
	v_max3_f32 v142, v142, v145, v146
	v_mul_f32_e32 v145, v118, v143
	v_mul_f32_e32 v146, v119, v143
	v_max3_f32 v142, v142, v145, v146
	v_mul_f32_e32 v145, v112, v143
	v_mul_f32_e32 v146, v113, v143
	v_max3_f32 v142, v142, v145, v146
	v_mul_f32_e32 v145, v114, v143
	v_mul_f32_e32 v146, v115, v143
	v_max3_f32 v142, v142, v145, v146
	v_mov_b32_e32 v145, v142
	s_nop 1
	v_permlane16_swap_b32_e32 v142, v145
	v_max_f32_e32 v145, v145, v145
	v_max_f32_e32 v142, v142, v142
	v_max_f32_e32 v142, v142, v145
	v_mov_b32_e32 v145, v142
	s_nop 1
	v_permlane32_swap_b32_e32 v142, v145
	v_max_f32_e32 v145, v145, v145
	v_max_f32_e32 v142, v142, v142
	v_max_f32_e32 v142, v142, v145
	v_fma_f32 v124, v124, v143, -v142
	v_exp_f32_e32 v124, v124
	v_fma_f32 v125, v125, v143, -v142
	v_exp_f32_e32 v125, v125
	v_fma_f32 v126, v126, v143, -v142
	v_exp_f32_e32 v126, v126
	v_fma_f32 v127, v127, v143, -v142
	v_exp_f32_e32 v127, v127
	v_fma_f32 v120, v120, v143, -v142
	v_add_f32_e32 v145, 0, v124
	v_exp_f32_e32 v120, v120
	v_fma_f32 v121, v121, v143, -v142
	v_add_f32_e32 v145, v125, v145
	v_exp_f32_e32 v121, v121
	v_fma_f32 v122, v122, v143, -v142
	v_add_f32_e32 v145, v126, v145
	v_exp_f32_e32 v122, v122
	v_fma_f32 v123, v123, v143, -v142
	v_add_f32_e32 v145, v127, v145
	v_exp_f32_e32 v123, v123
	v_fma_f32 v116, v116, v143, -v142
	v_add_f32_e32 v145, v120, v145
	v_exp_f32_e32 v116, v116
	v_fma_f32 v117, v117, v143, -v142
	v_add_f32_e32 v145, v121, v145
	v_exp_f32_e32 v117, v117
	v_fma_f32 v118, v118, v143, -v142
	v_add_f32_e32 v145, v122, v145
	v_exp_f32_e32 v118, v118
	v_fma_f32 v119, v119, v143, -v142
	v_add_f32_e32 v145, v123, v145
	v_exp_f32_e32 v119, v119
	v_fma_f32 v112, v112, v143, -v142
	v_add_f32_e32 v145, v116, v145
	v_exp_f32_e32 v112, v112
	v_fma_f32 v113, v113, v143, -v142
	v_add_f32_e32 v145, v117, v145
	v_exp_f32_e32 v113, v113
	v_fma_f32 v114, v114, v143, -v142
	v_add_f32_e32 v145, v118, v145
	v_exp_f32_e32 v114, v114
	v_fma_f32 v115, v115, v143, -v142
	v_add_f32_e32 v145, v119, v145
	v_exp_f32_e32 v115, v115
	v_add_f32_e32 v145, v112, v145
	v_add_f32_e32 v145, v113, v145
	v_add_f32_e32 v145, v114, v145
	v_add_f32_e32 v143, v115, v145
	v_mov_b32_e32 v145, v143
	s_nop 1
	v_permlane16_swap_b32_e32 v143, v145
	v_add_f32_e32 v143, v143, v145
	v_mov_b32_e32 v145, v143
	s_nop 1
	v_permlane32_swap_b32_e32 v143, v145
	s_and_saveexec_b64 s[58:59], s[40:41]
	v_add_f32_e32 v143, v143, v145
	v_add_u32_e32 v145, 0, v155
	v_add_u32_e32 v145, 0x21000, v145
	ds_write_b64 v145, v[142:143]
	s_or_b64 exec, exec, s[58:59]
	ds_read_b128 v[146:149], v144 offset:256
	s_waitcnt lgkmcnt(0)
	v_mov_b32_e32 v142, v147
	v_mov_b32_e32 v143, v148
	v_mov_b32_e32 v147, v149
	v_pk_add_f32 v[142:143], v[142:143], v[146:147]
	s_nop 0
	v_add_f32_e32 v142, v142, v143
	v_fmamk_f32 v142, v142, 0x3a800000, v198
	v_cmp_gt_f32_e32 vcc, s19, v142
	v_mul_f32_e32 v143, 0x4b800000, v142
	s_nop 0
	v_cndmask_b32_e32 v142, v142, v143, vcc
	v_rsq_f32_e32 v142, v142
	s_nop 0
	v_mul_f32_e32 v143, 0x45800000, v142
	v_cndmask_b32_e32 v143, v142, v143, vcc
	v_mul_f32_e32 v142, v108, v143
	v_mul_f32_e32 v145, v109, v143
	v_max3_f32 v142, v142, s8, v145
	v_mul_f32_e32 v145, v110, v143
	v_mul_f32_e32 v146, v111, v143
	v_max3_f32 v142, v142, v145, v146
	v_mul_f32_e32 v145, v104, v143
	v_mul_f32_e32 v146, v105, v143
	v_max3_f32 v142, v142, v145, v146
	v_mul_f32_e32 v145, v106, v143
	v_mul_f32_e32 v146, v107, v143
	v_max3_f32 v142, v142, v145, v146
	v_mul_f32_e32 v145, v100, v143
	v_mul_f32_e32 v146, v101, v143
	v_max3_f32 v142, v142, v145, v146
	v_mul_f32_e32 v145, v102, v143
	v_mul_f32_e32 v146, v103, v143
	v_max3_f32 v142, v142, v145, v146
	v_mul_f32_e32 v145, v96, v143
	v_mul_f32_e32 v146, v97, v143
	v_max3_f32 v142, v142, v145, v146
	v_mul_f32_e32 v145, v98, v143
	v_mul_f32_e32 v146, v99, v143
	v_max3_f32 v142, v142, v145, v146
	v_mov_b32_e32 v145, v142
	s_nop 1
	v_permlane16_swap_b32_e32 v142, v145
	v_max_f32_e32 v145, v145, v145
	v_max_f32_e32 v142, v142, v142
	v_max_f32_e32 v142, v142, v145
	v_mov_b32_e32 v145, v142
	s_nop 1
	v_permlane32_swap_b32_e32 v142, v145
	v_max_f32_e32 v145, v145, v145
	v_max_f32_e32 v142, v142, v142
	v_max_f32_e32 v142, v142, v145
	v_fma_f32 v108, v108, v143, -v142
	v_exp_f32_e32 v108, v108
	v_fma_f32 v109, v109, v143, -v142
	v_exp_f32_e32 v109, v109
	v_fma_f32 v110, v110, v143, -v142
	v_exp_f32_e32 v110, v110
	v_fma_f32 v111, v111, v143, -v142
	v_exp_f32_e32 v111, v111
	v_fma_f32 v104, v104, v143, -v142
	v_add_f32_e32 v145, 0, v108
	v_exp_f32_e32 v104, v104
	v_fma_f32 v105, v105, v143, -v142
	v_add_f32_e32 v145, v109, v145
	v_exp_f32_e32 v105, v105
	v_fma_f32 v106, v106, v143, -v142
	v_add_f32_e32 v145, v110, v145
	v_exp_f32_e32 v106, v106
	v_fma_f32 v107, v107, v143, -v142
	v_add_f32_e32 v145, v111, v145
	v_exp_f32_e32 v107, v107
	v_fma_f32 v100, v100, v143, -v142
	v_add_f32_e32 v145, v104, v145
	v_exp_f32_e32 v100, v100
	v_fma_f32 v101, v101, v143, -v142
	v_add_f32_e32 v145, v105, v145
	v_exp_f32_e32 v101, v101
	v_fma_f32 v102, v102, v143, -v142
	v_add_f32_e32 v145, v106, v145
	v_exp_f32_e32 v102, v102
	v_fma_f32 v103, v103, v143, -v142
	v_add_f32_e32 v145, v107, v145
	v_exp_f32_e32 v103, v103
	v_fma_f32 v96, v96, v143, -v142
	v_add_f32_e32 v145, v100, v145
	v_exp_f32_e32 v96, v96
	v_fma_f32 v97, v97, v143, -v142
	v_add_f32_e32 v145, v101, v145
	v_exp_f32_e32 v97, v97
	v_fma_f32 v98, v98, v143, -v142
	v_add_f32_e32 v145, v102, v145
	v_exp_f32_e32 v98, v98
	v_fma_f32 v99, v99, v143, -v142
	v_add_f32_e32 v145, v103, v145
	v_exp_f32_e32 v99, v99
	v_add_f32_e32 v145, v96, v145
	v_add_f32_e32 v145, v97, v145
	v_add_f32_e32 v145, v98, v145
	v_add_f32_e32 v143, v99, v145
	v_mov_b32_e32 v145, v143
	s_nop 1
	v_permlane16_swap_b32_e32 v143, v145
	v_add_f32_e32 v143, v143, v145
	v_mov_b32_e32 v145, v143
	s_nop 1
	v_permlane32_swap_b32_e32 v143, v145
	s_and_saveexec_b64 s[58:59], s[40:41]
	v_add_f32_e32 v143, v143, v145
	ds_write_b64 v166, v[142:143]
	s_or_b64 exec, exec, s[58:59]
	ds_read_b128 v[146:149], v144 offset:512
	s_waitcnt lgkmcnt(0)
	v_mov_b32_e32 v142, v147
	v_mov_b32_e32 v143, v148
	v_mov_b32_e32 v147, v149
	v_pk_add_f32 v[142:143], v[142:143], v[146:147]
	s_nop 0
	v_add_f32_e32 v142, v142, v143
	v_fmamk_f32 v142, v142, 0x3a800000, v198
	v_cmp_gt_f32_e32 vcc, s19, v142
	v_mul_f32_e32 v143, 0x4b800000, v142
	s_nop 0
	v_cndmask_b32_e32 v142, v142, v143, vcc
	v_rsq_f32_e32 v142, v142
	s_nop 0
	v_mul_f32_e32 v143, 0x45800000, v142
	v_cndmask_b32_e32 v143, v142, v143, vcc
	v_mul_f32_e32 v142, v92, v143
	v_mul_f32_e32 v145, v93, v143
	v_max3_f32 v142, v142, s8, v145
	v_mul_f32_e32 v145, v94, v143
	v_mul_f32_e32 v146, v95, v143
	v_max3_f32 v142, v142, v145, v146
	v_mul_f32_e32 v145, v88, v143
	v_mul_f32_e32 v146, v89, v143
	v_max3_f32 v142, v142, v145, v146
	v_mul_f32_e32 v145, v90, v143
	v_mul_f32_e32 v146, v91, v143
	v_max3_f32 v142, v142, v145, v146
	v_mul_f32_e32 v145, v84, v143
	v_mul_f32_e32 v146, v85, v143
	v_max3_f32 v142, v142, v145, v146
	v_mul_f32_e32 v145, v86, v143
	v_mul_f32_e32 v146, v87, v143
	v_max3_f32 v142, v142, v145, v146
	v_mul_f32_e32 v145, v80, v143
	v_mul_f32_e32 v146, v81, v143
	v_max3_f32 v142, v142, v145, v146
	v_mul_f32_e32 v145, v82, v143
	v_mul_f32_e32 v146, v83, v143
	v_max3_f32 v142, v142, v145, v146
	v_mov_b32_e32 v145, v142
	s_nop 1
	v_permlane16_swap_b32_e32 v142, v145
	v_max_f32_e32 v145, v145, v145
	v_max_f32_e32 v142, v142, v142
	v_max_f32_e32 v142, v142, v145
	v_mov_b32_e32 v145, v142
	s_nop 1
	v_permlane32_swap_b32_e32 v142, v145
	v_max_f32_e32 v145, v145, v145
	v_max_f32_e32 v142, v142, v142
	v_max_f32_e32 v142, v142, v145
	v_fma_f32 v92, v92, v143, -v142
	v_exp_f32_e32 v92, v92
	v_fma_f32 v93, v93, v143, -v142
	v_exp_f32_e32 v93, v93
	v_fma_f32 v94, v94, v143, -v142
	v_exp_f32_e32 v94, v94
	v_fma_f32 v95, v95, v143, -v142
	v_exp_f32_e32 v95, v95
	v_fma_f32 v88, v88, v143, -v142
	v_add_f32_e32 v145, 0, v92
	v_exp_f32_e32 v88, v88
	v_fma_f32 v89, v89, v143, -v142
	v_add_f32_e32 v145, v93, v145
	v_exp_f32_e32 v89, v89
	v_fma_f32 v90, v90, v143, -v142
	v_add_f32_e32 v145, v94, v145
	v_exp_f32_e32 v90, v90
	v_fma_f32 v91, v91, v143, -v142
	v_add_f32_e32 v145, v95, v145
	v_exp_f32_e32 v91, v91
	v_fma_f32 v84, v84, v143, -v142
	v_add_f32_e32 v145, v88, v145
	v_exp_f32_e32 v84, v84
	v_fma_f32 v85, v85, v143, -v142
	v_add_f32_e32 v145, v89, v145
	v_exp_f32_e32 v85, v85
	v_fma_f32 v86, v86, v143, -v142
	v_add_f32_e32 v145, v90, v145
	v_exp_f32_e32 v86, v86
	v_fma_f32 v87, v87, v143, -v142
	v_add_f32_e32 v145, v91, v145
	v_exp_f32_e32 v87, v87
	v_fma_f32 v80, v80, v143, -v142
	v_add_f32_e32 v145, v84, v145
	v_exp_f32_e32 v80, v80
	v_fma_f32 v81, v81, v143, -v142
	v_add_f32_e32 v145, v85, v145
	v_exp_f32_e32 v81, v81
	v_fma_f32 v82, v82, v143, -v142
	v_add_f32_e32 v145, v86, v145
	v_exp_f32_e32 v82, v82
	v_fma_f32 v83, v83, v143, -v142
	v_add_f32_e32 v145, v87, v145
	v_exp_f32_e32 v83, v83
	v_add_f32_e32 v145, v80, v145
	v_add_f32_e32 v145, v81, v145
	v_add_f32_e32 v145, v82, v145
	v_add_f32_e32 v143, v83, v145
	v_mov_b32_e32 v145, v143
	s_nop 1
	v_permlane16_swap_b32_e32 v143, v145
	v_add_f32_e32 v143, v143, v145
	v_mov_b32_e32 v145, v143
	s_nop 1
	v_permlane32_swap_b32_e32 v143, v145
	s_and_saveexec_b64 s[58:59], s[40:41]
	v_add_f32_e32 v143, v143, v145
	ds_write_b64 v167, v[142:143]
	s_or_b64 exec, exec, s[58:59]
	ds_read_b128 v[146:149], v144 offset:768
	s_waitcnt lgkmcnt(0)
	v_mov_b32_e32 v142, v147
	v_mov_b32_e32 v143, v148
	v_mov_b32_e32 v147, v149
	v_pk_add_f32 v[142:143], v[142:143], v[146:147]
	s_nop 0
	v_add_f32_e32 v142, v142, v143
	v_fmamk_f32 v142, v142, 0x3a800000, v198
	v_cmp_gt_f32_e32 vcc, s19, v142
	v_mul_f32_e32 v143, 0x4b800000, v142
	s_nop 0
	v_cndmask_b32_e32 v142, v142, v143, vcc
	v_rsq_f32_e32 v142, v142
	s_nop 0
	v_mul_f32_e32 v143, 0x45800000, v142
	v_cndmask_b32_e32 v143, v142, v143, vcc
	v_mul_f32_e32 v142, v76, v143
	v_mul_f32_e32 v145, v77, v143
	v_max3_f32 v142, v142, s8, v145
	v_mul_f32_e32 v145, v78, v143
	v_mul_f32_e32 v146, v79, v143
	v_max3_f32 v142, v142, v145, v146
	v_mul_f32_e32 v145, v72, v143
	v_mul_f32_e32 v146, v73, v143
	v_max3_f32 v142, v142, v145, v146
	v_mul_f32_e32 v145, v74, v143
	v_mul_f32_e32 v146, v75, v143
	v_max3_f32 v142, v142, v145, v146
	v_mul_f32_e32 v145, v68, v143
	v_mul_f32_e32 v146, v69, v143
	v_max3_f32 v142, v142, v145, v146
	v_mul_f32_e32 v145, v70, v143
	v_mul_f32_e32 v146, v71, v143
	v_max3_f32 v142, v142, v145, v146
	v_mul_f32_e32 v145, v64, v143
	v_mul_f32_e32 v146, v65, v143
	v_max3_f32 v142, v142, v145, v146
	v_mul_f32_e32 v145, v66, v143
	v_mul_f32_e32 v146, v67, v143
	v_max3_f32 v142, v142, v145, v146
	v_mov_b32_e32 v145, v142
	s_nop 1
	v_permlane16_swap_b32_e32 v142, v145
	v_max_f32_e32 v145, v145, v145
	v_max_f32_e32 v142, v142, v142
	v_max_f32_e32 v142, v142, v145
	v_mov_b32_e32 v145, v142
	s_nop 1
	v_permlane32_swap_b32_e32 v142, v145
	v_max_f32_e32 v145, v145, v145
	v_max_f32_e32 v142, v142, v142
	v_max_f32_e32 v142, v142, v145
	v_fma_f32 v76, v76, v143, -v142
	v_exp_f32_e32 v76, v76
	v_fma_f32 v77, v77, v143, -v142
	v_exp_f32_e32 v77, v77
	v_fma_f32 v78, v78, v143, -v142
	v_exp_f32_e32 v78, v78
	v_fma_f32 v79, v79, v143, -v142
	v_exp_f32_e32 v79, v79
	v_fma_f32 v72, v72, v143, -v142
	v_add_f32_e32 v145, 0, v76
	v_exp_f32_e32 v72, v72
	v_fma_f32 v73, v73, v143, -v142
	v_add_f32_e32 v145, v77, v145
	v_exp_f32_e32 v73, v73
	v_fma_f32 v74, v74, v143, -v142
	v_add_f32_e32 v145, v78, v145
	v_exp_f32_e32 v74, v74
	v_fma_f32 v75, v75, v143, -v142
	v_add_f32_e32 v145, v79, v145
	v_exp_f32_e32 v75, v75
	v_fma_f32 v68, v68, v143, -v142
	v_add_f32_e32 v145, v72, v145
	v_exp_f32_e32 v68, v68
	v_fma_f32 v69, v69, v143, -v142
	v_add_f32_e32 v145, v73, v145
	v_exp_f32_e32 v69, v69
	v_fma_f32 v70, v70, v143, -v142
	v_add_f32_e32 v145, v74, v145
	v_exp_f32_e32 v70, v70
	v_fma_f32 v71, v71, v143, -v142
	v_add_f32_e32 v145, v75, v145
	v_exp_f32_e32 v71, v71
	v_fma_f32 v64, v64, v143, -v142
	v_add_f32_e32 v145, v68, v145
	v_exp_f32_e32 v64, v64
	v_fma_f32 v65, v65, v143, -v142
	v_add_f32_e32 v145, v69, v145
	v_exp_f32_e32 v65, v65
	v_fma_f32 v66, v66, v143, -v142
	v_add_f32_e32 v145, v70, v145
	v_exp_f32_e32 v66, v66
	v_fma_f32 v67, v67, v143, -v142
	v_add_f32_e32 v145, v71, v145
	v_exp_f32_e32 v67, v67
	v_add_f32_e32 v145, v64, v145
	v_add_f32_e32 v145, v65, v145
	v_add_f32_e32 v145, v66, v145
	v_add_f32_e32 v143, v67, v145
	v_mov_b32_e32 v145, v143
	s_nop 1
	v_permlane16_swap_b32_e32 v143, v145
	v_add_f32_e32 v143, v143, v145
	v_mov_b32_e32 v145, v143
	s_nop 1
	v_permlane32_swap_b32_e32 v143, v145
	s_and_saveexec_b64 s[58:59], s[40:41]
	v_add_f32_e32 v143, v143, v145
	ds_write_b64 v168, v[142:143]
	s_or_b64 exec, exec, s[58:59]
	ds_read_b128 v[146:149], v144 offset:2048
	s_waitcnt lgkmcnt(0)
	v_mov_b32_e32 v142, v147
	v_mov_b32_e32 v143, v148
	v_mov_b32_e32 v147, v149
	v_pk_add_f32 v[142:143], v[142:143], v[146:147]
	s_nop 0
	v_add_f32_e32 v142, v142, v143
	v_fmamk_f32 v142, v142, 0x3a800000, v198
	v_cmp_gt_f32_e32 vcc, s19, v142
	v_mul_f32_e32 v143, 0x4b800000, v142
	s_nop 0
	v_cndmask_b32_e32 v142, v142, v143, vcc
	v_rsq_f32_e32 v142, v142
	s_nop 0
	v_mul_f32_e32 v143, 0x45800000, v142
	v_cndmask_b32_e32 v143, v142, v143, vcc
	v_mul_f32_e32 v142, v60, v143
	v_mul_f32_e32 v145, v61, v143
	v_max3_f32 v142, v142, s8, v145
	v_mul_f32_e32 v145, v62, v143
	v_mul_f32_e32 v146, v63, v143
	v_max3_f32 v142, v142, v145, v146
	v_mul_f32_e32 v145, v56, v143
	v_mul_f32_e32 v146, v57, v143
	v_max3_f32 v142, v142, v145, v146
	v_mul_f32_e32 v145, v58, v143
	v_mul_f32_e32 v146, v59, v143
	v_max3_f32 v142, v142, v145, v146
	v_mul_f32_e32 v145, v52, v143
	v_mul_f32_e32 v146, v53, v143
	v_max3_f32 v142, v142, v145, v146
	v_mul_f32_e32 v145, v54, v143
	v_mul_f32_e32 v146, v55, v143
	v_max3_f32 v142, v142, v145, v146
	v_mul_f32_e32 v145, v48, v143
	v_mul_f32_e32 v146, v49, v143
	v_max3_f32 v142, v142, v145, v146
	v_mul_f32_e32 v145, v50, v143
	v_mul_f32_e32 v146, v51, v143
	v_max3_f32 v142, v142, v145, v146
	v_mov_b32_e32 v145, v142
	s_nop 1
	v_permlane16_swap_b32_e32 v142, v145
	v_max_f32_e32 v145, v145, v145
	v_max_f32_e32 v142, v142, v142
	v_max_f32_e32 v142, v142, v145
	v_mov_b32_e32 v145, v142
	s_nop 1
	v_permlane32_swap_b32_e32 v142, v145
	v_max_f32_e32 v145, v145, v145
	v_max_f32_e32 v142, v142, v142
	v_max_f32_e32 v142, v142, v145
	v_fma_f32 v60, v60, v143, -v142
	v_exp_f32_e32 v60, v60
	v_fma_f32 v61, v61, v143, -v142
	v_exp_f32_e32 v61, v61
	v_fma_f32 v62, v62, v143, -v142
	v_exp_f32_e32 v62, v62
	v_fma_f32 v63, v63, v143, -v142
	v_exp_f32_e32 v63, v63
	v_fma_f32 v56, v56, v143, -v142
	v_add_f32_e32 v145, 0, v60
	v_exp_f32_e32 v56, v56
	v_fma_f32 v57, v57, v143, -v142
	v_add_f32_e32 v145, v61, v145
	v_exp_f32_e32 v57, v57
	v_fma_f32 v58, v58, v143, -v142
	v_add_f32_e32 v145, v62, v145
	v_exp_f32_e32 v58, v58
	v_fma_f32 v59, v59, v143, -v142
	v_add_f32_e32 v145, v63, v145
	v_exp_f32_e32 v59, v59
	v_fma_f32 v52, v52, v143, -v142
	v_add_f32_e32 v145, v56, v145
	v_exp_f32_e32 v52, v52
	v_fma_f32 v53, v53, v143, -v142
	v_add_f32_e32 v145, v57, v145
	v_exp_f32_e32 v53, v53
	v_fma_f32 v54, v54, v143, -v142
	v_add_f32_e32 v145, v58, v145
	v_exp_f32_e32 v54, v54
	v_fma_f32 v55, v55, v143, -v142
	v_add_f32_e32 v145, v59, v145
	v_exp_f32_e32 v55, v55
	v_fma_f32 v48, v48, v143, -v142
	v_add_f32_e32 v145, v52, v145
	v_exp_f32_e32 v48, v48
	v_fma_f32 v49, v49, v143, -v142
	v_add_f32_e32 v145, v53, v145
	v_exp_f32_e32 v49, v49
	v_fma_f32 v50, v50, v143, -v142
	v_add_f32_e32 v145, v54, v145
	v_exp_f32_e32 v50, v50
	v_fma_f32 v51, v51, v143, -v142
	v_add_f32_e32 v145, v55, v145
	v_exp_f32_e32 v51, v51
	v_add_f32_e32 v145, v48, v145
	v_add_f32_e32 v145, v49, v145
	v_add_f32_e32 v145, v50, v145
	v_add_f32_e32 v143, v51, v145
	v_mov_b32_e32 v145, v143
	s_nop 1
	v_permlane16_swap_b32_e32 v143, v145
	v_add_f32_e32 v143, v143, v145
	v_mov_b32_e32 v145, v143
	s_nop 1
	v_permlane32_swap_b32_e32 v143, v145
	s_and_saveexec_b64 s[58:59], s[40:41]
	v_add_f32_e32 v143, v143, v145
	ds_write_b64 v169, v[142:143]
	s_or_b64 exec, exec, s[58:59]
	ds_read_b128 v[146:149], v144 offset:2304
	s_waitcnt lgkmcnt(0)
	v_mov_b32_e32 v142, v147
	v_mov_b32_e32 v143, v148
	v_mov_b32_e32 v147, v149
	v_pk_add_f32 v[142:143], v[142:143], v[146:147]
	s_nop 0
	v_add_f32_e32 v142, v142, v143
	v_fmamk_f32 v142, v142, 0x3a800000, v198
	v_cmp_gt_f32_e32 vcc, s19, v142
	v_mul_f32_e32 v143, 0x4b800000, v142
	s_nop 0
	v_cndmask_b32_e32 v142, v142, v143, vcc
	v_rsq_f32_e32 v142, v142
	s_nop 0
	v_mul_f32_e32 v143, 0x45800000, v142
	v_cndmask_b32_e32 v143, v142, v143, vcc
	v_mul_f32_e32 v142, v44, v143
	v_mul_f32_e32 v145, v45, v143
	v_max3_f32 v142, v142, s8, v145
	v_mul_f32_e32 v145, v46, v143
	v_mul_f32_e32 v146, v47, v143
	v_max3_f32 v142, v142, v145, v146
	v_mul_f32_e32 v145, v40, v143
	v_mul_f32_e32 v146, v41, v143
	v_max3_f32 v142, v142, v145, v146
	v_mul_f32_e32 v145, v42, v143
	v_mul_f32_e32 v146, v43, v143
	v_max3_f32 v142, v142, v145, v146
	v_mul_f32_e32 v145, v36, v143
	v_mul_f32_e32 v146, v37, v143
	v_max3_f32 v142, v142, v145, v146
	v_mul_f32_e32 v145, v38, v143
	v_mul_f32_e32 v146, v39, v143
	v_max3_f32 v142, v142, v145, v146
	v_mul_f32_e32 v145, v32, v143
	v_mul_f32_e32 v146, v33, v143
	v_max3_f32 v142, v142, v145, v146
	v_mul_f32_e32 v145, v34, v143
	v_mul_f32_e32 v146, v35, v143
	v_max3_f32 v142, v142, v145, v146
	v_mov_b32_e32 v145, v142
	s_nop 1
	v_permlane16_swap_b32_e32 v142, v145
	v_max_f32_e32 v145, v145, v145
	v_max_f32_e32 v142, v142, v142
	v_max_f32_e32 v142, v142, v145
	v_mov_b32_e32 v145, v142
	s_nop 1
	v_permlane32_swap_b32_e32 v142, v145
	v_max_f32_e32 v145, v145, v145
	v_max_f32_e32 v142, v142, v142
	v_max_f32_e32 v142, v142, v145
	v_fma_f32 v44, v44, v143, -v142
	v_exp_f32_e32 v44, v44
	v_fma_f32 v45, v45, v143, -v142
	v_exp_f32_e32 v45, v45
	v_fma_f32 v46, v46, v143, -v142
	v_exp_f32_e32 v46, v46
	v_fma_f32 v47, v47, v143, -v142
	v_exp_f32_e32 v47, v47
	v_fma_f32 v40, v40, v143, -v142
	v_add_f32_e32 v145, 0, v44
	v_exp_f32_e32 v40, v40
	v_fma_f32 v41, v41, v143, -v142
	v_add_f32_e32 v145, v45, v145
	v_exp_f32_e32 v41, v41
	v_fma_f32 v42, v42, v143, -v142
	v_add_f32_e32 v145, v46, v145
	v_exp_f32_e32 v42, v42
	v_fma_f32 v43, v43, v143, -v142
	v_add_f32_e32 v145, v47, v145
	v_exp_f32_e32 v43, v43
	v_fma_f32 v36, v36, v143, -v142
	v_add_f32_e32 v145, v40, v145
	v_exp_f32_e32 v36, v36
	v_fma_f32 v37, v37, v143, -v142
	v_add_f32_e32 v145, v41, v145
	v_exp_f32_e32 v37, v37
	v_fma_f32 v38, v38, v143, -v142
	v_add_f32_e32 v145, v42, v145
	v_exp_f32_e32 v38, v38
	v_fma_f32 v39, v39, v143, -v142
	v_add_f32_e32 v145, v43, v145
	v_exp_f32_e32 v39, v39
	v_fma_f32 v32, v32, v143, -v142
	v_add_f32_e32 v145, v36, v145
	v_exp_f32_e32 v32, v32
	v_fma_f32 v33, v33, v143, -v142
	v_add_f32_e32 v145, v37, v145
	v_exp_f32_e32 v33, v33
	v_fma_f32 v34, v34, v143, -v142
	v_add_f32_e32 v145, v38, v145
	v_exp_f32_e32 v34, v34
	v_fma_f32 v35, v35, v143, -v142
	v_add_f32_e32 v145, v39, v145
	v_exp_f32_e32 v35, v35
	v_add_f32_e32 v145, v32, v145
	v_add_f32_e32 v145, v33, v145
	v_add_f32_e32 v145, v34, v145
	v_add_f32_e32 v143, v35, v145
	v_mov_b32_e32 v145, v143
	s_nop 1
	v_permlane16_swap_b32_e32 v143, v145
	v_add_f32_e32 v143, v143, v145
	v_mov_b32_e32 v145, v143
	s_nop 1
	v_permlane32_swap_b32_e32 v143, v145
	s_and_saveexec_b64 s[58:59], s[40:41]
	v_add_f32_e32 v143, v143, v145
	ds_write_b64 v170, v[142:143]
	s_or_b64 exec, exec, s[58:59]
	ds_read_b128 v[146:149], v144 offset:2560
	s_waitcnt lgkmcnt(0)
	v_mov_b32_e32 v142, v147
	v_mov_b32_e32 v143, v148
	v_mov_b32_e32 v147, v149
	v_pk_add_f32 v[142:143], v[142:143], v[146:147]
	s_nop 0
	v_add_f32_e32 v142, v142, v143
	v_fmamk_f32 v142, v142, 0x3a800000, v198
	v_cmp_gt_f32_e32 vcc, s19, v142
	v_mul_f32_e32 v143, 0x4b800000, v142
	s_nop 0
	v_cndmask_b32_e32 v142, v142, v143, vcc
	v_rsq_f32_e32 v142, v142
	s_nop 0
	v_mul_f32_e32 v143, 0x45800000, v142
	v_cndmask_b32_e32 v143, v142, v143, vcc
	v_mul_f32_e32 v142, v28, v143
	v_mul_f32_e32 v145, v29, v143
	v_max3_f32 v142, v142, s8, v145
	v_mul_f32_e32 v145, v30, v143
	v_mul_f32_e32 v146, v31, v143
	v_max3_f32 v142, v142, v145, v146
	v_mul_f32_e32 v145, v24, v143
	v_mul_f32_e32 v146, v25, v143
	v_max3_f32 v142, v142, v145, v146
	v_mul_f32_e32 v145, v26, v143
	v_mul_f32_e32 v146, v27, v143
	v_max3_f32 v142, v142, v145, v146
	v_mul_f32_e32 v145, v20, v143
	v_mul_f32_e32 v146, v21, v143
	v_max3_f32 v142, v142, v145, v146
	v_mul_f32_e32 v145, v22, v143
	v_mul_f32_e32 v146, v23, v143
	v_max3_f32 v142, v142, v145, v146
	v_mul_f32_e32 v145, v16, v143
	v_mul_f32_e32 v146, v17, v143
	v_max3_f32 v142, v142, v145, v146
	v_mul_f32_e32 v145, v18, v143
	v_mul_f32_e32 v146, v19, v143
	v_max3_f32 v142, v142, v145, v146
	v_mov_b32_e32 v145, v142
	s_nop 1
	v_permlane16_swap_b32_e32 v142, v145
	v_max_f32_e32 v145, v145, v145
	v_max_f32_e32 v142, v142, v142
	v_max_f32_e32 v142, v142, v145
	v_mov_b32_e32 v145, v142
	s_nop 1
	v_permlane32_swap_b32_e32 v142, v145
	v_max_f32_e32 v145, v145, v145
	v_max_f32_e32 v142, v142, v142
	v_max_f32_e32 v142, v142, v145
	v_fma_f32 v28, v28, v143, -v142
	v_exp_f32_e32 v28, v28
	v_fma_f32 v29, v29, v143, -v142
	v_exp_f32_e32 v29, v29
	v_fma_f32 v30, v30, v143, -v142
	v_exp_f32_e32 v30, v30
	v_fma_f32 v31, v31, v143, -v142
	v_exp_f32_e32 v31, v31
	v_fma_f32 v24, v24, v143, -v142
	v_add_f32_e32 v145, 0, v28
	v_exp_f32_e32 v24, v24
	v_fma_f32 v25, v25, v143, -v142
	v_add_f32_e32 v145, v29, v145
	v_exp_f32_e32 v25, v25
	v_fma_f32 v26, v26, v143, -v142
	v_add_f32_e32 v145, v30, v145
	v_exp_f32_e32 v26, v26
	v_fma_f32 v27, v27, v143, -v142
	v_add_f32_e32 v145, v31, v145
	v_exp_f32_e32 v27, v27
	v_fma_f32 v20, v20, v143, -v142
	v_add_f32_e32 v145, v24, v145
	v_exp_f32_e32 v20, v20
	v_fma_f32 v21, v21, v143, -v142
	v_add_f32_e32 v145, v25, v145
	v_exp_f32_e32 v21, v21
	v_fma_f32 v22, v22, v143, -v142
	v_add_f32_e32 v145, v26, v145
	v_exp_f32_e32 v22, v22
	v_fma_f32 v23, v23, v143, -v142
	v_add_f32_e32 v145, v27, v145
	v_exp_f32_e32 v23, v23
	v_fma_f32 v16, v16, v143, -v142
	v_add_f32_e32 v145, v20, v145
	v_exp_f32_e32 v16, v16
	v_fma_f32 v17, v17, v143, -v142
	v_add_f32_e32 v145, v21, v145
	v_exp_f32_e32 v17, v17
	v_fma_f32 v18, v18, v143, -v142
	v_add_f32_e32 v145, v22, v145
	v_exp_f32_e32 v18, v18
	v_fma_f32 v19, v19, v143, -v142
	v_add_f32_e32 v145, v23, v145
	v_exp_f32_e32 v19, v19
	v_add_f32_e32 v145, v16, v145
	v_add_f32_e32 v145, v17, v145
	v_add_f32_e32 v145, v18, v145
	v_add_f32_e32 v143, v19, v145
	v_mov_b32_e32 v145, v143
	s_nop 1
	v_permlane16_swap_b32_e32 v143, v145
	v_add_f32_e32 v143, v143, v145
	v_mov_b32_e32 v145, v143
	s_nop 1
	v_permlane32_swap_b32_e32 v143, v145
	s_and_saveexec_b64 s[58:59], s[40:41]
	v_add_f32_e32 v143, v143, v145
	ds_write_b64 v171, v[142:143]
	s_or_b64 exec, exec, s[58:59]
	ds_read_b128 v[142:145], v144 offset:2816
	s_waitcnt lgkmcnt(0)
	v_mov_b32_e32 v146, v143
	v_mov_b32_e32 v147, v144
	v_mov_b32_e32 v143, v145
	v_pk_add_f32 v[142:143], v[146:147], v[142:143]
	s_nop 0
	v_add_f32_e32 v142, v142, v143
	v_fmamk_f32 v142, v142, 0x3a800000, v198
	v_cmp_gt_f32_e32 vcc, s19, v142
	v_mul_f32_e32 v143, 0x4b800000, v142
	s_nop 0
	v_cndmask_b32_e32 v142, v142, v143, vcc
	v_rsq_f32_e32 v142, v142
	s_nop 0
	v_mul_f32_e32 v143, 0x45800000, v142
	v_cndmask_b32_e32 v149, v142, v143, vcc
	v_mul_f32_e32 v142, v12, v149
	v_mul_f32_e32 v143, v13, v149
	v_max3_f32 v142, v142, s8, v143
	v_mul_f32_e32 v143, v14, v149
	v_mul_f32_e32 v144, v15, v149
	v_max3_f32 v142, v142, v143, v144
	v_mul_f32_e32 v143, v8, v149
	v_mul_f32_e32 v144, v9, v149
	v_max3_f32 v142, v142, v143, v144
	v_mul_f32_e32 v143, v10, v149
	v_mul_f32_e32 v144, v11, v149
	v_max3_f32 v142, v142, v143, v144
	v_mul_f32_e32 v143, v4, v149
	v_mul_f32_e32 v144, v5, v149
	v_max3_f32 v142, v142, v143, v144
	v_mul_f32_e32 v143, v6, v149
	v_mul_f32_e32 v144, v7, v149
	v_max3_f32 v142, v142, v143, v144
	v_mul_f32_e32 v143, v0, v149
	v_mul_f32_e32 v144, v1, v149
	v_max3_f32 v142, v142, v143, v144
	v_mul_f32_e32 v143, v2, v149
	v_mul_f32_e32 v144, v3, v149
	v_max3_f32 v142, v142, v143, v144
	v_mov_b32_e32 v143, v142
	s_nop 1
	v_permlane16_swap_b32_e32 v142, v143
	v_max_f32_e32 v143, v143, v143
	v_max_f32_e32 v142, v142, v142
	v_max_f32_e32 v142, v142, v143
	v_mov_b32_e32 v143, v142
	s_nop 1
	v_permlane32_swap_b32_e32 v142, v143
	v_max_f32_e32 v143, v143, v143
	v_max_f32_e32 v142, v142, v142
	v_max_f32_e32 v150, v142, v143
	v_fma_f32 v12, v12, v149, -v150
	v_exp_f32_e32 v12, v12
	v_fma_f32 v13, v13, v149, -v150
	v_exp_f32_e32 v13, v13
	v_fma_f32 v14, v14, v149, -v150
	v_exp_f32_e32 v14, v14
	v_fma_f32 v15, v15, v149, -v150
	v_exp_f32_e32 v15, v15
	v_fma_f32 v8, v8, v149, -v150
	v_add_f32_e32 v142, 0, v12
	v_exp_f32_e32 v8, v8
	v_fma_f32 v9, v9, v149, -v150
	v_add_f32_e32 v142, v13, v142
	v_exp_f32_e32 v9, v9
	v_add_f32_e32 v142, v14, v142
	v_add_f32_e32 v142, v15, v142
	v_add_f32_e32 v142, v8, v142
	v_fma_f32 v10, v10, v149, -v150
	v_add_f32_e32 v143, v9, v142
	v_exp_f32_e32 v142, v10
	v_fma_f32 v11, v11, v149, -v150
	v_fma_f32 v4, v4, v149, -v150
	v_fma_f32 v5, v5, v149, -v150
	v_add_f32_e32 v10, v142, v143
	v_exp_f32_e32 v143, v11
	v_fma_f32 v0, v0, v149, -v150
	v_exp_f32_e32 v146, v0
	v_fma_f32 v1, v1, v149, -v150
	v_add_f32_e32 v11, v143, v10
	v_exp_f32_e32 v10, v4
	v_exp_f32_e32 v147, v1
	v_fma_f32 v1, v2, v149, -v150
	v_exp_f32_e32 v148, v1
	v_add_f32_e32 v4, v10, v11
	v_exp_f32_e32 v11, v5
	v_fma_f32 v5, v6, v149, -v150
	v_exp_f32_e32 v144, v5
	v_fma_f32 v5, v7, v149, -v150
	v_exp_f32_e32 v145, v5
	v_add_f32_e32 v4, v11, v4
	v_add_f32_e32 v4, v144, v4
	v_fma_f32 v1, v3, v149, -v150
	v_add_f32_e32 v4, v145, v4
	v_exp_f32_e32 v149, v1
	v_add_f32_e32 v0, v146, v4
	v_add_f32_e32 v0, v147, v0
	v_add_f32_e32 v0, v148, v0
	v_add_f32_e32 v0, v149, v0
	v_mov_b32_e32 v1, v0
	s_nop 1
	v_permlane16_swap_b32_e32 v0, v1
	v_add_f32_e32 v0, v0, v1
	v_mov_b32_e32 v1, v0
	s_nop 1
	v_permlane32_swap_b32_e32 v0, v1
	s_and_saveexec_b64 s[58:59], s[40:41]
	v_add_f32_e32 v151, v0, v1
	ds_write_b64 v172, v[150:151]
	s_or_b64 exec, exec, s[58:59]
	s_waitcnt lgkmcnt(0)
	s_barrier
	ds_read_b128 v[0:3], v173 offset:16
	ds_read_b128 v[4:7], v173
	s_cmp_lt_i32 s66, 1
	s_waitcnt lgkmcnt(0)
	v_max_f32_e32 v150, v2, v2
	v_max_f32_e32 v151, v0, v0
	v_max_f32_e32 v150, v151, v150
	v_max3_f32 v150, v4, v6, v150
	v_sub_f32_e32 v4, v4, v150
	v_exp_f32_e32 v4, v4
	v_sub_f32_e32 v6, v6, v150
	v_exp_f32_e32 v6, v6
	v_mov_b32_e32 v181, v4
	s_cbranch_scc1 .LBB0_1464
	s_cmp_lg_u32 s66, 1
	s_mov_b64 s[58:59], -1
	s_cbranch_scc0 .LBB0_1462
	v_cndmask_b32_e64 v151, v2, v0, s[42:43]
	v_sub_f32_e32 v151, v151, v150
	v_exp_f32_e32 v181, v151
	s_mov_b64 s[58:59], 0

.LBB0_1688:
	s_or_b64 exec, exec, s[48:49]
	s_ashr_i32 s45, s44, 31
	s_lshl_b64 s[48:49], s[44:45], 19
	s_add_u32 s48, s80, s48
	s_addc_u32 s49, s81, s49
	s_and_b64 s[50:51], s[42:43], exec
	s_cselect_b32 s45, s49, s55
	s_cselect_b32 s53, s48, s54
	s_ashr_i32 s47, s46, 31
	s_lshl_b64 s[50:51], s[46:47], 19
	s_add_u32 s50, s22, s50
	s_addc_u32 s51, s23, s51
	s_and_b64 s[58:59], s[42:43], exec
	s_cselect_b32 s47, s51, s57
	s_cselect_b32 s65, s50, s56
	s_add_u32 s54, s54, 0x40080
	s_addc_u32 s55, s55, 0
	s_add_u32 s66, s56, 0x100
	v_mov_b32_e32 v0, 0
	s_addc_u32 s67, s57, 0
	s_mov_b32 s68, -2
	v_mov_b32_e32 v1, v0
	v_mov_b32_e32 v2, v0
	v_mov_b32_e32 v3, v0
	v_mov_b32_e32 v4, v0
	v_mov_b32_e32 v5, v0
	v_mov_b32_e32 v6, v0
	v_mov_b32_e32 v7, v0
	v_mov_b32_e32 v16, v0
	v_mov_b32_e32 v17, v0
	v_mov_b32_e32 v18, v0
	v_mov_b32_e32 v19, v0
	v_mov_b32_e32 v20, v0
	v_mov_b32_e32 v21, v0
	v_mov_b32_e32 v22, v0
	v_mov_b32_e32 v23, v0
	v_mov_b32_e32 v32, v0
	v_mov_b32_e32 v33, v0
	v_mov_b32_e32 v34, v0
	v_mov_b32_e32 v35, v0
	v_mov_b32_e32 v36, v0
	v_mov_b32_e32 v37, v0
	v_mov_b32_e32 v38, v0
	v_mov_b32_e32 v39, v0
	v_mov_b32_e32 v48, v0
	v_mov_b32_e32 v49, v0
	v_mov_b32_e32 v50, v0
	v_mov_b32_e32 v51, v0
	v_mov_b32_e32 v52, v0
	v_mov_b32_e32 v53, v0
	v_mov_b32_e32 v54, v0
	v_mov_b32_e32 v55, v0
	v_mov_b32_e32 v8, v0
	v_mov_b32_e32 v9, v0
	v_mov_b32_e32 v10, v0
	v_mov_b32_e32 v11, v0
	v_mov_b32_e32 v12, v0
	v_mov_b32_e32 v13, v0
	v_mov_b32_e32 v14, v0
	v_mov_b32_e32 v15, v0
	v_mov_b32_e32 v24, v0
	v_mov_b32_e32 v25, v0
	v_mov_b32_e32 v26, v0
	v_mov_b32_e32 v27, v0
	v_mov_b32_e32 v28, v0
	v_mov_b32_e32 v29, v0
	v_mov_b32_e32 v30, v0
	v_mov_b32_e32 v31, v0
	v_mov_b32_e32 v40, v0
	v_mov_b32_e32 v41, v0
	v_mov_b32_e32 v42, v0
	v_mov_b32_e32 v43, v0
	v_mov_b32_e32 v44, v0
	v_mov_b32_e32 v45, v0
	v_mov_b32_e32 v46, v0
	v_mov_b32_e32 v47, v0
	v_mov_b32_e32 v56, v0
	v_mov_b32_e32 v57, v0
	v_mov_b32_e32 v58, v0
	v_mov_b32_e32 v59, v0
	v_mov_b32_e32 v60, v0
	v_mov_b32_e32 v61, v0
	v_mov_b32_e32 v62, v0
	v_mov_b32_e32 v63, v0
	v_mov_b32_e32 v64, v0
	v_mov_b32_e32 v65, v0
	v_mov_b32_e32 v66, v0
	v_mov_b32_e32 v67, v0
	v_mov_b32_e32 v68, v0
	v_mov_b32_e32 v69, v0
	v_mov_b32_e32 v70, v0
	v_mov_b32_e32 v71, v0
	v_mov_b32_e32 v80, v0
	v_mov_b32_e32 v81, v0
	v_mov_b32_e32 v82, v0
	v_mov_b32_e32 v83, v0
	v_mov_b32_e32 v84, v0
	v_mov_b32_e32 v85, v0
	v_mov_b32_e32 v86, v0
	v_mov_b32_e32 v87, v0
	v_mov_b32_e32 v96, v0
	v_mov_b32_e32 v97, v0
	v_mov_b32_e32 v98, v0
	v_mov_b32_e32 v99, v0
	v_mov_b32_e32 v100, v0
	v_mov_b32_e32 v101, v0
	v_mov_b32_e32 v102, v0
	v_mov_b32_e32 v103, v0
	v_mov_b32_e32 v112, v0
	v_mov_b32_e32 v113, v0
	v_mov_b32_e32 v114, v0
	v_mov_b32_e32 v115, v0
	v_mov_b32_e32 v116, v0
	v_mov_b32_e32 v117, v0
	v_mov_b32_e32 v118, v0
	v_mov_b32_e32 v119, v0
	v_mov_b32_e32 v72, v0
	v_mov_b32_e32 v73, v0
	v_mov_b32_e32 v74, v0
	v_mov_b32_e32 v75, v0
	v_mov_b32_e32 v76, v0
	v_mov_b32_e32 v77, v0
	v_mov_b32_e32 v78, v0
	v_mov_b32_e32 v79, v0
	v_mov_b32_e32 v88, v0
	v_mov_b32_e32 v89, v0
	v_mov_b32_e32 v90, v0
	v_mov_b32_e32 v91, v0
	v_mov_b32_e32 v92, v0
	v_mov_b32_e32 v93, v0
	v_mov_b32_e32 v94, v0
	v_mov_b32_e32 v95, v0
	v_mov_b32_e32 v104, v0
	v_mov_b32_e32 v105, v0
	v_mov_b32_e32 v106, v0
	v_mov_b32_e32 v107, v0
	v_mov_b32_e32 v108, v0
	v_mov_b32_e32 v109, v0
	v_mov_b32_e32 v110, v0
	v_mov_b32_e32 v111, v0
	v_mov_b32_e32 v120, v0
	v_mov_b32_e32 v121, v0
	v_mov_b32_e32 v122, v0
	v_mov_b32_e32 v123, v0
	v_mov_b32_e32 v124, v0
	v_mov_b32_e32 v125, v0
	v_mov_b32_e32 v126, v0
	v_mov_b32_e32 v127, v0
	s_cmp_eq_u32 s9, 0
	s_cbranch_scc1 .LBB0_1689
	s_add_u32 s56, s54, 0xfffc0080
	s_addc_u32 s57, s55, -1
	s_add_i32 s69, 0, 0x10000
	s_cmp_eq_u32 s68, 12
	s_cselect_b32 s59, s45, s57
	s_cselect_b32 s58, s53, s56
	v_add_u32_e32 v146, s69, v149
	s_cselect_b32 s57, s47, s67
	s_cselect_b32 s56, s65, s66
	s_add_i32 s72, 0, 0x14000
	ds_read_b128 v[142:145], v146
	ds_read_b128 v[154:157], v146 offset:1024
	ds_read_b128 v[158:161], v146 offset:2048
	ds_read_b128 v[162:165], v146 offset:3072
	v_add_u32_e32 v146, s72, v149
	ds_read_b128 v[166:169], v146
	ds_read_b128 v[170:173], v146 offset:1024
	ds_read_b128 v[174:177], v146 offset:2048
	ds_read_b128 v[178:181], v146 offset:3072
	ds_read_b128 v[182:185], v153
	ds_read_b128 v[186:189], v153 offset:1024
	ds_read_b128 v[190:193], v153 offset:2048
	ds_read_b128 v[194:197], v153 offset:3072
	ds_read_b128 v[200:203], v153 offset:4096
	ds_read_b128 v[204:207], v153 offset:5120
	ds_read_b128 v[216:219], v153 offset:6144
	ds_read_b128 v[220:223], v153 offset:7168
	s_waitcnt vmcnt(24)
	s_waitcnt lgkmcnt(0)
	s_barrier
	s_setprio 1
	s_waitcnt lgkmcnt(0)
	v_mfma_f32_16x16x32_bf16 v[124:127], v[142:145], v[182:185], v[124:127]
	v_mfma_f32_16x16x32_bf16 v[120:123], v[158:161], v[182:185], v[120:123]
	v_mfma_f32_16x16x32_bf16 v[108:111], v[142:145], v[190:193], v[108:111]
	v_mfma_f32_16x16x32_bf16 v[104:107], v[158:161], v[190:193], v[104:107]
	v_mfma_f32_16x16x32_bf16 v[92:95], v[142:145], v[200:203], v[92:95]
	v_mfma_f32_16x16x32_bf16 v[88:91], v[158:161], v[200:203], v[88:91]
	v_mfma_f32_16x16x32_bf16 v[76:79], v[142:145], v[216:219], v[76:79]
	v_mfma_f32_16x16x32_bf16 v[72:75], v[158:161], v[216:219], v[72:75]
	v_mfma_f32_16x16x32_bf16 v[124:127], v[154:157], v[186:189], v[124:127]
	v_mfma_f32_16x16x32_bf16 v[120:123], v[162:165], v[186:189], v[120:123]
	v_mfma_f32_16x16x32_bf16 v[108:111], v[154:157], v[194:197], v[108:111]
	v_mfma_f32_16x16x32_bf16 v[104:107], v[162:165], v[194:197], v[104:107]
	v_mfma_f32_16x16x32_bf16 v[92:95], v[154:157], v[204:207], v[92:95]
	v_mfma_f32_16x16x32_bf16 v[88:91], v[162:165], v[204:207], v[88:91]
	v_mfma_f32_16x16x32_bf16 v[76:79], v[154:157], v[220:223], v[76:79]
	v_mfma_f32_16x16x32_bf16 v[72:75], v[162:165], v[220:223], v[72:75]
	s_setprio 0
	s_setprio 1
	v_mfma_f32_16x16x32_bf16 v[116:119], v[166:169], v[182:185], v[116:119]
	v_mfma_f32_16x16x32_bf16 v[112:115], v[174:177], v[182:185], v[112:115]
	v_mfma_f32_16x16x32_bf16 v[100:103], v[166:169], v[190:193], v[100:103]
	v_mfma_f32_16x16x32_bf16 v[96:99], v[174:177], v[190:193], v[96:99]
	v_mfma_f32_16x16x32_bf16 v[84:87], v[166:169], v[200:203], v[84:87]
	v_mfma_f32_16x16x32_bf16 v[80:83], v[174:177], v[200:203], v[80:83]
	v_mfma_f32_16x16x32_bf16 v[68:71], v[166:169], v[216:219], v[68:71]
	v_mfma_f32_16x16x32_bf16 v[64:67], v[174:177], v[216:219], v[64:67]
	v_mfma_f32_16x16x32_bf16 v[116:119], v[170:173], v[186:189], v[116:119]
	v_mfma_f32_16x16x32_bf16 v[112:115], v[178:181], v[186:189], v[112:115]
	v_mfma_f32_16x16x32_bf16 v[100:103], v[170:173], v[194:197], v[100:103]
	v_mfma_f32_16x16x32_bf16 v[96:99], v[178:181], v[194:197], v[96:99]
	v_mfma_f32_16x16x32_bf16 v[84:87], v[170:173], v[204:207], v[84:87]
	v_mfma_f32_16x16x32_bf16 v[80:83], v[178:181], v[204:207], v[80:83]
	v_mfma_f32_16x16x32_bf16 v[68:71], v[170:173], v[220:223], v[68:71]
	v_mfma_f32_16x16x32_bf16 v[64:67], v[178:181], v[220:223], v[64:67]
	s_setprio 0
	s_barrier
	s_add_i32 s69, s69, s0
	v_lshl_add_u64 v[146:147], s[56:57], 0, v[128:129]
	s_mov_b32 m0, s69
	ds_read_b128 v[182:185], v153 offset:16384
	ds_read_b128 v[186:189], v153 offset:17408
	ds_read_b128 v[190:193], v153 offset:18432
	ds_read_b128 v[194:197], v153 offset:19456
	ds_read_b128 v[200:203], v153 offset:20480
	ds_read_b128 v[204:207], v153 offset:21504
	ds_read_b128 v[216:219], v153 offset:22528
	ds_read_b128 v[220:223], v153 offset:23552
	global_load_lds_dwordx4 v[146:147], off
	s_add_i32 m0, s69, 0x2000
	s_add_u32 s70, s56, 0x40000
	v_lshl_add_u64 v[208:209], s[56:57], 0, v[134:135]
	s_addc_u32 s71, s57, 0
	s_add_i32 s69, s72, s0
	global_load_lds_dwordx4 v[208:209], off
	v_lshl_add_u64 v[210:211], s[70:71], 0, v[128:129]
	s_mov_b32 m0, s69
	v_lshl_add_u64 v[214:215], s[58:59], 0, v[132:133]
	global_load_lds_dwordx4 v[210:211], off
	v_lshl_add_u64 v[210:211], s[70:71], 0, v[134:135]
	s_add_i32 m0, s69, 0x2000
	s_nop 0
	global_load_lds_dwordx4 v[210:211], off
	v_lshl_add_u64 v[210:211], s[58:59], 0, v[130:131]
	s_mov_b32 m0, s1
	s_nop 0
	global_load_lds_dwordx4 v[210:211], off
	s_mov_b32 m0, s33
	s_nop 0
	global_load_lds_dwordx4 v[214:215], off
	s_waitcnt vmcnt(24)
	s_waitcnt lgkmcnt(0)
	s_barrier
	s_setprio 1
	s_waitcnt lgkmcnt(0)
	v_mfma_f32_16x16x32_bf16 v[60:63], v[142:145], v[182:185], v[60:63]
	v_mfma_f32_16x16x32_bf16 v[56:59], v[158:161], v[182:185], v[56:59]
	v_mfma_f32_16x16x32_bf16 v[44:47], v[142:145], v[190:193], v[44:47]
	v_mfma_f32_16x16x32_bf16 v[40:43], v[158:161], v[190:193], v[40:43]
	v_mfma_f32_16x16x32_bf16 v[28:31], v[142:145], v[200:203], v[28:31]
	v_mfma_f32_16x16x32_bf16 v[24:27], v[158:161], v[200:203], v[24:27]
	v_mfma_f32_16x16x32_bf16 v[12:15], v[142:145], v[216:219], v[12:15]
	v_mfma_f32_16x16x32_bf16 v[8:11], v[158:161], v[216:219], v[8:11]
	v_mfma_f32_16x16x32_bf16 v[60:63], v[154:157], v[186:189], v[60:63]
	v_mfma_f32_16x16x32_bf16 v[56:59], v[162:165], v[186:189], v[56:59]
	v_mfma_f32_16x16x32_bf16 v[44:47], v[154:157], v[194:197], v[44:47]
	v_mfma_f32_16x16x32_bf16 v[40:43], v[162:165], v[194:197], v[40:43]
	v_mfma_f32_16x16x32_bf16 v[28:31], v[154:157], v[204:207], v[28:31]
	v_mfma_f32_16x16x32_bf16 v[24:27], v[162:165], v[204:207], v[24:27]
	v_mfma_f32_16x16x32_bf16 v[12:15], v[154:157], v[220:223], v[12:15]
	v_mfma_f32_16x16x32_bf16 v[8:11], v[162:165], v[220:223], v[8:11]
	s_setprio 0
	s_setprio 1
	v_mfma_f32_16x16x32_bf16 v[52:55], v[166:169], v[182:185], v[52:55]
	v_mfma_f32_16x16x32_bf16 v[48:51], v[174:177], v[182:185], v[48:51]
	v_mfma_f32_16x16x32_bf16 v[36:39], v[166:169], v[190:193], v[36:39]
	v_mfma_f32_16x16x32_bf16 v[32:35], v[174:177], v[190:193], v[32:35]
	v_mfma_f32_16x16x32_bf16 v[20:23], v[166:169], v[200:203], v[20:23]
	v_mfma_f32_16x16x32_bf16 v[16:19], v[174:177], v[200:203], v[16:19]
	v_mfma_f32_16x16x32_bf16 v[4:7], v[166:169], v[216:219], v[4:7]
	v_mfma_f32_16x16x32_bf16 v[0:3], v[174:177], v[216:219], v[0:3]
	v_mfma_f32_16x16x32_bf16 v[52:55], v[170:173], v[186:189], v[52:55]
	v_mfma_f32_16x16x32_bf16 v[48:51], v[178:181], v[186:189], v[48:51]
	v_mfma_f32_16x16x32_bf16 v[36:39], v[170:173], v[194:197], v[36:39]
	v_mfma_f32_16x16x32_bf16 v[32:35], v[178:181], v[194:197], v[32:35]
	v_mfma_f32_16x16x32_bf16 v[20:23], v[170:173], v[204:207], v[20:23]
	v_mfma_f32_16x16x32_bf16 v[16:19], v[178:181], v[204:207], v[16:19]
	v_mfma_f32_16x16x32_bf16 v[4:7], v[170:173], v[220:223], v[4:7]
	v_mfma_f32_16x16x32_bf16 v[0:3], v[178:181], v[220:223], v[0:3]
	s_setprio 0
	s_barrier
	s_add_i32 s69, 0, 0x18000
	s_add_i32 s70, 0, 0x1c000
	v_add_u32_e32 v162, s69, v149
	v_add_u32_e32 v178, s70, v149
	ds_read_b128 v[142:145], v162
	ds_read_b128 v[154:157], v162 offset:1024
	ds_read_b128 v[158:161], v162 offset:2048
	ds_read_b128 v[162:165], v162 offset:3072
	ds_read_b128 v[166:169], v178
	ds_read_b128 v[170:173], v178 offset:1024
	ds_read_b128 v[174:177], v178 offset:2048
	ds_read_b128 v[178:181], v178 offset:3072
	s_add_u32 s58, s58, 0x40000
	s_addc_u32 s59, s59, 0
	s_mov_b32 m0, s60
	v_lshl_add_u64 v[224:225], s[58:59], 0, v[130:131]
	ds_read_b128 v[182:185], v153 offset:32768
	ds_read_b128 v[186:189], v153 offset:33792
	ds_read_b128 v[190:193], v153 offset:34816
	ds_read_b128 v[194:197], v153 offset:35840
	ds_read_b128 v[200:203], v153 offset:36864
	ds_read_b128 v[204:207], v153 offset:37888
	ds_read_b128 v[216:219], v153 offset:38912
	ds_read_b128 v[220:223], v153 offset:39936
	global_load_lds_dwordx4 v[224:225], off
	v_lshl_add_u64 v[224:225], s[58:59], 0, v[132:133]
	s_mov_b32 m0, s61
	s_nop 0
	global_load_lds_dwordx4 v[224:225], off
	s_waitcnt vmcnt(24)
	s_waitcnt lgkmcnt(0)
	s_barrier
	s_setprio 1
	s_waitcnt lgkmcnt(0)
	v_mfma_f32_16x16x32_bf16 v[124:127], v[142:145], v[182:185], v[124:127]
	v_mfma_f32_16x16x32_bf16 v[120:123], v[158:161], v[182:185], v[120:123]
	v_mfma_f32_16x16x32_bf16 v[108:111], v[142:145], v[190:193], v[108:111]
	v_mfma_f32_16x16x32_bf16 v[104:107], v[158:161], v[190:193], v[104:107]
	v_mfma_f32_16x16x32_bf16 v[92:95], v[142:145], v[200:203], v[92:95]
	v_mfma_f32_16x16x32_bf16 v[88:91], v[158:161], v[200:203], v[88:91]
	v_mfma_f32_16x16x32_bf16 v[76:79], v[142:145], v[216:219], v[76:79]
	v_mfma_f32_16x16x32_bf16 v[72:75], v[158:161], v[216:219], v[72:75]
	v_mfma_f32_16x16x32_bf16 v[124:127], v[154:157], v[186:189], v[124:127]
	v_mfma_f32_16x16x32_bf16 v[120:123], v[162:165], v[186:189], v[120:123]
	v_mfma_f32_16x16x32_bf16 v[108:111], v[154:157], v[194:197], v[108:111]
	v_mfma_f32_16x16x32_bf16 v[104:107], v[162:165], v[194:197], v[104:107]
	v_mfma_f32_16x16x32_bf16 v[92:95], v[154:157], v[204:207], v[92:95]
	v_mfma_f32_16x16x32_bf16 v[88:91], v[162:165], v[204:207], v[88:91]
	v_mfma_f32_16x16x32_bf16 v[76:79], v[154:157], v[220:223], v[76:79]
	v_mfma_f32_16x16x32_bf16 v[72:75], v[162:165], v[220:223], v[72:75]
	s_setprio 0
	s_setprio 1
	v_mfma_f32_16x16x32_bf16 v[116:119], v[166:169], v[182:185], v[116:119]
	v_mfma_f32_16x16x32_bf16 v[112:115], v[174:177], v[182:185], v[112:115]
	v_mfma_f32_16x16x32_bf16 v[100:103], v[166:169], v[190:193], v[100:103]
	v_mfma_f32_16x16x32_bf16 v[96:99], v[174:177], v[190:193], v[96:99]
	v_mfma_f32_16x16x32_bf16 v[84:87], v[166:169], v[200:203], v[84:87]
	v_mfma_f32_16x16x32_bf16 v[80:83], v[174:177], v[200:203], v[80:83]
	v_mfma_f32_16x16x32_bf16 v[68:71], v[166:169], v[216:219], v[68:71]
	v_mfma_f32_16x16x32_bf16 v[64:67], v[174:177], v[216:219], v[64:67]
	v_mfma_f32_16x16x32_bf16 v[116:119], v[170:173], v[186:189], v[116:119]
	v_mfma_f32_16x16x32_bf16 v[112:115], v[178:181], v[186:189], v[112:115]
	v_mfma_f32_16x16x32_bf16 v[100:103], v[170:173], v[194:197], v[100:103]
	v_mfma_f32_16x16x32_bf16 v[96:99], v[178:181], v[194:197], v[96:99]
	v_mfma_f32_16x16x32_bf16 v[84:87], v[170:173], v[204:207], v[84:87]
	v_mfma_f32_16x16x32_bf16 v[80:83], v[178:181], v[204:207], v[80:83]
	v_mfma_f32_16x16x32_bf16 v[68:71], v[170:173], v[220:223], v[68:71]
	v_mfma_f32_16x16x32_bf16 v[64:67], v[178:181], v[220:223], v[64:67]
	s_setprio 0
	s_barrier
	s_branch .Lmlp1_q3
.LBB0_1689:
	s_add_u32 s56, s54, 0xfffc0080
	s_addc_u32 s57, s55, -1
	s_add_i32 s69, 0, 0x10000
	s_cmp_eq_u32 s68, 12
	s_cselect_b32 s59, s45, s57
	s_cselect_b32 s58, s53, s56
	v_add_u32_e32 v146, s69, v149
	s_cselect_b32 s57, s47, s67
	s_cselect_b32 s56, s65, s66
	s_add_i32 s72, 0, 0x14000
	ds_read_b128 v[142:145], v146
	ds_read_b128 v[154:157], v146 offset:1024
	ds_read_b128 v[158:161], v146 offset:2048
	ds_read_b128 v[162:165], v146 offset:3072
	v_add_u32_e32 v146, s72, v149
	ds_read_b128 v[166:169], v146
	ds_read_b128 v[170:173], v146 offset:1024
	ds_read_b128 v[174:177], v146 offset:2048
	ds_read_b128 v[178:181], v146 offset:3072
	v_lshl_add_u64 v[146:147], s[54:55], 0, v[138:139]
	s_add_i32 m0, s1, 0xc000
	ds_read_b128 v[182:185], v153
	ds_read_b128 v[186:189], v153 offset:1024
	ds_read_b128 v[190:193], v153 offset:2048
	ds_read_b128 v[194:197], v153 offset:3072
	ds_read_b128 v[200:203], v153 offset:4096
	ds_read_b128 v[204:207], v153 offset:5120
	ds_read_b128 v[216:219], v153 offset:6144
	ds_read_b128 v[220:223], v153 offset:7168
	global_load_lds_dwordx4 v[146:147], off
	v_lshl_add_u64 v[146:147], s[54:55], 0, v[140:141]
	s_add_i32 m0, s1, 0xe000
	s_nop 0
	global_load_lds_dwordx4 v[146:147], off
	s_waitcnt vmcnt(8)
	s_waitcnt lgkmcnt(0)
	s_barrier
	s_setprio 1
	s_waitcnt lgkmcnt(0)
	v_mfma_f32_16x16x32_bf16 v[124:127], v[142:145], v[182:185], v[124:127]
	v_mfma_f32_16x16x32_bf16 v[120:123], v[158:161], v[182:185], v[120:123]
	v_mfma_f32_16x16x32_bf16 v[108:111], v[142:145], v[190:193], v[108:111]
	v_mfma_f32_16x16x32_bf16 v[104:107], v[158:161], v[190:193], v[104:107]
	v_mfma_f32_16x16x32_bf16 v[92:95], v[142:145], v[200:203], v[92:95]
	v_mfma_f32_16x16x32_bf16 v[88:91], v[158:161], v[200:203], v[88:91]
	v_mfma_f32_16x16x32_bf16 v[76:79], v[142:145], v[216:219], v[76:79]
	v_mfma_f32_16x16x32_bf16 v[72:75], v[158:161], v[216:219], v[72:75]
	v_mfma_f32_16x16x32_bf16 v[124:127], v[154:157], v[186:189], v[124:127]
	v_mfma_f32_16x16x32_bf16 v[120:123], v[162:165], v[186:189], v[120:123]
	v_mfma_f32_16x16x32_bf16 v[108:111], v[154:157], v[194:197], v[108:111]
	v_mfma_f32_16x16x32_bf16 v[104:107], v[162:165], v[194:197], v[104:107]
	v_mfma_f32_16x16x32_bf16 v[92:95], v[154:157], v[204:207], v[92:95]
	v_mfma_f32_16x16x32_bf16 v[88:91], v[162:165], v[204:207], v[88:91]
	v_mfma_f32_16x16x32_bf16 v[76:79], v[154:157], v[220:223], v[76:79]
	v_mfma_f32_16x16x32_bf16 v[72:75], v[162:165], v[220:223], v[72:75]
	s_setprio 0
	s_setprio 1
	v_mfma_f32_16x16x32_bf16 v[116:119], v[166:169], v[182:185], v[116:119]
	v_mfma_f32_16x16x32_bf16 v[112:115], v[174:177], v[182:185], v[112:115]
	v_mfma_f32_16x16x32_bf16 v[100:103], v[166:169], v[190:193], v[100:103]
	v_mfma_f32_16x16x32_bf16 v[96:99], v[174:177], v[190:193], v[96:99]
	v_mfma_f32_16x16x32_bf16 v[84:87], v[166:169], v[200:203], v[84:87]
	v_mfma_f32_16x16x32_bf16 v[80:83], v[174:177], v[200:203], v[80:83]
	v_mfma_f32_16x16x32_bf16 v[68:71], v[166:169], v[216:219], v[68:71]
	v_mfma_f32_16x16x32_bf16 v[64:67], v[174:177], v[216:219], v[64:67]
	v_mfma_f32_16x16x32_bf16 v[116:119], v[170:173], v[186:189], v[116:119]
	v_mfma_f32_16x16x32_bf16 v[112:115], v[178:181], v[186:189], v[112:115]
	v_mfma_f32_16x16x32_bf16 v[100:103], v[170:173], v[194:197], v[100:103]
	v_mfma_f32_16x16x32_bf16 v[96:99], v[178:181], v[194:197], v[96:99]
	v_mfma_f32_16x16x32_bf16 v[84:87], v[170:173], v[204:207], v[84:87]
	v_mfma_f32_16x16x32_bf16 v[80:83], v[178:181], v[204:207], v[80:83]
	v_mfma_f32_16x16x32_bf16 v[68:71], v[170:173], v[220:223], v[68:71]
	v_mfma_f32_16x16x32_bf16 v[64:67], v[178:181], v[220:223], v[64:67]
	s_setprio 0
	s_barrier
	s_add_i32 s69, s69, s0
	v_lshl_add_u64 v[146:147], s[56:57], 0, v[128:129]
	s_mov_b32 m0, s69
	ds_read_b128 v[182:185], v153 offset:16384
	ds_read_b128 v[186:189], v153 offset:17408
	ds_read_b128 v[190:193], v153 offset:18432
	ds_read_b128 v[194:197], v153 offset:19456
	ds_read_b128 v[200:203], v153 offset:20480
	ds_read_b128 v[204:207], v153 offset:21504
	ds_read_b128 v[216:219], v153 offset:22528
	ds_read_b128 v[220:223], v153 offset:23552
	global_load_lds_dwordx4 v[146:147], off
	s_add_i32 m0, s69, 0x2000
	s_add_u32 s70, s56, 0x40000
	v_lshl_add_u64 v[208:209], s[56:57], 0, v[134:135]
	s_addc_u32 s71, s57, 0
	s_add_i32 s69, s72, s0
	global_load_lds_dwordx4 v[208:209], off
	v_lshl_add_u64 v[210:211], s[70:71], 0, v[128:129]
	s_mov_b32 m0, s69
	v_lshl_add_u64 v[214:215], s[58:59], 0, v[132:133]
	global_load_lds_dwordx4 v[210:211], off
	v_lshl_add_u64 v[210:211], s[70:71], 0, v[134:135]
	s_add_i32 m0, s69, 0x2000
	s_nop 0
	global_load_lds_dwordx4 v[210:211], off
	v_lshl_add_u64 v[210:211], s[58:59], 0, v[130:131]
	s_mov_b32 m0, s1
	s_nop 0
	global_load_lds_dwordx4 v[210:211], off
	s_mov_b32 m0, s33
	s_nop 0
	global_load_lds_dwordx4 v[214:215], off
	s_waitcnt vmcnt(8)
	s_waitcnt lgkmcnt(0)
	s_barrier
	s_setprio 1
	s_waitcnt lgkmcnt(0)
	v_mfma_f32_16x16x32_bf16 v[60:63], v[142:145], v[182:185], v[60:63]
	v_mfma_f32_16x16x32_bf16 v[56:59], v[158:161], v[182:185], v[56:59]
	v_mfma_f32_16x16x32_bf16 v[44:47], v[142:145], v[190:193], v[44:47]
	v_mfma_f32_16x16x32_bf16 v[40:43], v[158:161], v[190:193], v[40:43]
	v_mfma_f32_16x16x32_bf16 v[28:31], v[142:145], v[200:203], v[28:31]
	v_mfma_f32_16x16x32_bf16 v[24:27], v[158:161], v[200:203], v[24:27]
	v_mfma_f32_16x16x32_bf16 v[12:15], v[142:145], v[216:219], v[12:15]
	v_mfma_f32_16x16x32_bf16 v[8:11], v[158:161], v[216:219], v[8:11]
	v_mfma_f32_16x16x32_bf16 v[60:63], v[154:157], v[186:189], v[60:63]
	v_mfma_f32_16x16x32_bf16 v[56:59], v[162:165], v[186:189], v[56:59]
	v_mfma_f32_16x16x32_bf16 v[44:47], v[154:157], v[194:197], v[44:47]
	v_mfma_f32_16x16x32_bf16 v[40:43], v[162:165], v[194:197], v[40:43]
	v_mfma_f32_16x16x32_bf16 v[28:31], v[154:157], v[204:207], v[28:31]
	v_mfma_f32_16x16x32_bf16 v[24:27], v[162:165], v[204:207], v[24:27]
	v_mfma_f32_16x16x32_bf16 v[12:15], v[154:157], v[220:223], v[12:15]
	v_mfma_f32_16x16x32_bf16 v[8:11], v[162:165], v[220:223], v[8:11]
	s_setprio 0
	s_setprio 1
	v_mfma_f32_16x16x32_bf16 v[52:55], v[166:169], v[182:185], v[52:55]
	v_mfma_f32_16x16x32_bf16 v[48:51], v[174:177], v[182:185], v[48:51]
	v_mfma_f32_16x16x32_bf16 v[36:39], v[166:169], v[190:193], v[36:39]
	v_mfma_f32_16x16x32_bf16 v[32:35], v[174:177], v[190:193], v[32:35]
	v_mfma_f32_16x16x32_bf16 v[20:23], v[166:169], v[200:203], v[20:23]
	v_mfma_f32_16x16x32_bf16 v[16:19], v[174:177], v[200:203], v[16:19]
	v_mfma_f32_16x16x32_bf16 v[4:7], v[166:169], v[216:219], v[4:7]
	v_mfma_f32_16x16x32_bf16 v[0:3], v[174:177], v[216:219], v[0:3]
	v_mfma_f32_16x16x32_bf16 v[52:55], v[170:173], v[186:189], v[52:55]
	v_mfma_f32_16x16x32_bf16 v[48:51], v[178:181], v[186:189], v[48:51]
	v_mfma_f32_16x16x32_bf16 v[36:39], v[170:173], v[194:197], v[36:39]
	v_mfma_f32_16x16x32_bf16 v[32:35], v[178:181], v[194:197], v[32:35]
	v_mfma_f32_16x16x32_bf16 v[20:23], v[170:173], v[204:207], v[20:23]
	v_mfma_f32_16x16x32_bf16 v[16:19], v[178:181], v[204:207], v[16:19]
	v_mfma_f32_16x16x32_bf16 v[4:7], v[170:173], v[220:223], v[4:7]
	v_mfma_f32_16x16x32_bf16 v[0:3], v[178:181], v[220:223], v[0:3]
	s_setprio 0
	s_barrier
	s_add_i32 s69, 0, 0x18000
	s_add_i32 s70, 0, 0x1c000
	v_add_u32_e32 v162, s69, v149
	v_add_u32_e32 v178, s70, v149
	ds_read_b128 v[142:145], v162
	ds_read_b128 v[154:157], v162 offset:1024
	ds_read_b128 v[158:161], v162 offset:2048
	ds_read_b128 v[162:165], v162 offset:3072
	ds_read_b128 v[166:169], v178
	ds_read_b128 v[170:173], v178 offset:1024
	ds_read_b128 v[174:177], v178 offset:2048
	ds_read_b128 v[178:181], v178 offset:3072
	s_add_u32 s58, s58, 0x40000
	s_addc_u32 s59, s59, 0
	s_mov_b32 m0, s60
	v_lshl_add_u64 v[224:225], s[58:59], 0, v[130:131]
	ds_read_b128 v[182:185], v153 offset:32768
	ds_read_b128 v[186:189], v153 offset:33792
	ds_read_b128 v[190:193], v153 offset:34816
	ds_read_b128 v[194:197], v153 offset:35840
	ds_read_b128 v[200:203], v153 offset:36864
	ds_read_b128 v[204:207], v153 offset:37888
	ds_read_b128 v[216:219], v153 offset:38912
	ds_read_b128 v[220:223], v153 offset:39936
	global_load_lds_dwordx4 v[224:225], off
	v_lshl_add_u64 v[224:225], s[58:59], 0, v[132:133]
	s_mov_b32 m0, s61
	s_nop 0
	global_load_lds_dwordx4 v[224:225], off
	s_waitcnt vmcnt(8)
	s_waitcnt lgkmcnt(0)
	s_barrier
	s_setprio 1
	s_waitcnt lgkmcnt(0)
	v_mfma_f32_16x16x32_bf16 v[124:127], v[142:145], v[182:185], v[124:127]
	v_mfma_f32_16x16x32_bf16 v[120:123], v[158:161], v[182:185], v[120:123]
	v_mfma_f32_16x16x32_bf16 v[108:111], v[142:145], v[190:193], v[108:111]
	v_mfma_f32_16x16x32_bf16 v[104:107], v[158:161], v[190:193], v[104:107]
	v_mfma_f32_16x16x32_bf16 v[92:95], v[142:145], v[200:203], v[92:95]
	v_mfma_f32_16x16x32_bf16 v[88:91], v[158:161], v[200:203], v[88:91]
	v_mfma_f32_16x16x32_bf16 v[76:79], v[142:145], v[216:219], v[76:79]
	v_mfma_f32_16x16x32_bf16 v[72:75], v[158:161], v[216:219], v[72:75]
	v_mfma_f32_16x16x32_bf16 v[124:127], v[154:157], v[186:189], v[124:127]
	v_mfma_f32_16x16x32_bf16 v[120:123], v[162:165], v[186:189], v[120:123]
	v_mfma_f32_16x16x32_bf16 v[108:111], v[154:157], v[194:197], v[108:111]
	v_mfma_f32_16x16x32_bf16 v[104:107], v[162:165], v[194:197], v[104:107]
	v_mfma_f32_16x16x32_bf16 v[92:95], v[154:157], v[204:207], v[92:95]
	v_mfma_f32_16x16x32_bf16 v[88:91], v[162:165], v[204:207], v[88:91]
	v_mfma_f32_16x16x32_bf16 v[76:79], v[154:157], v[220:223], v[76:79]
	v_mfma_f32_16x16x32_bf16 v[72:75], v[162:165], v[220:223], v[72:75]
	s_setprio 0
	s_setprio 1
	v_mfma_f32_16x16x32_bf16 v[116:119], v[166:169], v[182:185], v[116:119]
	v_mfma_f32_16x16x32_bf16 v[112:115], v[174:177], v[182:185], v[112:115]
	v_mfma_f32_16x16x32_bf16 v[100:103], v[166:169], v[190:193], v[100:103]
	v_mfma_f32_16x16x32_bf16 v[96:99], v[174:177], v[190:193], v[96:99]
	v_mfma_f32_16x16x32_bf16 v[84:87], v[166:169], v[200:203], v[84:87]
	v_mfma_f32_16x16x32_bf16 v[80:83], v[174:177], v[200:203], v[80:83]
	v_mfma_f32_16x16x32_bf16 v[68:71], v[166:169], v[216:219], v[68:71]
	v_mfma_f32_16x16x32_bf16 v[64:67], v[174:177], v[216:219], v[64:67]
	v_mfma_f32_16x16x32_bf16 v[116:119], v[170:173], v[186:189], v[116:119]
	v_mfma_f32_16x16x32_bf16 v[112:115], v[178:181], v[186:189], v[112:115]
	v_mfma_f32_16x16x32_bf16 v[100:103], v[170:173], v[194:197], v[100:103]
	v_mfma_f32_16x16x32_bf16 v[96:99], v[178:181], v[194:197], v[96:99]
	v_mfma_f32_16x16x32_bf16 v[84:87], v[170:173], v[204:207], v[84:87]
	v_mfma_f32_16x16x32_bf16 v[80:83], v[178:181], v[204:207], v[80:83]
	v_mfma_f32_16x16x32_bf16 v[68:71], v[170:173], v[220:223], v[68:71]
	v_mfma_f32_16x16x32_bf16 v[64:67], v[178:181], v[220:223], v[64:67]
	s_setprio 0
	s_barrier
.Lmlp1_q3:
	s_add_i32 s58, s69, s0
	v_lshl_add_u64 v[146:147], v[146:147], 0, s[88:89]
	s_mov_b32 m0, s58
	ds_read_b128 v[182:185], v153 offset:49152
	ds_read_b128 v[186:189], v153 offset:50176
	ds_read_b128 v[190:193], v153 offset:51200
	ds_read_b128 v[194:197], v153 offset:52224
	ds_read_b128 v[200:203], v153 offset:53248
	ds_read_b128 v[204:207], v153 offset:54272
	ds_read_b128 v[216:219], v153 offset:55296
	ds_read_b128 v[220:223], v153 offset:56320
	global_load_lds_dwordx4 v[146:147], off
	s_add_i32 m0, s58, 0x2000
	s_add_u32 s56, s56, 0x40080
	v_lshl_add_u64 v[146:147], v[208:209], 0, s[88:89]
	s_addc_u32 s57, s57, 0
	s_add_i32 s58, s70, s0
	global_load_lds_dwordx4 v[146:147], off
	v_lshl_add_u64 v[146:147], s[56:57], 0, v[128:129]
	s_mov_b32 m0, s58
	s_nop 0
	global_load_lds_dwordx4 v[146:147], off
	v_lshl_add_u64 v[146:147], s[56:57], 0, v[134:135]
	s_add_i32 m0, s58, 0x2000
	s_nop 0
	global_load_lds_dwordx4 v[146:147], off
	v_lshl_add_u64 v[146:147], v[210:211], 0, s[88:89]
	s_mov_b32 m0, s62
	s_nop 0
	global_load_lds_dwordx4 v[146:147], off
	v_lshl_add_u64 v[146:147], v[214:215], 0, s[88:89]
	s_mov_b32 m0, s63
	s_nop 0
	global_load_lds_dwordx4 v[146:147], off
	s_waitcnt vmcnt(8)
	s_waitcnt lgkmcnt(0)
	s_barrier
	s_setprio 1
	s_waitcnt lgkmcnt(0)
	v_mfma_f32_16x16x32_bf16 v[60:63], v[142:145], v[182:185], v[60:63]
	v_mfma_f32_16x16x32_bf16 v[56:59], v[158:161], v[182:185], v[56:59]
	v_mfma_f32_16x16x32_bf16 v[44:47], v[142:145], v[190:193], v[44:47]
	v_mfma_f32_16x16x32_bf16 v[40:43], v[158:161], v[190:193], v[40:43]
	v_mfma_f32_16x16x32_bf16 v[28:31], v[142:145], v[200:203], v[28:31]
	v_mfma_f32_16x16x32_bf16 v[24:27], v[158:161], v[200:203], v[24:27]
	v_mfma_f32_16x16x32_bf16 v[12:15], v[142:145], v[216:219], v[12:15]
	v_mfma_f32_16x16x32_bf16 v[8:11], v[158:161], v[216:219], v[8:11]
	v_mfma_f32_16x16x32_bf16 v[60:63], v[154:157], v[186:189], v[60:63]
	v_mfma_f32_16x16x32_bf16 v[56:59], v[162:165], v[186:189], v[56:59]
	v_mfma_f32_16x16x32_bf16 v[44:47], v[154:157], v[194:197], v[44:47]
	v_mfma_f32_16x16x32_bf16 v[40:43], v[162:165], v[194:197], v[40:43]
	v_mfma_f32_16x16x32_bf16 v[28:31], v[154:157], v[204:207], v[28:31]
	v_mfma_f32_16x16x32_bf16 v[24:27], v[162:165], v[204:207], v[24:27]
	v_mfma_f32_16x16x32_bf16 v[12:15], v[154:157], v[220:223], v[12:15]
	v_mfma_f32_16x16x32_bf16 v[8:11], v[162:165], v[220:223], v[8:11]
	s_setprio 0
	s_setprio 1
	v_mfma_f32_16x16x32_bf16 v[52:55], v[166:169], v[182:185], v[52:55]
	v_mfma_f32_16x16x32_bf16 v[48:51], v[174:177], v[182:185], v[48:51]
	v_mfma_f32_16x16x32_bf16 v[36:39], v[166:169], v[190:193], v[36:39]
	v_mfma_f32_16x16x32_bf16 v[32:35], v[174:177], v[190:193], v[32:35]
	v_mfma_f32_16x16x32_bf16 v[20:23], v[166:169], v[200:203], v[20:23]
	v_mfma_f32_16x16x32_bf16 v[16:19], v[174:177], v[200:203], v[16:19]
	v_mfma_f32_16x16x32_bf16 v[4:7], v[166:169], v[216:219], v[4:7]
	v_mfma_f32_16x16x32_bf16 v[0:3], v[174:177], v[216:219], v[0:3]
	v_mfma_f32_16x16x32_bf16 v[52:55], v[170:173], v[186:189], v[52:55]
	v_mfma_f32_16x16x32_bf16 v[48:51], v[178:181], v[186:189], v[48:51]
	v_mfma_f32_16x16x32_bf16 v[36:39], v[170:173], v[194:197], v[36:39]
	v_mfma_f32_16x16x32_bf16 v[32:35], v[178:181], v[194:197], v[32:35]
	v_mfma_f32_16x16x32_bf16 v[20:23], v[170:173], v[204:207], v[20:23]
	v_mfma_f32_16x16x32_bf16 v[16:19], v[178:181], v[204:207], v[16:19]
	v_mfma_f32_16x16x32_bf16 v[4:7], v[170:173], v[220:223], v[4:7]
	v_mfma_f32_16x16x32_bf16 v[0:3], v[178:181], v[220:223], v[0:3]
	s_setprio 0
	s_barrier
	s_add_i32 s68, s68, 2
	s_add_u32 s54, s54, 0x100
	s_addc_u32 s55, s55, 0
	s_add_u32 s66, s66, 0x100
	s_addc_u32 s67, s67, 0
	s_cmp_gt_u32 s68, 13
	s_cbranch_scc0 .LBB0_1689
	s_and_b64 vcc, exec, s[30:31]
	s_cbranch_vccz .LBB0_1692
	s_barrier
.LBB0_1692:
	s_add_u32 s100, s53, 0x40080
	s_addc_u32 s101, s45, 0
	v_lshl_add_u64 v[146:147], s[100:101], 0, v[138:139]
	s_add_i32 m0, s1, 0xc000
	s_nop 0
	global_load_lds_dwordx4 v[146:147], off
	v_lshl_add_u64 v[146:147], s[100:101], 0, v[140:141]
	s_add_i32 m0, s1, 0xe000
	s_nop 0
	global_load_lds_dwordx4 v[146:147], off
	s_lshl_b32 s9, s9, 12
	s_and_b32 s9, s9, 0x1000
	v_add_u32_e32 v154, s9, v151
	ds_read_b128 v[156:159], v154
	v_lshl_or_b32 v142, s8, 8, v152
	v_ashrrev_i32_e32 v143, 31, v142
	v_lshl_add_u64 v[144:145], v[142:143], 1, s[74:75]
	v_lshl_add_u32 v146, s52, 8, v148
	s_waitcnt lgkmcnt(0)
	v_mov_b32_e32 v142, v157
	v_mov_b32_e32 v143, v158
	v_mov_b32_e32 v157, v159
	v_pk_add_f32 v[142:143], v[142:143], v[156:157]
	v_ashrrev_i32_e32 v147, 31, v146
	v_add_f32_e32 v142, v142, v143
	v_fmamk_f32 v142, v142, 0x3a800000, v198
	v_mul_f32_e32 v143, 0x4b800000, v142
	v_cmp_gt_f32_e32 vcc, s19, v142
	s_mov_b32 s8, 0x100000
	s_mov_b64 s[72:73], s[24:25]
	v_cndmask_b32_e32 v142, v142, v143, vcc
	v_rsq_f32_e32 v155, v142
	v_lshlrev_b64 v[142:143], 13, v[146:147]
	v_lshl_add_u64 v[142:143], v[144:145], 0, v[142:143]
	v_mul_f32_e32 v147, 0x45800000, v155
	v_cndmask_b32_e32 v156, v155, v147, vcc
	v_pk_mul_f32 v[120:121], v[120:121], v[156:157] op_sel_hi:[1,0]
	v_pk_mul_f32 v[124:125], v[124:125], v[156:157] op_sel_hi:[1,0]
	v_pk_mul_f32 v[122:123], v[122:123], v[156:157] op_sel_hi:[1,0]
	v_max_f32_e32 v120, 0, v120
	v_pk_mul_f32 v[126:127], v[126:127], v[156:157] op_sel_hi:[1,0]
	v_mul_f32_e32 v147, v120, v120
	v_max_f32_e32 v120, 0, v125
	v_max_f32_e32 v121, 0, v121
	v_max_f32_e32 v122, 0, v122
	v_max_f32_e32 v124, 0, v124
	v_mul_f32_e32 v120, v120, v120
	v_mul_f32_e32 v125, v121, v121
	v_max_f32_e32 v121, 0, v126
	v_mul_f32_e32 v126, v122, v122
	v_max_f32_e32 v122, 0, v127
	v_max_f32_e32 v123, 0, v123
	v_pk_mul_f32 v[114:115], v[114:115], v[156:157] op_sel_hi:[1,0]
	v_pk_mul_f32 v[112:113], v[112:113], v[156:157] op_sel_hi:[1,0]
	v_mul_f32_e32 v124, v124, v124
	v_mul_f32_e32 v121, v121, v121
	v_mul_f32_e32 v122, v122, v122
	v_mul_f32_e32 v123, v123, v123
	v_cvt_pk_bf16_f32 v120, v124, v120
	v_pk_mul_f32 v[118:119], v[118:119], v[156:157] op_sel_hi:[1,0]
	v_pk_mul_f32 v[116:117], v[116:117], v[156:157] op_sel_hi:[1,0]
	v_max_f32_e32 v112, 0, v112
	v_max_f32_e32 v113, 0, v113
	v_max_f32_e32 v114, 0, v114
	v_cvt_pk_bf16_f32 v121, v121, v122
	v_cvt_pk_bf16_f32 v122, v147, v125
	v_cvt_pk_bf16_f32 v123, v126, v123
	global_store_dwordx4 v[142:143], v[120:123], off
	v_max_f32_e32 v116, 0, v116
	v_max_f32_e32 v115, 0, v115
	v_mul_f32_e32 v120, v112, v112
	v_max_f32_e32 v112, 0, v117
	v_mul_f32_e32 v117, v113, v113
	v_max_f32_e32 v113, 0, v118
	v_mul_f32_e32 v118, v114, v114
	v_max_f32_e32 v114, 0, v119
	v_mul_f32_e32 v116, v116, v116
	v_mul_f32_e32 v112, v112, v112
	v_mul_f32_e32 v113, v113, v113
	v_mul_f32_e32 v114, v114, v114
	v_mul_f32_e32 v115, v115, v115
	v_cvt_pk_bf16_f32 v112, v116, v112
	v_cvt_pk_bf16_f32 v113, v113, v114
	v_cvt_pk_bf16_f32 v114, v120, v117
	v_cvt_pk_bf16_f32 v115, v118, v115
	ds_read_b128 v[116:119], v154 offset:256
	global_store_dwordx4 v[142:143], v[112:115], off offset:256
	s_nop 1
	v_or_b32_e32 v112, 16, v146
	s_waitcnt lgkmcnt(0)
	v_mov_b32_e32 v114, v117
	v_mov_b32_e32 v115, v118
	v_mov_b32_e32 v117, v119
	v_pk_add_f32 v[114:115], v[114:115], v[116:117]
	s_nop 0
	v_add_f32_e32 v113, v114, v115
	v_fmamk_f32 v113, v113, 0x3a800000, v198
	v_mul_f32_e32 v114, 0x4b800000, v113
	v_cmp_gt_f32_e32 vcc, s19, v113
	s_nop 1
	v_cndmask_b32_e32 v113, v113, v114, vcc
	v_rsq_f32_e32 v114, v113
	v_ashrrev_i32_e32 v113, 31, v112
	v_lshlrev_b64 v[112:113], 13, v[112:113]
	v_lshl_add_u64 v[112:113], v[144:145], 0, v[112:113]
	v_mul_f32_e32 v115, 0x45800000, v114
	v_cndmask_b32_e32 v114, v114, v115, vcc
	v_pk_mul_f32 v[104:105], v[104:105], v[114:115] op_sel_hi:[1,0]
	v_pk_mul_f32 v[108:109], v[108:109], v[114:115] op_sel_hi:[1,0]
	v_pk_mul_f32 v[106:107], v[106:107], v[114:115] op_sel_hi:[1,0]
	v_max_f32_e32 v104, 0, v104
	v_pk_mul_f32 v[110:111], v[110:111], v[114:115] op_sel_hi:[1,0]
	v_mul_f32_e32 v115, v104, v104
	v_max_f32_e32 v104, 0, v109
	v_max_f32_e32 v105, 0, v105
	v_max_f32_e32 v106, 0, v106
	v_max_f32_e32 v108, 0, v108
	v_mul_f32_e32 v104, v104, v104
	v_mul_f32_e32 v109, v105, v105
	v_max_f32_e32 v105, 0, v110
	v_mul_f32_e32 v110, v106, v106
	v_max_f32_e32 v106, 0, v111
	v_max_f32_e32 v107, 0, v107
	v_pk_mul_f32 v[98:99], v[98:99], v[114:115] op_sel_hi:[1,0]
	v_pk_mul_f32 v[96:97], v[96:97], v[114:115] op_sel_hi:[1,0]
	v_mul_f32_e32 v108, v108, v108
	v_mul_f32_e32 v105, v105, v105
	v_mul_f32_e32 v106, v106, v106
	v_mul_f32_e32 v107, v107, v107
	v_cvt_pk_bf16_f32 v104, v108, v104
	v_pk_mul_f32 v[102:103], v[102:103], v[114:115] op_sel_hi:[1,0]
	v_pk_mul_f32 v[100:101], v[100:101], v[114:115] op_sel_hi:[1,0]
	v_max_f32_e32 v96, 0, v96
	v_max_f32_e32 v97, 0, v97
	v_max_f32_e32 v98, 0, v98
	v_cvt_pk_bf16_f32 v105, v105, v106
	v_cvt_pk_bf16_f32 v106, v115, v109
	v_cvt_pk_bf16_f32 v107, v110, v107
	global_store_dwordx4 v[112:113], v[104:107], off
	v_max_f32_e32 v100, 0, v100
	v_max_f32_e32 v99, 0, v99
	v_mul_f32_e32 v104, v96, v96
	v_max_f32_e32 v96, 0, v101
	v_mul_f32_e32 v101, v97, v97
	v_max_f32_e32 v97, 0, v102
	v_mul_f32_e32 v102, v98, v98
	v_max_f32_e32 v98, 0, v103
	v_mul_f32_e32 v100, v100, v100
	v_mul_f32_e32 v96, v96, v96
	v_mul_f32_e32 v97, v97, v97
	v_mul_f32_e32 v98, v98, v98
	v_mul_f32_e32 v99, v99, v99
	v_cvt_pk_bf16_f32 v96, v100, v96
	v_cvt_pk_bf16_f32 v97, v97, v98
	v_cvt_pk_bf16_f32 v98, v104, v101
	v_cvt_pk_bf16_f32 v99, v102, v99
	ds_read_b128 v[100:103], v154 offset:512
	global_store_dwordx4 v[112:113], v[96:99], off offset:256
	s_nop 1
	v_or_b32_e32 v96, 32, v146
	s_waitcnt lgkmcnt(0)
	v_mov_b32_e32 v98, v101
	v_mov_b32_e32 v99, v102
	v_mov_b32_e32 v101, v103
	v_pk_add_f32 v[98:99], v[98:99], v[100:101]
	s_nop 0
	v_add_f32_e32 v97, v98, v99
	v_fmamk_f32 v97, v97, 0x3a800000, v198
	v_mul_f32_e32 v98, 0x4b800000, v97
	v_cmp_gt_f32_e32 vcc, s19, v97
	s_nop 1
	v_cndmask_b32_e32 v97, v97, v98, vcc
	v_rsq_f32_e32 v98, v97
	v_ashrrev_i32_e32 v97, 31, v96
	v_lshlrev_b64 v[96:97], 13, v[96:97]
	v_lshl_add_u64 v[96:97], v[144:145], 0, v[96:97]
	v_mul_f32_e32 v99, 0x45800000, v98
	v_cndmask_b32_e32 v98, v98, v99, vcc
	v_pk_mul_f32 v[88:89], v[88:89], v[98:99] op_sel_hi:[1,0]
	v_pk_mul_f32 v[92:93], v[92:93], v[98:99] op_sel_hi:[1,0]
	v_pk_mul_f32 v[90:91], v[90:91], v[98:99] op_sel_hi:[1,0]
	v_max_f32_e32 v88, 0, v88
	v_pk_mul_f32 v[94:95], v[94:95], v[98:99] op_sel_hi:[1,0]
	v_mul_f32_e32 v99, v88, v88
	v_max_f32_e32 v88, 0, v93
	v_max_f32_e32 v89, 0, v89
	v_max_f32_e32 v90, 0, v90
	v_max_f32_e32 v92, 0, v92
	v_mul_f32_e32 v88, v88, v88
	v_mul_f32_e32 v93, v89, v89
	v_max_f32_e32 v89, 0, v94
	v_mul_f32_e32 v94, v90, v90
	v_max_f32_e32 v90, 0, v95
	v_max_f32_e32 v91, 0, v91
	v_pk_mul_f32 v[82:83], v[82:83], v[98:99] op_sel_hi:[1,0]
	v_pk_mul_f32 v[80:81], v[80:81], v[98:99] op_sel_hi:[1,0]
	v_mul_f32_e32 v92, v92, v92
	v_mul_f32_e32 v89, v89, v89
	v_mul_f32_e32 v90, v90, v90
	v_mul_f32_e32 v91, v91, v91
	v_cvt_pk_bf16_f32 v88, v92, v88
	v_pk_mul_f32 v[86:87], v[86:87], v[98:99] op_sel_hi:[1,0]
	v_pk_mul_f32 v[84:85], v[84:85], v[98:99] op_sel_hi:[1,0]
	v_max_f32_e32 v80, 0, v80
	v_max_f32_e32 v81, 0, v81
	v_max_f32_e32 v82, 0, v82
	v_cvt_pk_bf16_f32 v89, v89, v90
	v_cvt_pk_bf16_f32 v90, v99, v93
	v_cvt_pk_bf16_f32 v91, v94, v91
	global_store_dwordx4 v[96:97], v[88:91], off
	v_max_f32_e32 v84, 0, v84
	v_max_f32_e32 v83, 0, v83
	v_mul_f32_e32 v88, v80, v80
	v_max_f32_e32 v80, 0, v85
	v_mul_f32_e32 v85, v81, v81
	v_max_f32_e32 v81, 0, v86
	v_mul_f32_e32 v86, v82, v82
	v_max_f32_e32 v82, 0, v87
	v_mul_f32_e32 v84, v84, v84
	v_mul_f32_e32 v80, v80, v80
	v_mul_f32_e32 v81, v81, v81
	v_mul_f32_e32 v82, v82, v82
	v_mul_f32_e32 v83, v83, v83
	v_cvt_pk_bf16_f32 v80, v84, v80
	v_cvt_pk_bf16_f32 v81, v81, v82
	v_cvt_pk_bf16_f32 v82, v88, v85
	v_cvt_pk_bf16_f32 v83, v86, v83
	ds_read_b128 v[84:87], v154 offset:768
	global_store_dwordx4 v[96:97], v[80:83], off offset:256
	s_nop 1
	v_or_b32_e32 v80, 48, v146
	s_waitcnt lgkmcnt(0)
	v_mov_b32_e32 v82, v85
	v_mov_b32_e32 v83, v86
	v_mov_b32_e32 v85, v87
	v_pk_add_f32 v[82:83], v[82:83], v[84:85]
	s_nop 0
	v_add_f32_e32 v81, v82, v83
	v_fmamk_f32 v81, v81, 0x3a800000, v198
	v_mul_f32_e32 v82, 0x4b800000, v81
	v_cmp_gt_f32_e32 vcc, s19, v81
	s_nop 1
	v_cndmask_b32_e32 v81, v81, v82, vcc
	v_rsq_f32_e32 v82, v81
	v_ashrrev_i32_e32 v81, 31, v80
	v_lshlrev_b64 v[80:81], 13, v[80:81]
	v_lshl_add_u64 v[80:81], v[144:145], 0, v[80:81]
	v_mul_f32_e32 v83, 0x45800000, v82
	v_cndmask_b32_e32 v82, v82, v83, vcc
	v_pk_mul_f32 v[72:73], v[72:73], v[82:83] op_sel_hi:[1,0]
	v_pk_mul_f32 v[76:77], v[76:77], v[82:83] op_sel_hi:[1,0]
	v_pk_mul_f32 v[74:75], v[74:75], v[82:83] op_sel_hi:[1,0]
	v_max_f32_e32 v72, 0, v72
	v_pk_mul_f32 v[78:79], v[78:79], v[82:83] op_sel_hi:[1,0]
	v_mul_f32_e32 v83, v72, v72
	v_max_f32_e32 v72, 0, v77
	v_max_f32_e32 v73, 0, v73
	v_max_f32_e32 v74, 0, v74
	v_max_f32_e32 v76, 0, v76
	v_mul_f32_e32 v72, v72, v72
	v_mul_f32_e32 v77, v73, v73
	v_max_f32_e32 v73, 0, v78
	v_mul_f32_e32 v78, v74, v74
	v_max_f32_e32 v74, 0, v79
	v_max_f32_e32 v75, 0, v75
	v_pk_mul_f32 v[66:67], v[66:67], v[82:83] op_sel_hi:[1,0]
	v_pk_mul_f32 v[64:65], v[64:65], v[82:83] op_sel_hi:[1,0]
	v_mul_f32_e32 v76, v76, v76
	v_mul_f32_e32 v73, v73, v73
	v_mul_f32_e32 v74, v74, v74
	v_mul_f32_e32 v75, v75, v75
	v_cvt_pk_bf16_f32 v72, v76, v72
	v_pk_mul_f32 v[70:71], v[70:71], v[82:83] op_sel_hi:[1,0]
	v_pk_mul_f32 v[68:69], v[68:69], v[82:83] op_sel_hi:[1,0]
	v_max_f32_e32 v64, 0, v64
	v_max_f32_e32 v65, 0, v65
	v_max_f32_e32 v66, 0, v66
	v_cvt_pk_bf16_f32 v73, v73, v74
	v_cvt_pk_bf16_f32 v74, v83, v77
	v_cvt_pk_bf16_f32 v75, v78, v75
	global_store_dwordx4 v[80:81], v[72:75], off
	v_max_f32_e32 v68, 0, v68
	v_max_f32_e32 v67, 0, v67
	v_mul_f32_e32 v72, v64, v64
	v_max_f32_e32 v64, 0, v69
	v_mul_f32_e32 v69, v65, v65
	v_max_f32_e32 v65, 0, v70
	v_mul_f32_e32 v70, v66, v66
	v_max_f32_e32 v66, 0, v71
	v_mul_f32_e32 v68, v68, v68
	v_mul_f32_e32 v64, v64, v64
	v_mul_f32_e32 v65, v65, v65
	v_mul_f32_e32 v66, v66, v66
	v_mul_f32_e32 v67, v67, v67
	v_cvt_pk_bf16_f32 v64, v68, v64
	v_cvt_pk_bf16_f32 v65, v65, v66
	v_cvt_pk_bf16_f32 v66, v72, v69
	v_cvt_pk_bf16_f32 v67, v70, v67
	ds_read_b128 v[68:71], v154 offset:2048
	global_store_dwordx4 v[80:81], v[64:67], off offset:256
	s_waitcnt lgkmcnt(0)
	v_mov_b32_e32 v72, v69
	v_mov_b32_e32 v73, v70
	v_mov_b32_e32 v69, v71
	v_pk_add_f32 v[68:69], v[72:73], v[68:69]
	s_nop 0
	v_add_f32_e32 v68, v68, v69
	v_fmamk_f32 v68, v68, 0x3a800000, v198
	v_mul_f32_e32 v69, 0x4b800000, v68
	v_cmp_gt_f32_e32 vcc, s19, v68
	s_nop 1
	v_cndmask_b32_e32 v68, v68, v69, vcc
	v_rsq_f32_e32 v68, v68
	s_nop 0
	v_mul_f32_e32 v64, 0x45800000, v68
	v_cndmask_b32_e32 v64, v68, v64, vcc
	v_pk_mul_f32 v[56:57], v[56:57], v[64:65] op_sel_hi:[1,0]
	v_pk_mul_f32 v[60:61], v[60:61], v[64:65] op_sel_hi:[1,0]
	v_pk_mul_f32 v[58:59], v[58:59], v[64:65] op_sel_hi:[1,0]
	v_max_f32_e32 v56, 0, v56
	v_pk_mul_f32 v[62:63], v[62:63], v[64:65] op_sel_hi:[1,0]
	v_max_f32_e32 v60, 0, v60
	v_mul_f32_e32 v65, v56, v56
	v_max_f32_e32 v56, 0, v61
	v_max_f32_e32 v57, 0, v57
	v_max_f32_e32 v58, 0, v58
	v_mul_f32_e32 v60, v60, v60
	v_mul_f32_e32 v56, v56, v56
	v_mul_f32_e32 v61, v57, v57
	v_max_f32_e32 v57, 0, v62
	v_mul_f32_e32 v62, v58, v58
	v_max_f32_e32 v58, 0, v63
	v_mul_f32_e32 v57, v57, v57
	v_max_f32_e32 v59, 0, v59
	v_mul_f32_e32 v58, v58, v58
	v_cvt_pk_bf16_f32 v56, v60, v56
	v_add_co_u32_e32 v60, vcc, s8, v142
	v_pk_mul_f32 v[50:51], v[50:51], v[64:65] op_sel_hi:[1,0]
	v_pk_mul_f32 v[48:49], v[48:49], v[64:65] op_sel_hi:[1,0]
	v_mul_f32_e32 v59, v59, v59
	v_cvt_pk_bf16_f32 v57, v57, v58
	v_cvt_pk_bf16_f32 v58, v65, v61
	v_addc_co_u32_e32 v61, vcc, 0, v143, vcc
	v_pk_mul_f32 v[54:55], v[54:55], v[64:65] op_sel_hi:[1,0]
	v_pk_mul_f32 v[52:53], v[52:53], v[64:65] op_sel_hi:[1,0]
	v_max_f32_e32 v48, 0, v48
	v_max_f32_e32 v49, 0, v49
	v_max_f32_e32 v50, 0, v50
	v_cvt_pk_bf16_f32 v59, v62, v59
	global_store_dwordx4 v[60:61], v[56:59], off
	v_max_f32_e32 v52, 0, v52
	v_max_f32_e32 v51, 0, v51
	v_mul_f32_e32 v56, v48, v48
	v_max_f32_e32 v48, 0, v53
	v_mul_f32_e32 v53, v49, v49
	v_max_f32_e32 v49, 0, v54
	v_mul_f32_e32 v54, v50, v50
	v_max_f32_e32 v50, 0, v55
	v_mul_f32_e32 v52, v52, v52
	v_mul_f32_e32 v48, v48, v48
	v_mul_f32_e32 v49, v49, v49
	v_mul_f32_e32 v50, v50, v50
	v_mul_f32_e32 v51, v51, v51
	v_cvt_pk_bf16_f32 v48, v52, v48
	v_cvt_pk_bf16_f32 v49, v49, v50
	v_cvt_pk_bf16_f32 v50, v56, v53
	v_cvt_pk_bf16_f32 v51, v54, v51
	ds_read_b128 v[52:55], v154 offset:2304
	s_mov_b64 s[8:9], 0x100000
	s_waitcnt lgkmcnt(0)
	v_mov_b32_e32 v56, v53
	v_mov_b32_e32 v57, v54
	v_mov_b32_e32 v53, v55
	v_pk_add_f32 v[52:53], v[56:57], v[52:53]
	s_nop 0
	v_add_f32_e32 v52, v52, v53
	v_fmamk_f32 v52, v52, 0x3a800000, v198
	v_mul_f32_e32 v53, 0x4b800000, v52
	v_cmp_gt_f32_e32 vcc, s19, v52
	s_nop 1
	v_cndmask_b32_e32 v52, v52, v53, vcc
	v_rsq_f32_e32 v54, v52
	v_lshl_add_u64 v[52:53], v[142:143], 0, s[8:9]
	global_store_dwordx4 v[52:53], v[48:51], off offset:256
	s_mov_b32 s8, 0x120000
	s_nop 0
	v_mul_f32_e32 v48, 0x45800000, v54
	v_cndmask_b32_e32 v48, v54, v48, vcc
	v_pk_mul_f32 v[40:41], v[40:41], v[48:49] op_sel_hi:[1,0]
	v_pk_mul_f32 v[44:45], v[44:45], v[48:49] op_sel_hi:[1,0]
	v_pk_mul_f32 v[42:43], v[42:43], v[48:49] op_sel_hi:[1,0]
	v_max_f32_e32 v40, 0, v40
	v_pk_mul_f32 v[46:47], v[46:47], v[48:49] op_sel_hi:[1,0]
	v_max_f32_e32 v44, 0, v44
	v_mul_f32_e32 v49, v40, v40
	v_max_f32_e32 v40, 0, v45
	v_max_f32_e32 v41, 0, v41
	v_max_f32_e32 v42, 0, v42
	v_mul_f32_e32 v44, v44, v44
	v_mul_f32_e32 v40, v40, v40
	v_mul_f32_e32 v45, v41, v41
	v_max_f32_e32 v41, 0, v46
	v_mul_f32_e32 v46, v42, v42
	v_max_f32_e32 v42, 0, v47
	v_mul_f32_e32 v41, v41, v41
	v_max_f32_e32 v43, 0, v43
	v_mul_f32_e32 v42, v42, v42
	v_cvt_pk_bf16_f32 v40, v44, v40
	v_add_co_u32_e32 v44, vcc, s8, v142
	v_pk_mul_f32 v[34:35], v[34:35], v[48:49] op_sel_hi:[1,0]
	v_pk_mul_f32 v[32:33], v[32:33], v[48:49] op_sel_hi:[1,0]
	v_mul_f32_e32 v43, v43, v43
	v_cvt_pk_bf16_f32 v41, v41, v42
	v_cvt_pk_bf16_f32 v42, v49, v45
	v_addc_co_u32_e32 v45, vcc, 0, v143, vcc
	v_pk_mul_f32 v[38:39], v[38:39], v[48:49] op_sel_hi:[1,0]
	v_pk_mul_f32 v[36:37], v[36:37], v[48:49] op_sel_hi:[1,0]
	v_max_f32_e32 v32, 0, v32
	v_max_f32_e32 v33, 0, v33
	v_max_f32_e32 v34, 0, v34
	v_cvt_pk_bf16_f32 v43, v46, v43
	global_store_dwordx4 v[44:45], v[40:43], off
	v_max_f32_e32 v36, 0, v36
	v_max_f32_e32 v35, 0, v35
	v_mul_f32_e32 v40, v32, v32
	v_max_f32_e32 v32, 0, v37
	v_mul_f32_e32 v37, v33, v33
	v_max_f32_e32 v33, 0, v38
	v_mul_f32_e32 v38, v34, v34
	v_max_f32_e32 v34, 0, v39
	v_mul_f32_e32 v36, v36, v36
	v_mul_f32_e32 v32, v32, v32
	v_mul_f32_e32 v33, v33, v33
	v_mul_f32_e32 v34, v34, v34
	v_mul_f32_e32 v35, v35, v35
	v_cvt_pk_bf16_f32 v32, v36, v32
	v_cvt_pk_bf16_f32 v33, v33, v34
	v_cvt_pk_bf16_f32 v34, v40, v37
	v_cvt_pk_bf16_f32 v35, v38, v35
	ds_read_b128 v[36:39], v154 offset:2560
	s_mov_b64 s[8:9], 0x120000
	s_waitcnt lgkmcnt(0)
	v_mov_b32_e32 v40, v37
	v_mov_b32_e32 v41, v38
	v_mov_b32_e32 v37, v39
	v_pk_add_f32 v[36:37], v[40:41], v[36:37]
	s_nop 0
	v_add_f32_e32 v36, v36, v37
	v_fmamk_f32 v36, v36, 0x3a800000, v198
	v_mul_f32_e32 v37, 0x4b800000, v36
	v_cmp_gt_f32_e32 vcc, s19, v36
	s_nop 1
	v_cndmask_b32_e32 v36, v36, v37, vcc
	v_rsq_f32_e32 v38, v36
	v_lshl_add_u64 v[36:37], v[142:143], 0, s[8:9]
	global_store_dwordx4 v[36:37], v[32:35], off offset:256
	s_mov_b32 s8, 0x140000
	s_nop 0
	v_mul_f32_e32 v32, 0x45800000, v38
	v_cndmask_b32_e32 v32, v38, v32, vcc
	v_pk_mul_f32 v[24:25], v[24:25], v[32:33] op_sel_hi:[1,0]
	v_pk_mul_f32 v[28:29], v[28:29], v[32:33] op_sel_hi:[1,0]
	v_pk_mul_f32 v[26:27], v[26:27], v[32:33] op_sel_hi:[1,0]
	v_max_f32_e32 v24, 0, v24
	v_pk_mul_f32 v[30:31], v[30:31], v[32:33] op_sel_hi:[1,0]
	v_max_f32_e32 v28, 0, v28
	v_mul_f32_e32 v33, v24, v24
	v_max_f32_e32 v24, 0, v29
	v_max_f32_e32 v25, 0, v25
	v_max_f32_e32 v26, 0, v26
	v_mul_f32_e32 v28, v28, v28
	v_mul_f32_e32 v24, v24, v24
	v_mul_f32_e32 v29, v25, v25
	v_max_f32_e32 v25, 0, v30
	v_mul_f32_e32 v30, v26, v26
	v_max_f32_e32 v26, 0, v31
	v_mul_f32_e32 v25, v25, v25
	v_max_f32_e32 v27, 0, v27
	v_mul_f32_e32 v26, v26, v26
	v_cvt_pk_bf16_f32 v24, v28, v24
	v_add_co_u32_e32 v28, vcc, s8, v142
	v_pk_mul_f32 v[18:19], v[18:19], v[32:33] op_sel_hi:[1,0]
	v_pk_mul_f32 v[16:17], v[16:17], v[32:33] op_sel_hi:[1,0]
	v_mul_f32_e32 v27, v27, v27
	v_cvt_pk_bf16_f32 v25, v25, v26
	v_cvt_pk_bf16_f32 v26, v33, v29
	v_addc_co_u32_e32 v29, vcc, 0, v143, vcc
	v_pk_mul_f32 v[22:23], v[22:23], v[32:33] op_sel_hi:[1,0]
	v_pk_mul_f32 v[20:21], v[20:21], v[32:33] op_sel_hi:[1,0]
	v_max_f32_e32 v16, 0, v16
	v_max_f32_e32 v17, 0, v17
	v_max_f32_e32 v18, 0, v18
	v_cvt_pk_bf16_f32 v27, v30, v27
	global_store_dwordx4 v[28:29], v[24:27], off
	v_max_f32_e32 v20, 0, v20
	v_max_f32_e32 v19, 0, v19
	v_mul_f32_e32 v24, v16, v16
	v_max_f32_e32 v16, 0, v21
	v_mul_f32_e32 v21, v17, v17
	v_max_f32_e32 v17, 0, v22
	v_mul_f32_e32 v22, v18, v18
	v_max_f32_e32 v18, 0, v23
	v_mul_f32_e32 v20, v20, v20
	v_mul_f32_e32 v16, v16, v16
	v_mul_f32_e32 v17, v17, v17
	v_mul_f32_e32 v18, v18, v18
	v_mul_f32_e32 v19, v19, v19
	v_cvt_pk_bf16_f32 v16, v20, v16
	v_cvt_pk_bf16_f32 v17, v17, v18
	v_cvt_pk_bf16_f32 v18, v24, v21
	v_cvt_pk_bf16_f32 v19, v22, v19
	ds_read_b128 v[20:23], v154 offset:2816
	s_mov_b64 s[8:9], 0x140000
	s_waitcnt lgkmcnt(0)
	v_mov_b32_e32 v24, v21
	v_mov_b32_e32 v25, v22
	v_mov_b32_e32 v21, v23
	v_pk_add_f32 v[20:21], v[24:25], v[20:21]
	s_nop 0
	v_add_f32_e32 v20, v20, v21
	v_fmamk_f32 v20, v20, 0x3a800000, v198
	v_mul_f32_e32 v21, 0x4b800000, v20
	v_cmp_gt_f32_e32 vcc, s19, v20
	s_nop 1
	v_cndmask_b32_e32 v20, v20, v21, vcc
	v_rsq_f32_e32 v22, v20
	v_lshl_add_u64 v[20:21], v[142:143], 0, s[8:9]
	global_store_dwordx4 v[20:21], v[16:19], off offset:256
	s_mov_b64 s[8:9], 0x160000
	s_nop 0
	v_mul_f32_e32 v18, 0x45800000, v22
	v_cndmask_b32_e32 v18, v22, v18, vcc
	v_pk_mul_f32 v[8:9], v[8:9], v[18:19] op_sel_hi:[1,0]
	v_pk_mul_f32 v[12:13], v[12:13], v[18:19] op_sel_hi:[1,0]
	v_pk_mul_f32 v[10:11], v[10:11], v[18:19] op_sel_hi:[1,0]
	v_max_f32_e32 v8, 0, v8
	v_pk_mul_f32 v[14:15], v[14:15], v[18:19] op_sel_hi:[1,0]
	v_max_f32_e32 v12, 0, v12
	v_mul_f32_e32 v19, v8, v8
	v_max_f32_e32 v8, 0, v13
	v_max_f32_e32 v9, 0, v9
	v_max_f32_e32 v10, 0, v10
	v_lshl_add_u64 v[16:17], v[142:143], 0, s[8:9]
	v_mul_f32_e32 v12, v12, v12
	v_mul_f32_e32 v8, v8, v8
	v_mul_f32_e32 v13, v9, v9
	v_max_f32_e32 v9, 0, v14
	v_mul_f32_e32 v14, v10, v10
	v_max_f32_e32 v10, 0, v15
	s_mov_b32 s8, 0x160000
	v_mul_f32_e32 v9, v9, v9
	v_max_f32_e32 v11, 0, v11
	v_mul_f32_e32 v10, v10, v10
	v_cvt_pk_bf16_f32 v8, v12, v8
	v_add_co_u32_e32 v12, vcc, s8, v142
	v_pk_mul_f32 v[2:3], v[2:3], v[18:19] op_sel_hi:[1,0]
	v_pk_mul_f32 v[0:1], v[0:1], v[18:19] op_sel_hi:[1,0]
	v_mul_f32_e32 v11, v11, v11
	v_cvt_pk_bf16_f32 v9, v9, v10
	v_cvt_pk_bf16_f32 v10, v19, v13
	v_addc_co_u32_e32 v13, vcc, 0, v143, vcc
	v_pk_mul_f32 v[6:7], v[6:7], v[18:19] op_sel_hi:[1,0]
	v_pk_mul_f32 v[4:5], v[4:5], v[18:19] op_sel_hi:[1,0]
	v_max_f32_e32 v0, 0, v0
	v_max_f32_e32 v1, 0, v1
	v_max_f32_e32 v2, 0, v2
	v_cvt_pk_bf16_f32 v11, v14, v11
	global_store_dwordx4 v[12:13], v[8:11], off
	v_max_f32_e32 v3, 0, v3
	v_max_f32_e32 v4, 0, v4
	v_mul_f32_e32 v8, v0, v0
	v_max_f32_e32 v0, 0, v5
	v_mul_f32_e32 v5, v1, v1
	v_max_f32_e32 v1, 0, v6
	v_mul_f32_e32 v6, v2, v2
	v_max_f32_e32 v2, 0, v7
	v_mul_f32_e32 v0, v0, v0
	v_mul_f32_e32 v1, v1, v1
	v_mul_f32_e32 v2, v2, v2
	v_mul_f32_e32 v3, v3, v3
	s_andn2_b64 vcc, exec, s[42:43]
	s_mov_b64 s[42:43], -1
	v_mul_f32_e32 v4, v4, v4
	v_cvt_pk_bf16_f32 v0, v4, v0
	v_cvt_pk_bf16_f32 v1, v1, v2
	v_cvt_pk_bf16_f32 v2, v8, v5
	v_cvt_pk_bf16_f32 v3, v6, v3
	global_store_dwordx4 v[16:17], v[0:3], off offset:256
	s_cbranch_vccnz .LBB0_1677
	s_andn2_b64 vcc, exec, s[26:27]
	s_cbranch_vccnz .LBB0_1676
	s_barrier
	s_branch .LBB0_1676

	.amdhsa_kernel _Z3fwd4Args
		.amdhsa_group_segment_fixed_size 0
		.amdhsa_private_segment_fixed_size 0
		.amdhsa_kernarg_size 560
		.amdhsa_user_sgpr_count 2
		.amdhsa_user_sgpr_dispatch_ptr 0
		.amdhsa_user_sgpr_queue_ptr 0
		.amdhsa_user_sgpr_kernarg_segment_ptr 1
		.amdhsa_user_sgpr_dispatch_id 0
		.amdhsa_user_sgpr_kernarg_preload_length 0
		.amdhsa_user_sgpr_kernarg_preload_offset 0
		.amdhsa_user_sgpr_private_segment_size 0
		.amdhsa_uses_dynamic_stack 0
		.amdhsa_enable_private_segment 0
		.amdhsa_system_sgpr_workgroup_id_x 1
		.amdhsa_system_sgpr_workgroup_id_y 0
		.amdhsa_system_sgpr_workgroup_id_z 0
		.amdhsa_system_sgpr_workgroup_info 0
		.amdhsa_system_vgpr_workitem_id 0
		.amdhsa_next_free_vgpr 256
		.amdhsa_next_free_sgpr 102
		.amdhsa_accum_offset 256
		.amdhsa_reserve_vcc 1
		.amdhsa_float_round_mode_32 0
		.amdhsa_float_round_mode_16_64 0
		.amdhsa_float_denorm_mode_32 3
		.amdhsa_float_denorm_mode_16_64 3
		.amdhsa_dx10_clamp 1
		.amdhsa_ieee_mode 1
		.amdhsa_fp16_overflow 0
		.amdhsa_tg_split 0
		.amdhsa_exception_fp_ieee_invalid_op 0
		.amdhsa_exception_fp_denorm_src 0
		.amdhsa_exception_fp_ieee_div_zero 0
		.amdhsa_exception_fp_ieee_overflow 0
		.amdhsa_exception_fp_ieee_underflow 0
		.amdhsa_exception_fp_ieee_inexact 0
		.amdhsa_exception_int_div_zero 0
	.end_amdhsa_kernel

amdhsa.kernels:
  - .agpr_count:     0
    .args:
      - .offset:         0
        .size:           304
        .value_kind:     by_value
      - .offset:         304
        .size:           4
        .value_kind:     hidden_block_count_x
      - .offset:         308
        .size:           4
        .value_kind:     hidden_block_count_y
      - .offset:         312
        .size:           4
        .value_kind:     hidden_block_count_z
      - .offset:         316
        .size:           2
        .value_kind:     hidden_group_size_x
      - .offset:         318
        .size:           2
        .value_kind:     hidden_group_size_y
      - .offset:         320
        .size:           2
        .value_kind:     hidden_group_size_z
      - .offset:         322
        .size:           2
        .value_kind:     hidden_remainder_x
      - .offset:         324
        .size:           2
        .value_kind:     hidden_remainder_y
      - .offset:         326
        .size:           2
        .value_kind:     hidden_remainder_z
      - .offset:         344
        .size:           8
        .value_kind:     hidden_global_offset_x
      - .offset:         352
        .size:           8
        .value_kind:     hidden_global_offset_y
      - .offset:         360
        .size:           8
        .value_kind:     hidden_global_offset_z
      - .offset:         368
        .size:           2
        .value_kind:     hidden_grid_dims
      - .offset:         424
        .size:           4
        .value_kind:     hidden_dynamic_lds_size
    .group_segment_fixed_size: 0
    .kernarg_segment_align: 8
    .kernarg_segment_size: 560
    .language:       OpenCL C
    .language_version:
      - 2
      - 0
    .max_flat_workgroup_size: 512
    .name:           _Z3fwd4Args
    .private_segment_fixed_size: 0
    .sgpr_count:     108
    .sgpr_spill_count: 330
    .symbol:         _Z3fwd4Args.kd
    .uniform_work_group_size: 1
    .uses_dynamic_stack: false
    .vgpr_count:     256
    .vgpr_spill_count: 0
    .wavefront_size: 64
